# static s_setprio 1 for waves 0-3 for the whole kernel, per-segment GEMM priority flips deleted
# speedup vs baseline: 1.0061x; 1.0016x over previous
; #define LAS __attribute__((address_space(3)))
; __global__ void __launch_bounds__(NTHR, 2) fwd(Args args) {
;     ...
;     F.tid = threadIdx.x; F.lane = F.tid & 63; F.wave = __builtin_amdgcn_readfirstlane(F.tid >> 6);
;     F.G = gridDim.x; F.gw = blockIdx.x * NWAVES + F.wave; F.NGW = F.G * NWAVES;
;     volatile LAS unsigned* MISC = (volatile LAS unsigned*)(F.lds + MISC_OFF);
;     for (int u = F.tid; u < (LDS_BYTES - LDSCTL_OFF) / 4; u += NTHR) ((LAS unsigned*)(F.lds + LDSCTL_OFF))[u] = 0u;
;     __syncthreads();
;     if (F.tid < N_INPUTS) { const unsigned long long p = (unsigned long long)args.in[F.tid]; LAS unsigned* t = (LAS unsigned*)(F.lds + PTAB_OFF) + 2 * F.tid; t[0] = (unsigned)p; t[1] = (unsigned)(p >> 32); }
;     __syncthreads();
;     XcdBarrier bar; bar.bar = F.ctl + CW_BAR; bar.x = 0; bar.st = nullptr;
;     if (N_LAUNCHES == 1) bar = xcd_barrier_post(F.ctl + CW_BAR, MISC + 8);
;     const int lo = args.ph_lo, hi = args.ph_hi;
;     float* out = args.out;
;     if (IN(0)) { p0_ada(F, inptr(F, IN_C), inptr(F, IN_ADAW), inptr(F, IN_ADAB), (float*)(F.ws + WS_MOD)); __syncthreads(); conv_all<0>(F); }
.LBB0_13:
	s_or_b64 exec, exec, s[0:1]
	v_readlane_b32 s0, v255, 0
	v_readlane_b32 s1, v255, 1
	s_load_dwordx2 s[4:5], s[0:1], 0xc8
	s_lshr_b32 s1, s54, 6
	s_lshl_b32 s0, s2, 3
	s_lshl_b32 s49, s48, 3
	v_writelane_b32 v255, s1, 9
	s_cmp_ge_u32 s1, 4
	s_cbranch_scc1 .Lprio_static
	s_setprio 1
.Lprio_static:
	s_add_i32 s0, s1, s0
	v_writelane_b32 v255, s0, 10
	s_waitcnt lgkmcnt(0)
	s_cmp_lt_i32 s4, 1
	s_cselect_b64 s[0:1], -1, 0
	v_writelane_b32 v255, s4, 11
	s_cmp_gt_i32 s5, 0
	v_and_b32_e32 v194, 63, v0
	v_writelane_b32 v255, s5, 12
	s_cselect_b64 s[4:5], -1, 0
	s_and_b64 s[0:1], s[0:1], s[4:5]
	s_andn2_b64 vcc, exec, s[0:1]
	s_cbranch_vccnz .LBB0_45
	s_add_i32 s3, 0, 0x20208
	v_mov_b32_e32 v1, s3
	s_add_i32 s3, 0, 0x20218
	ds_read2_b64 v[2:5], v1 offset1:1
	v_mov_b32_e32 v1, s3
	ds_read_b64 v[6:7], v1
	v_lshlrev_b32_e32 v1, 3, v0
	s_mov_b64 s[8:9], 0x800
	s_waitcnt lgkmcnt(1)
	v_readfirstlane_b32 s6, v2
	v_readfirstlane_b32 s7, v3
	v_lshlrev_b32_e32 v2, 2, v0
	v_mov_b32_e32 v3, 0
	v_readfirstlane_b32 s3, v4
	v_readfirstlane_b32 s4, v5
	s_waitcnt lgkmcnt(0)
	v_readfirstlane_b32 s5, v6
	v_readfirstlane_b32 s14, v7
	v_lshl_add_u64 v[4:5], s[6:7], 0, v[2:3]
	s_mov_b64 s[6:7], 0
	s_movk_i32 s10, 0x3dff
	v_mov_b32_e32 v3, v0

; #define PG8_STAGE(bufoff, gbase, voff) do { _Pragma("unroll") for (int _i = 0; _i < 2; ++_i) \
;         __builtin_amdgcn_global_load_lds((const unsigned*)((const char*)(gbase) + (voff)[_i]), (LAS unsigned*)(lds + (bufoff) + ldsw + _i * 8192), 16, 0, 0); } while (0)
; #define PG8_LDA(dst, b, h) do { _Pragma("unroll") for (int m = 0; m < 4; ++m) dst[m] = PG8_LD32(lds + PG8_SA(b, h) + aoff + m * 2048); } while (0)
; #define PG8_LDB(dst, b, h) do { _Pragma("unroll") for (int n = 0; n < 2; ++n) dst[n] = PG8_LD32(lds + PG8_SB(b, h) + boff + n * 2048); } while (0)
; #define PG8_WAIT_V(n) asm volatile("s_waitcnt vmcnt(" #n ")" ::: "memory")
; #define PG8_WAIT_L(n) asm volatile("s_waitcnt lgkmcnt(" #n ")" ::: "memory")
; #define PG8_BAR __builtin_amdgcn_s_barrier()
; #define PG8_SCHED __builtin_amdgcn_sched_barrier(0)
; template <class Epi, class Sched, bool ALIGN_EPI, int DT>
; __device__ __forceinline__ void gemm_phase(LAS unsigned char* lds, const int KB, const Sched& S, const Epi& E) {
;     ...
;             const size_t k1 = (size_t)(t + 1) * kstep, k2 = last ? 0 : (size_t)(t + 2) * kstep, k3 = k2 + kstep;
;             const char* b2 = last ? nB : cB + (size_t)(t + 2) * kstep; const char* b3 = b2 + kstep;
;             PG8_LDB(B0, 0, 0); PG8_LDB(B1, 0, 1); PG8_SCHED; PG8_LDA(At, 0, 0); PG8_STA(PG8_SA(1, 1), false, 1, k1);
;             PG8_WAIT_V(8); PG8_WAIT_L(0); PG8_BAR; PG8_MMA(0, 0, At, B0); PG8_MMA(0, 1, At, B1); PG8_BAR; PG8_SCHED;
;             PG8_LDA(At, 0, 1); PG8_STAGE(PG8_SB(0, 0), b2, voffB); PG8_STAGE(PG8_SB(0, 1), b2 + hstep, voffB); PG8_STA(PG8_SA(0, 0), last, 0, k2);
;             PG8_WAIT_V(8); PG8_WAIT_L(0); PG8_BAR; PG8_MMA(1, 0, At, B0); PG8_MMA(1, 1, At, B1); PG8_BAR; PG8_SCHED;
;             PG8_LDB(B0, 1, 0); PG8_LDB(B1, 1, 1); PG8_SCHED; PG8_LDA(At, 1, 0); PG8_STA(PG8_SA(0, 1), last, 1, k2);
;             PG8_WAIT_V(8); PG8_WAIT_L(0); PG8_BAR; PG8_MMA(0, 0, At, B0); PG8_MMA(0, 1, At, B1); PG8_BAR; PG8_SCHED;
;             PG8_LDA(At, 1, 1); PG8_STAGE(PG8_SB(1, 0), b3, voffB); PG8_STAGE(PG8_SB(1, 1), b3 + hstep, voffB); PG8_STA(PG8_SA(1, 0), last, 0, k3);
;             PG8_WAIT_V(8); PG8_WAIT_L(0); PG8_BAR; PG8_MMA(1, 0, At, B0); PG8_MMA(1, 1, At, B1); PG8_BAR; PG8_SCHED;
;         }
.LBB0_193:
	ds_read_b128 v[152:155], v175
	ds_read_b128 v[156:159], v175 offset:1024
	ds_read_b128 v[160:163], v175 offset:2048
	ds_read_b128 v[164:167], v175 offset:3072
	ds_read_b128 v[168:171], v176
	ds_read_b128 v[182:185], v176 offset:1024
	ds_read_b128 v[186:189], v176 offset:2048
	ds_read_b128 v[190:193], v176 offset:3072
	s_add_u32 s38, s36, 0x100
	s_addc_u32 s39, s37, 0
	s_add_u32 s68, s25, s36
	s_addc_u32 s69, s66, s37
	s_cmp_eq_u32 s67, 12
	s_cselect_b64 s[42:43], -1, 0
	s_and_b64 s[40:41], s[42:43], exec
	s_cselect_b32 s70, 0, s38
	s_cselect_b32 s41, s0, s69
	s_cselect_b32 s40, s23, s68
	v_lshl_add_u64 v[228:229], v[148:149], 0, s[36:37]
	s_add_i32 m0, s45, 0xc000
	ds_read_b128 v[196:199], v177
	ds_read_b128 v[200:203], v177 offset:1024
	ds_read_b128 v[204:207], v177 offset:2048
	ds_read_b128 v[208:211], v177 offset:3072
	ds_read_b128 v[212:215], v177 offset:4096
	ds_read_b128 v[216:219], v177 offset:5120
	ds_read_b128 v[220:223], v177 offset:6144
	ds_read_b128 v[224:227], v177 offset:7168
	global_load_lds_dwordx4 v[228:229], off
	v_lshl_add_u64 v[228:229], v[150:151], 0, s[36:37]
	s_add_i32 m0, s45, 0xe000
	s_nop 0
	global_load_lds_dwordx4 v[228:229], off
	s_waitcnt vmcnt(8)
	s_waitcnt lgkmcnt(0)
	s_barrier
	s_waitcnt lgkmcnt(0)
	v_mfma_i32_16x16x64_i8 v[126:129], v[152:155], v[196:199], v[126:129]
	v_mfma_i32_16x16x64_i8 v[122:125], v[160:163], v[196:199], v[122:125]
	v_mfma_i32_16x16x64_i8 v[110:113], v[152:155], v[204:207], v[110:113]
	v_mfma_i32_16x16x64_i8 v[106:109], v[160:163], v[204:207], v[106:109]
	v_mfma_i32_16x16x64_i8 v[94:97], v[152:155], v[212:215], v[94:97]
	v_mfma_i32_16x16x64_i8 v[90:93], v[160:163], v[212:215], v[90:93]
	v_mfma_i32_16x16x64_i8 v[78:81], v[152:155], v[220:223], v[78:81]
	v_mfma_i32_16x16x64_i8 v[74:77], v[160:163], v[220:223], v[74:77]
	v_mfma_i32_16x16x64_i8 v[126:129], v[156:159], v[200:203], v[126:129]
	v_mfma_i32_16x16x64_i8 v[122:125], v[164:167], v[200:203], v[122:125]
	v_mfma_i32_16x16x64_i8 v[110:113], v[156:159], v[208:211], v[110:113]
	v_mfma_i32_16x16x64_i8 v[106:109], v[164:167], v[208:211], v[106:109]
	v_mfma_i32_16x16x64_i8 v[94:97], v[156:159], v[216:219], v[94:97]
	v_mfma_i32_16x16x64_i8 v[90:93], v[164:167], v[216:219], v[90:93]
	v_mfma_i32_16x16x64_i8 v[78:81], v[156:159], v[224:227], v[78:81]
	v_mfma_i32_16x16x64_i8 v[74:77], v[164:167], v[224:227], v[74:77]
	v_mfma_i32_16x16x64_i8 v[118:121], v[168:171], v[196:199], v[118:121]
	v_mfma_i32_16x16x64_i8 v[114:117], v[186:189], v[196:199], v[114:117]
	v_mfma_i32_16x16x64_i8 v[102:105], v[168:171], v[204:207], v[102:105]
	v_mfma_i32_16x16x64_i8 v[98:101], v[186:189], v[204:207], v[98:101]
	v_mfma_i32_16x16x64_i8 v[86:89], v[168:171], v[212:215], v[86:89]
	v_mfma_i32_16x16x64_i8 v[82:85], v[186:189], v[212:215], v[82:85]
	v_mfma_i32_16x16x64_i8 v[70:73], v[168:171], v[220:223], v[70:73]
	v_mfma_i32_16x16x64_i8 v[66:69], v[186:189], v[220:223], v[66:69]
	v_mfma_i32_16x16x64_i8 v[118:121], v[182:185], v[200:203], v[118:121]
	v_mfma_i32_16x16x64_i8 v[114:117], v[190:193], v[200:203], v[114:117]
	v_mfma_i32_16x16x64_i8 v[102:105], v[182:185], v[208:211], v[102:105]
	v_mfma_i32_16x16x64_i8 v[98:101], v[190:193], v[208:211], v[98:101]
	v_mfma_i32_16x16x64_i8 v[86:89], v[182:185], v[216:219], v[86:89]
	v_mfma_i32_16x16x64_i8 v[82:85], v[190:193], v[216:219], v[82:85]
	v_mfma_i32_16x16x64_i8 v[70:73], v[182:185], v[224:227], v[70:73]
	v_mfma_i32_16x16x64_i8 v[66:69], v[190:193], v[224:227], v[66:69]
	s_barrier
	s_add_i32 s36, s62, s5
	v_lshl_add_u64 v[228:229], s[40:41], 0, v[134:135]
	s_mov_b32 m0, s36
	ds_read_b128 v[196:199], v177 offset:16384
	ds_read_b128 v[200:203], v177 offset:17408
	ds_read_b128 v[204:207], v177 offset:18432
	ds_read_b128 v[208:211], v177 offset:19456
	ds_read_b128 v[212:215], v177 offset:20480
	ds_read_b128 v[216:219], v177 offset:21504
	ds_read_b128 v[220:223], v177 offset:22528
	ds_read_b128 v[224:227], v177 offset:23552
	global_load_lds_dwordx4 v[228:229], off
	s_add_i32 m0, s36, 0x2000
	s_add_u32 s36, s40, 0x40000
	v_lshl_add_u64 v[230:231], s[40:41], 0, v[132:133]
	s_addc_u32 s37, s41, 0
	s_add_i32 s68, s63, s5
	global_load_lds_dwordx4 v[230:231], off
	v_lshl_add_u64 v[232:233], s[36:37], 0, v[134:135]
	s_mov_b32 m0, s68
	s_nop 0
	global_load_lds_dwordx4 v[232:233], off
	v_lshl_add_u64 v[232:233], s[36:37], 0, v[132:133]
	s_add_i32 m0, s68, 0x2000
	s_and_b64 s[36:37], s[8:9], s[42:43]
	s_and_b64 s[36:37], s[36:37], exec
	s_cselect_b32 s36, s26, s34
	s_cselect_b32 s37, s27, s35
	s_add_u32 s36, s36, s70
	s_addc_u32 s37, s37, 0
	global_load_lds_dwordx4 v[232:233], off
	v_lshl_add_u64 v[232:233], s[36:37], 0, v[136:137]
	s_mov_b32 m0, s45
	v_lshl_add_u64 v[234:235], s[36:37], 0, v[138:139]
	global_load_lds_dwordx4 v[232:233], off
	s_mov_b32 m0, s46
	s_nop 0
	global_load_lds_dwordx4 v[234:235], off
	s_waitcnt vmcnt(8)
	s_waitcnt lgkmcnt(0)
	s_barrier
; #define PG8_STAGE(bufoff, gbase, voff) do { _Pragma("unroll") for (int _i = 0; _i < 2; ++_i) \
;         __builtin_amdgcn_global_load_lds((const unsigned*)((const char*)(gbase) + (voff)[_i]), (LAS unsigned*)(lds + (bufoff) + ldsw + _i * 8192), 16, 0, 0); } while (0)
; #define PG8_LDA(dst, b, h) do { _Pragma("unroll") for (int m = 0; m < 4; ++m) dst[m] = PG8_LD32(lds + PG8_SA(b, h) + aoff + m * 2048); } while (0)
; #define PG8_LDB(dst, b, h) do { _Pragma("unroll") for (int n = 0; n < 2; ++n) dst[n] = PG8_LD32(lds + PG8_SB(b, h) + boff + n * 2048); } while (0)
; #define PG8_WAIT_V(n) asm volatile("s_waitcnt vmcnt(" #n ")" ::: "memory")
; #define PG8_WAIT_L(n) asm volatile("s_waitcnt lgkmcnt(" #n ")" ::: "memory")
; #define PG8_BAR __builtin_amdgcn_s_barrier()
; #define PG8_SCHED __builtin_amdgcn_sched_barrier(0)
; template <class Epi, class Sched, bool ALIGN_EPI, int DT>
; __device__ __forceinline__ void gemm_phase(LAS unsigned char* lds, const int KB, const Sched& S, const Epi& E) {
;     ...
;             const size_t k1 = (size_t)(t + 1) * kstep, k2 = last ? 0 : (size_t)(t + 2) * kstep, k3 = k2 + kstep;
;             const char* b2 = last ? nB : cB + (size_t)(t + 2) * kstep; const char* b3 = b2 + kstep;
;             PG8_LDB(B0, 0, 0); PG8_LDB(B1, 0, 1); PG8_SCHED; PG8_LDA(At, 0, 0); PG8_STA(PG8_SA(1, 1), false, 1, k1);
;             PG8_WAIT_V(8); PG8_WAIT_L(0); PG8_BAR; PG8_MMA(0, 0, At, B0); PG8_MMA(0, 1, At, B1); PG8_BAR; PG8_SCHED;
;             PG8_LDA(At, 0, 1); PG8_STAGE(PG8_SB(0, 0), b2, voffB); PG8_STAGE(PG8_SB(0, 1), b2 + hstep, voffB); PG8_STA(PG8_SA(0, 0), last, 0, k2);
;             PG8_WAIT_V(8); PG8_WAIT_L(0); PG8_BAR; PG8_MMA(1, 0, At, B0); PG8_MMA(1, 1, At, B1); PG8_BAR; PG8_SCHED;
;             PG8_LDB(B0, 1, 0); PG8_LDB(B1, 1, 1); PG8_SCHED; PG8_LDA(At, 1, 0); PG8_STA(PG8_SA(0, 1), last, 1, k2);
;             PG8_WAIT_V(8); PG8_WAIT_L(0); PG8_BAR; PG8_MMA(0, 0, At, B0); PG8_MMA(0, 1, At, B1); PG8_BAR; PG8_SCHED;
;             PG8_LDA(At, 1, 1); PG8_STAGE(PG8_SB(1, 0), b3, voffB); PG8_STAGE(PG8_SB(1, 1), b3 + hstep, voffB); PG8_STA(PG8_SA(1, 0), last, 0, k3);
;             PG8_WAIT_V(8); PG8_WAIT_L(0); PG8_BAR; PG8_MMA(1, 0, At, B0); PG8_MMA(1, 1, At, B1); PG8_BAR; PG8_SCHED;
;         }
	s_waitcnt lgkmcnt(0)
	v_mfma_i32_16x16x64_i8 v[62:65], v[152:155], v[196:199], v[62:65]
	v_mfma_i32_16x16x64_i8 v[58:61], v[160:163], v[196:199], v[58:61]
	v_mfma_i32_16x16x64_i8 v[46:49], v[152:155], v[204:207], v[46:49]
	v_mfma_i32_16x16x64_i8 v[42:45], v[160:163], v[204:207], v[42:45]
	v_mfma_i32_16x16x64_i8 v[30:33], v[152:155], v[212:215], v[30:33]
	v_mfma_i32_16x16x64_i8 v[26:29], v[160:163], v[212:215], v[26:29]
	v_mfma_i32_16x16x64_i8 v[6:9], v[152:155], v[220:223], v[6:9]
	v_mfma_i32_16x16x64_i8 v[2:5], v[160:163], v[220:223], v[2:5]
	v_mfma_i32_16x16x64_i8 v[62:65], v[156:159], v[200:203], v[62:65]
	v_mfma_i32_16x16x64_i8 v[58:61], v[164:167], v[200:203], v[58:61]
	v_mfma_i32_16x16x64_i8 v[46:49], v[156:159], v[208:211], v[46:49]
	v_mfma_i32_16x16x64_i8 v[42:45], v[164:167], v[208:211], v[42:45]
	v_mfma_i32_16x16x64_i8 v[30:33], v[156:159], v[216:219], v[30:33]
	v_mfma_i32_16x16x64_i8 v[26:29], v[164:167], v[216:219], v[26:29]
	v_mfma_i32_16x16x64_i8 v[6:9], v[156:159], v[224:227], v[6:9]
	v_mfma_i32_16x16x64_i8 v[2:5], v[164:167], v[224:227], v[2:5]
	v_mfma_i32_16x16x64_i8 v[54:57], v[168:171], v[196:199], v[54:57]
	v_mfma_i32_16x16x64_i8 v[50:53], v[186:189], v[196:199], v[50:53]
	v_mfma_i32_16x16x64_i8 v[38:41], v[168:171], v[204:207], v[38:41]
	v_mfma_i32_16x16x64_i8 v[34:37], v[186:189], v[204:207], v[34:37]
	v_mfma_i32_16x16x64_i8 v[14:17], v[168:171], v[212:215], v[14:17]
	v_mfma_i32_16x16x64_i8 v[10:13], v[186:189], v[212:215], v[10:13]
	v_mfma_i32_16x16x64_i8 v[22:25], v[168:171], v[220:223], v[22:25]
	v_mfma_i32_16x16x64_i8 v[18:21], v[186:189], v[220:223], v[18:21]
	v_mfma_i32_16x16x64_i8 v[54:57], v[182:185], v[200:203], v[54:57]
	v_mfma_i32_16x16x64_i8 v[50:53], v[190:193], v[200:203], v[50:53]
	v_mfma_i32_16x16x64_i8 v[38:41], v[182:185], v[208:211], v[38:41]
	v_mfma_i32_16x16x64_i8 v[34:37], v[190:193], v[208:211], v[34:37]
	v_mfma_i32_16x16x64_i8 v[14:17], v[182:185], v[216:219], v[14:17]
	v_mfma_i32_16x16x64_i8 v[10:13], v[190:193], v[216:219], v[10:13]
	v_mfma_i32_16x16x64_i8 v[22:25], v[182:185], v[224:227], v[22:25]
	v_mfma_i32_16x16x64_i8 v[18:21], v[190:193], v[224:227], v[18:21]
	s_barrier
	s_add_i32 s42, 0, 0x18000
	v_add_u32_e32 v1, s42, v173
	s_add_i32 s43, 0, 0x1c000
	ds_read_b128 v[152:155], v1
	ds_read_b128 v[156:159], v1 offset:1024
	ds_read_b128 v[160:163], v1 offset:2048
	ds_read_b128 v[164:167], v1 offset:3072
	v_add_u32_e32 v1, s43, v173
	ds_read_b128 v[168:171], v1
	ds_read_b128 v[182:185], v1 offset:1024
	ds_read_b128 v[186:189], v1 offset:2048
	ds_read_b128 v[190:193], v1 offset:3072
	s_add_u32 s36, s36, 0x40000
	s_addc_u32 s37, s37, 0
	s_mov_b32 m0, s47
	v_lshl_add_u64 v[236:237], s[36:37], 0, v[136:137]
	ds_read_b128 v[196:199], v177 offset:32768
	ds_read_b128 v[200:203], v177 offset:33792
	ds_read_b128 v[204:207], v177 offset:34816
	ds_read_b128 v[208:211], v177 offset:35840
	ds_read_b128 v[212:215], v177 offset:36864
	ds_read_b128 v[216:219], v177 offset:37888
	ds_read_b128 v[220:223], v177 offset:38912
	ds_read_b128 v[224:227], v177 offset:39936
	global_load_lds_dwordx4 v[236:237], off
	v_lshl_add_u64 v[236:237], s[36:37], 0, v[138:139]
	s_mov_b32 m0, s49
	s_nop 0
	global_load_lds_dwordx4 v[236:237], off
	s_waitcnt vmcnt(8)
	s_waitcnt lgkmcnt(0)
	s_barrier
	s_waitcnt lgkmcnt(0)
	v_mfma_i32_16x16x64_i8 v[126:129], v[152:155], v[196:199], v[126:129]
	v_mfma_i32_16x16x64_i8 v[122:125], v[160:163], v[196:199], v[122:125]
	v_mfma_i32_16x16x64_i8 v[110:113], v[152:155], v[204:207], v[110:113]
	v_mfma_i32_16x16x64_i8 v[106:109], v[160:163], v[204:207], v[106:109]
	v_mfma_i32_16x16x64_i8 v[94:97], v[152:155], v[212:215], v[94:97]
	v_mfma_i32_16x16x64_i8 v[90:93], v[160:163], v[212:215], v[90:93]
	v_mfma_i32_16x16x64_i8 v[78:81], v[152:155], v[220:223], v[78:81]
	v_mfma_i32_16x16x64_i8 v[74:77], v[160:163], v[220:223], v[74:77]
	v_mfma_i32_16x16x64_i8 v[126:129], v[156:159], v[200:203], v[126:129]
	v_mfma_i32_16x16x64_i8 v[122:125], v[164:167], v[200:203], v[122:125]
	v_mfma_i32_16x16x64_i8 v[110:113], v[156:159], v[208:211], v[110:113]
	v_mfma_i32_16x16x64_i8 v[106:109], v[164:167], v[208:211], v[106:109]
	v_mfma_i32_16x16x64_i8 v[94:97], v[156:159], v[216:219], v[94:97]
	v_mfma_i32_16x16x64_i8 v[90:93], v[164:167], v[216:219], v[90:93]
	v_mfma_i32_16x16x64_i8 v[78:81], v[156:159], v[224:227], v[78:81]
	v_mfma_i32_16x16x64_i8 v[74:77], v[164:167], v[224:227], v[74:77]
	v_mfma_i32_16x16x64_i8 v[118:121], v[168:171], v[196:199], v[118:121]
	v_mfma_i32_16x16x64_i8 v[114:117], v[186:189], v[196:199], v[114:117]
	v_mfma_i32_16x16x64_i8 v[102:105], v[168:171], v[204:207], v[102:105]
	v_mfma_i32_16x16x64_i8 v[98:101], v[186:189], v[204:207], v[98:101]
	v_mfma_i32_16x16x64_i8 v[86:89], v[168:171], v[212:215], v[86:89]
	v_mfma_i32_16x16x64_i8 v[82:85], v[186:189], v[212:215], v[82:85]
	v_mfma_i32_16x16x64_i8 v[70:73], v[168:171], v[220:223], v[70:73]
	v_mfma_i32_16x16x64_i8 v[66:69], v[186:189], v[220:223], v[66:69]
	v_mfma_i32_16x16x64_i8 v[118:121], v[182:185], v[200:203], v[118:121]
	v_mfma_i32_16x16x64_i8 v[114:117], v[190:193], v[200:203], v[114:117]
	v_mfma_i32_16x16x64_i8 v[102:105], v[182:185], v[208:211], v[102:105]
	v_mfma_i32_16x16x64_i8 v[98:101], v[190:193], v[208:211], v[98:101]
	v_mfma_i32_16x16x64_i8 v[86:89], v[182:185], v[216:219], v[86:89]
	v_mfma_i32_16x16x64_i8 v[82:85], v[190:193], v[216:219], v[82:85]
	v_mfma_i32_16x16x64_i8 v[70:73], v[182:185], v[224:227], v[70:73]
	v_mfma_i32_16x16x64_i8 v[66:69], v[190:193], v[224:227], v[66:69]
	s_barrier
; #define PG8_STAGE(bufoff, gbase, voff) do { _Pragma("unroll") for (int _i = 0; _i < 2; ++_i) \
;         __builtin_amdgcn_global_load_lds((const unsigned*)((const char*)(gbase) + (voff)[_i]), (LAS unsigned*)(lds + (bufoff) + ldsw + _i * 8192), 16, 0, 0); } while (0)
; #define PG8_LDA(dst, b, h) do { _Pragma("unroll") for (int m = 0; m < 4; ++m) dst[m] = PG8_LD32(lds + PG8_SA(b, h) + aoff + m * 2048); } while (0)
; #define PG8_LDB(dst, b, h) do { _Pragma("unroll") for (int n = 0; n < 2; ++n) dst[n] = PG8_LD32(lds + PG8_SB(b, h) + boff + n * 2048); } while (0)
; #define PG8_WAIT_V(n) asm volatile("s_waitcnt vmcnt(" #n ")" ::: "memory")
; #define PG8_WAIT_L(n) asm volatile("s_waitcnt lgkmcnt(" #n ")" ::: "memory")
; #define PG8_BAR __builtin_amdgcn_s_barrier()
; #define PG8_SCHED __builtin_amdgcn_sched_barrier(0)
; template <class Epi, class Sched, bool ALIGN_EPI, int DT>
; __device__ __forceinline__ void gemm_phase(LAS unsigned char* lds, const int KB, const Sched& S, const Epi& E) {
;     ...
;             const size_t k1 = (size_t)(t + 1) * kstep, k2 = last ? 0 : (size_t)(t + 2) * kstep, k3 = k2 + kstep;
;             const char* b2 = last ? nB : cB + (size_t)(t + 2) * kstep; const char* b3 = b2 + kstep;
;             PG8_LDB(B0, 0, 0); PG8_LDB(B1, 0, 1); PG8_SCHED; PG8_LDA(At, 0, 0); PG8_STA(PG8_SA(1, 1), false, 1, k1);
;             PG8_WAIT_V(8); PG8_WAIT_L(0); PG8_BAR; PG8_MMA(0, 0, At, B0); PG8_MMA(0, 1, At, B1); PG8_BAR; PG8_SCHED;
;             PG8_LDA(At, 0, 1); PG8_STAGE(PG8_SB(0, 0), b2, voffB); PG8_STAGE(PG8_SB(0, 1), b2 + hstep, voffB); PG8_STA(PG8_SA(0, 0), last, 0, k2);
;             PG8_WAIT_V(8); PG8_WAIT_L(0); PG8_BAR; PG8_MMA(1, 0, At, B0); PG8_MMA(1, 1, At, B1); PG8_BAR; PG8_SCHED;
;             PG8_LDB(B0, 1, 0); PG8_LDB(B1, 1, 1); PG8_SCHED; PG8_LDA(At, 1, 0); PG8_STA(PG8_SA(0, 1), last, 1, k2);
;             PG8_WAIT_V(8); PG8_WAIT_L(0); PG8_BAR; PG8_MMA(0, 0, At, B0); PG8_MMA(0, 1, At, B1); PG8_BAR; PG8_SCHED;
;             PG8_LDA(At, 1, 1); PG8_STAGE(PG8_SB(1, 0), b3, voffB); PG8_STAGE(PG8_SB(1, 1), b3 + hstep, voffB); PG8_STA(PG8_SA(1, 0), last, 0, k3);
;             PG8_WAIT_V(8); PG8_WAIT_L(0); PG8_BAR; PG8_MMA(1, 0, At, B0); PG8_MMA(1, 1, At, B1); PG8_BAR; PG8_SCHED;
;         }
	s_add_i32 s36, s42, s5
	v_lshl_add_u64 v[228:229], v[228:229], 0, s[18:19]
	s_mov_b32 m0, s36
	ds_read_b128 v[196:199], v177 offset:49152
	ds_read_b128 v[200:203], v177 offset:50176
	ds_read_b128 v[204:207], v177 offset:51200
	ds_read_b128 v[208:211], v177 offset:52224
	ds_read_b128 v[212:215], v177 offset:53248
	ds_read_b128 v[216:219], v177 offset:54272
	ds_read_b128 v[220:223], v177 offset:55296
	ds_read_b128 v[224:227], v177 offset:56320
	global_load_lds_dwordx4 v[228:229], off
	s_add_i32 m0, s36, 0x2000
	s_add_u32 s36, s40, 0x40080
	v_lshl_add_u64 v[228:229], v[230:231], 0, s[18:19]
	s_addc_u32 s37, s41, 0
	s_add_i32 s40, s43, s5
	global_load_lds_dwordx4 v[228:229], off
	v_lshl_add_u64 v[228:229], s[36:37], 0, v[134:135]
	s_mov_b32 m0, s40
	s_nop 0
	global_load_lds_dwordx4 v[228:229], off
	v_lshl_add_u64 v[228:229], s[36:37], 0, v[132:133]
	s_add_i32 m0, s40, 0x2000
	s_nop 0
	global_load_lds_dwordx4 v[228:229], off
	v_lshl_add_u64 v[228:229], v[232:233], 0, s[18:19]
	s_mov_b32 m0, s55
	s_nop 0
	global_load_lds_dwordx4 v[228:229], off
	v_lshl_add_u64 v[228:229], v[234:235], 0, s[18:19]
	s_mov_b32 m0, s56
	s_nop 0
	global_load_lds_dwordx4 v[228:229], off
	s_waitcnt vmcnt(8)
	s_waitcnt lgkmcnt(0)
	s_barrier
	s_waitcnt lgkmcnt(0)
	v_mfma_i32_16x16x64_i8 v[62:65], v[152:155], v[196:199], v[62:65]
	v_mfma_i32_16x16x64_i8 v[58:61], v[160:163], v[196:199], v[58:61]
	v_mfma_i32_16x16x64_i8 v[46:49], v[152:155], v[204:207], v[46:49]
	v_mfma_i32_16x16x64_i8 v[42:45], v[160:163], v[204:207], v[42:45]
	v_mfma_i32_16x16x64_i8 v[30:33], v[152:155], v[212:215], v[30:33]
	v_mfma_i32_16x16x64_i8 v[26:29], v[160:163], v[212:215], v[26:29]
	v_mfma_i32_16x16x64_i8 v[6:9], v[152:155], v[220:223], v[6:9]
	v_mfma_i32_16x16x64_i8 v[2:5], v[160:163], v[220:223], v[2:5]
	v_mfma_i32_16x16x64_i8 v[62:65], v[156:159], v[200:203], v[62:65]
	v_mfma_i32_16x16x64_i8 v[58:61], v[164:167], v[200:203], v[58:61]
	v_mfma_i32_16x16x64_i8 v[46:49], v[156:159], v[208:211], v[46:49]
	v_mfma_i32_16x16x64_i8 v[42:45], v[164:167], v[208:211], v[42:45]
	v_mfma_i32_16x16x64_i8 v[30:33], v[156:159], v[216:219], v[30:33]
	v_mfma_i32_16x16x64_i8 v[26:29], v[164:167], v[216:219], v[26:29]
	v_mfma_i32_16x16x64_i8 v[6:9], v[156:159], v[224:227], v[6:9]
	v_mfma_i32_16x16x64_i8 v[2:5], v[164:167], v[224:227], v[2:5]
	v_mfma_i32_16x16x64_i8 v[54:57], v[168:171], v[196:199], v[54:57]
	v_mfma_i32_16x16x64_i8 v[50:53], v[186:189], v[196:199], v[50:53]
	v_mfma_i32_16x16x64_i8 v[38:41], v[168:171], v[204:207], v[38:41]
	v_mfma_i32_16x16x64_i8 v[34:37], v[186:189], v[204:207], v[34:37]
	v_mfma_i32_16x16x64_i8 v[14:17], v[168:171], v[212:215], v[14:17]
	v_mfma_i32_16x16x64_i8 v[10:13], v[186:189], v[212:215], v[10:13]
	v_mfma_i32_16x16x64_i8 v[22:25], v[168:171], v[220:223], v[22:25]
	v_mfma_i32_16x16x64_i8 v[18:21], v[186:189], v[220:223], v[18:21]
	v_mfma_i32_16x16x64_i8 v[54:57], v[182:185], v[200:203], v[54:57]
	v_mfma_i32_16x16x64_i8 v[50:53], v[190:193], v[200:203], v[50:53]
	v_mfma_i32_16x16x64_i8 v[38:41], v[182:185], v[208:211], v[38:41]
	v_mfma_i32_16x16x64_i8 v[34:37], v[190:193], v[208:211], v[34:37]
	v_mfma_i32_16x16x64_i8 v[14:17], v[182:185], v[216:219], v[14:17]
	v_mfma_i32_16x16x64_i8 v[10:13], v[190:193], v[216:219], v[10:13]
	v_mfma_i32_16x16x64_i8 v[22:25], v[182:185], v[224:227], v[22:25]
	v_mfma_i32_16x16x64_i8 v[18:21], v[190:193], v[224:227], v[18:21]
	s_barrier
	s_add_i32 s67, s67, 2
	s_cmp_gt_u32 s67, 13
	s_mov_b64 s[36:37], s[38:39]
	s_cbranch_scc0 .LBB0_193
	s_and_b64 vcc, exec, s[20:21]
	s_cbranch_vccz .LBB0_196
	s_barrier

; #define PG8_STAGE(bufoff, gbase, voff) do { _Pragma("unroll") for (int _i = 0; _i < 2; ++_i) \
;         __builtin_amdgcn_global_load_lds((const unsigned*)((const char*)(gbase) + (voff)[_i]), (LAS unsigned*)(lds + (bufoff) + ldsw + _i * 8192), 16, 0, 0); } while (0)
; #define PG8_LDA(dst, b, h) do { _Pragma("unroll") for (int m = 0; m < 4; ++m) dst[m] = PG8_LD32(lds + PG8_SA(b, h) + aoff + m * 2048); } while (0)
; #define PG8_LDB(dst, b, h) do { _Pragma("unroll") for (int n = 0; n < 2; ++n) dst[n] = PG8_LD32(lds + PG8_SB(b, h) + boff + n * 2048); } while (0)
; #define PG8_WAIT_V(n) asm volatile("s_waitcnt vmcnt(" #n ")" ::: "memory")
; #define PG8_WAIT_L(n) asm volatile("s_waitcnt lgkmcnt(" #n ")" ::: "memory")
; #define PG8_BAR __builtin_amdgcn_s_barrier()
; #define PG8_SCHED __builtin_amdgcn_sched_barrier(0)
; template <class Epi, class Sched, bool ALIGN_EPI, int DT>
; __device__ __forceinline__ void gemm_phase(LAS unsigned char* lds, const int KB, const Sched& S, const Epi& E) {
;     ...
;             const size_t k1 = (size_t)(t + 1) * kstep, k2 = last ? 0 : (size_t)(t + 2) * kstep, k3 = k2 + kstep;
;             const char* b2 = last ? nB : cB + (size_t)(t + 2) * kstep; const char* b3 = b2 + kstep;
;             PG8_LDB(B0, 0, 0); PG8_LDB(B1, 0, 1); PG8_SCHED; PG8_LDA(At, 0, 0); PG8_STA(PG8_SA(1, 1), false, 1, k1);
;             PG8_WAIT_V(8); PG8_WAIT_L(0); PG8_BAR; PG8_MMA(0, 0, At, B0); PG8_MMA(0, 1, At, B1); PG8_BAR; PG8_SCHED;
;             PG8_LDA(At, 0, 1); PG8_STAGE(PG8_SB(0, 0), b2, voffB); PG8_STAGE(PG8_SB(0, 1), b2 + hstep, voffB); PG8_STA(PG8_SA(0, 0), last, 0, k2);
;             PG8_WAIT_V(8); PG8_WAIT_L(0); PG8_BAR; PG8_MMA(1, 0, At, B0); PG8_MMA(1, 1, At, B1); PG8_BAR; PG8_SCHED;
;             PG8_LDB(B0, 1, 0); PG8_LDB(B1, 1, 1); PG8_SCHED; PG8_LDA(At, 1, 0); PG8_STA(PG8_SA(0, 1), last, 1, k2);
;             PG8_WAIT_V(8); PG8_WAIT_L(0); PG8_BAR; PG8_MMA(0, 0, At, B0); PG8_MMA(0, 1, At, B1); PG8_BAR; PG8_SCHED;
;             PG8_LDA(At, 1, 1); PG8_STAGE(PG8_SB(1, 0), b3, voffB); PG8_STAGE(PG8_SB(1, 1), b3 + hstep, voffB); PG8_STA(PG8_SA(1, 0), last, 0, k3);
;             PG8_WAIT_V(8); PG8_WAIT_L(0); PG8_BAR; PG8_MMA(1, 0, At, B0); PG8_MMA(1, 1, At, B1); PG8_BAR; PG8_SCHED;
;         }
.LBB0_1018:
	ds_read_b128 v[18:21], v193
	ds_read_b128 v[22:25], v193 offset:1024
	ds_read_b128 v[26:29], v193 offset:2048
	ds_read_b128 v[30:33], v193 offset:3072
	ds_read_b128 v[2:5], v195
	ds_read_b128 v[6:9], v195 offset:1024
	ds_read_b128 v[10:13], v195 offset:2048
	ds_read_b128 v[14:17], v195 offset:3072
	s_add_u32 s34, s38, 0x100
	s_addc_u32 s35, s39, 0
	s_add_u32 s68, s63, s38
	s_addc_u32 s69, s66, s39
	s_cmp_eq_u32 s67, 12
	s_cselect_b64 s[40:41], -1, 0
	s_and_b64 s[36:37], s[40:41], exec
	s_cselect_b32 s37, s21, s69
	s_cselect_b32 s36, s23, s68
	s_cselect_b32 s68, 0, s35
	s_cselect_b32 s69, 0, s34
	v_lshl_add_u64 v[222:223], v[178:179], 0, s[38:39]
	s_add_i32 m0, s29, 0xc000
	ds_read_b128 v[182:185], v196
	ds_read_b128 v[186:189], v196 offset:1024
	ds_read_b128 v[198:201], v196 offset:2048
	ds_read_b128 v[202:205], v196 offset:3072
	ds_read_b128 v[206:209], v196 offset:4096
	ds_read_b128 v[210:213], v196 offset:5120
	ds_read_b128 v[214:217], v196 offset:6144
	ds_read_b128 v[218:221], v196 offset:7168
	global_load_lds_dwordx4 v[222:223], off
	v_lshl_add_u64 v[222:223], v[180:181], 0, s[38:39]
	s_add_i32 m0, s29, 0xe000
	s_nop 0
	global_load_lds_dwordx4 v[222:223], off
	s_waitcnt vmcnt(8)
	s_waitcnt lgkmcnt(0)
	s_barrier
	s_waitcnt lgkmcnt(0)
	v_mfma_scale_f32_16x16x128_f8f6f4 v[158:161], v[18:25], v[182:189], v[158:161], v190, v190 op_sel_hi:[0,0,0]
	v_mfma_scale_f32_16x16x128_f8f6f4 v[154:157], v[26:33], v[182:189], v[154:157], v190, v190 op_sel_hi:[0,0,0]
	v_mfma_scale_f32_16x16x128_f8f6f4 v[150:153], v[18:25], v[198:205], v[150:153], v190, v190 op_sel_hi:[0,0,0]
	v_mfma_scale_f32_16x16x128_f8f6f4 v[142:145], v[26:33], v[198:205], v[142:145], v190, v190 op_sel_hi:[0,0,0]
	v_mfma_scale_f32_16x16x128_f8f6f4 v[134:137], v[18:25], v[206:213], v[134:137], v190, v190 op_sel_hi:[0,0,0]
	v_mfma_scale_f32_16x16x128_f8f6f4 v[126:129], v[26:33], v[206:213], v[126:129], v190, v190 op_sel_hi:[0,0,0]
	v_mfma_scale_f32_16x16x128_f8f6f4 v[118:121], v[18:25], v[214:221], v[118:121], v190, v190 op_sel_hi:[0,0,0]
	v_mfma_scale_f32_16x16x128_f8f6f4 v[110:113], v[26:33], v[214:221], v[110:113], v190, v190 op_sel_hi:[0,0,0]
	v_mfma_scale_f32_16x16x128_f8f6f4 v[146:149], v[2:9], v[182:189], v[146:149], v190, v190 op_sel_hi:[0,0,0]
	v_mfma_scale_f32_16x16x128_f8f6f4 v[138:141], v[10:17], v[182:189], v[138:141], v190, v190 op_sel_hi:[0,0,0]
	v_mfma_scale_f32_16x16x128_f8f6f4 v[130:133], v[2:9], v[198:205], v[130:133], v190, v190 op_sel_hi:[0,0,0]
	v_mfma_scale_f32_16x16x128_f8f6f4 v[122:125], v[10:17], v[198:205], v[122:125], v190, v190 op_sel_hi:[0,0,0]
	v_mfma_scale_f32_16x16x128_f8f6f4 v[114:117], v[2:9], v[206:213], v[114:117], v190, v190 op_sel_hi:[0,0,0]
	v_mfma_scale_f32_16x16x128_f8f6f4 v[106:109], v[10:17], v[206:213], v[106:109], v190, v190 op_sel_hi:[0,0,0]
	v_mfma_scale_f32_16x16x128_f8f6f4 v[102:105], v[2:9], v[214:221], v[102:105], v190, v190 op_sel_hi:[0,0,0]
	v_mfma_scale_f32_16x16x128_f8f6f4 v[98:101], v[10:17], v[214:221], v[98:101], v190, v190 op_sel_hi:[0,0,0]
	s_barrier
	s_add_i32 s38, s53, s42
	v_lshl_add_u64 v[182:183], s[36:37], 0, v[162:163]
	s_mov_b32 m0, s38
	ds_read_b128 v[198:201], v196 offset:16384
	ds_read_b128 v[202:205], v196 offset:17408
	ds_read_b128 v[206:209], v196 offset:18432
	ds_read_b128 v[210:213], v196 offset:19456
	ds_read_b128 v[214:217], v196 offset:20480
	ds_read_b128 v[218:221], v196 offset:21504
	ds_read_b128 v[222:225], v196 offset:22528
	ds_read_b128 v[226:229], v196 offset:23552
	global_load_lds_dwordx4 v[182:183], off
	s_add_i32 m0, s38, 0x2000
	s_add_u32 s38, s36, 0x40000
	v_lshl_add_u64 v[184:185], s[36:37], 0, v[164:165]
	s_addc_u32 s39, s37, 0
	s_add_i32 s70, s54, s42
	global_load_lds_dwordx4 v[184:185], off
	v_lshl_add_u64 v[186:187], s[38:39], 0, v[162:163]
	s_mov_b32 m0, s70
	s_nop 0
	global_load_lds_dwordx4 v[186:187], off
	v_lshl_add_u64 v[186:187], s[38:39], 0, v[164:165]
	s_add_i32 m0, s70, 0x2000
	s_and_b64 s[38:39], s[6:7], s[40:41]
	s_and_b64 s[38:39], s[38:39], exec
	s_cselect_b32 s38, s24, s30
	s_cselect_b32 s39, s25, s31
	s_add_u32 s38, s38, s69
	s_addc_u32 s39, s39, s68
	global_load_lds_dwordx4 v[186:187], off
	v_lshl_add_u64 v[186:187], s[38:39], 0, v[166:167]
	s_mov_b32 m0, s29
	v_lshl_add_u64 v[188:189], s[38:39], 0, v[168:169]
	global_load_lds_dwordx4 v[186:187], off
	s_mov_b32 m0, s43
	s_nop 0
	global_load_lds_dwordx4 v[188:189], off
	s_waitcnt vmcnt(8)
	s_waitcnt lgkmcnt(0)
	s_barrier
	s_waitcnt lgkmcnt(0)
	v_mfma_scale_f32_16x16x128_f8f6f4 v[94:97], v[18:25], v[198:205], v[94:97], v190, v190 op_sel_hi:[0,0,0]
	v_mfma_scale_f32_16x16x128_f8f6f4 v[90:93], v[26:33], v[198:205], v[90:93], v190, v190 op_sel_hi:[0,0,0]
	v_mfma_scale_f32_16x16x128_f8f6f4 v[86:89], v[18:25], v[206:213], v[86:89], v190, v190 op_sel_hi:[0,0,0]
	v_mfma_scale_f32_16x16x128_f8f6f4 v[78:81], v[26:33], v[206:213], v[78:81], v190, v190 op_sel_hi:[0,0,0]
	v_mfma_scale_f32_16x16x128_f8f6f4 v[62:65], v[18:25], v[214:221], v[62:65], v190, v190 op_sel_hi:[0,0,0]
	v_mfma_scale_f32_16x16x128_f8f6f4 v[54:57], v[26:33], v[214:221], v[54:57], v190, v190 op_sel_hi:[0,0,0]
	v_mfma_scale_f32_16x16x128_f8f6f4 v[46:49], v[18:25], v[222:229], v[46:49], v190, v190 op_sel_hi:[0,0,0]
	v_mfma_scale_f32_16x16x128_f8f6f4 v[38:41], v[26:33], v[222:229], v[38:41], v190, v190 op_sel_hi:[0,0,0]
	v_mfma_scale_f32_16x16x128_f8f6f4 v[82:85], v[2:9], v[198:205], v[82:85], v190, v190 op_sel_hi:[0,0,0]
	v_mfma_scale_f32_16x16x128_f8f6f4 v[74:77], v[10:17], v[198:205], v[74:77], v190, v190 op_sel_hi:[0,0,0]
	v_mfma_scale_f32_16x16x128_f8f6f4 v[58:61], v[2:9], v[206:213], v[58:61], v190, v190 op_sel_hi:[0,0,0]
	v_mfma_scale_f32_16x16x128_f8f6f4 v[50:53], v[10:17], v[206:213], v[50:53], v190, v190 op_sel_hi:[0,0,0]
	v_mfma_scale_f32_16x16x128_f8f6f4 v[42:45], v[2:9], v[214:221], v[42:45], v190, v190 op_sel_hi:[0,0,0]
	v_mfma_scale_f32_16x16x128_f8f6f4 v[34:37], v[10:17], v[214:221], v[34:37], v190, v190 op_sel_hi:[0,0,0]
	v_mfma_scale_f32_16x16x128_f8f6f4 v[70:73], v[2:9], v[222:229], v[70:73], v190, v190 op_sel_hi:[0,0,0]
	v_mfma_scale_f32_16x16x128_f8f6f4 v[66:69], v[10:17], v[222:229], v[66:69], v190, v190 op_sel_hi:[0,0,0]
	s_barrier
; #define PG8_STAGE(bufoff, gbase, voff) do { _Pragma("unroll") for (int _i = 0; _i < 2; ++_i) \
;         __builtin_amdgcn_global_load_lds((const unsigned*)((const char*)(gbase) + (voff)[_i]), (LAS unsigned*)(lds + (bufoff) + ldsw + _i * 8192), 16, 0, 0); } while (0)
; #define PG8_LDA(dst, b, h) do { _Pragma("unroll") for (int m = 0; m < 4; ++m) dst[m] = PG8_LD32(lds + PG8_SA(b, h) + aoff + m * 2048); } while (0)
; #define PG8_LDB(dst, b, h) do { _Pragma("unroll") for (int n = 0; n < 2; ++n) dst[n] = PG8_LD32(lds + PG8_SB(b, h) + boff + n * 2048); } while (0)
; #define PG8_WAIT_V(n) asm volatile("s_waitcnt vmcnt(" #n ")" ::: "memory")
; #define PG8_WAIT_L(n) asm volatile("s_waitcnt lgkmcnt(" #n ")" ::: "memory")
; #define PG8_BAR __builtin_amdgcn_s_barrier()
; #define PG8_SCHED __builtin_amdgcn_sched_barrier(0)
; template <class Epi, class Sched, bool ALIGN_EPI, int DT>
; __device__ __forceinline__ void gemm_phase(LAS unsigned char* lds, const int KB, const Sched& S, const Epi& E) {
;     ...
;             const size_t k1 = (size_t)(t + 1) * kstep, k2 = last ? 0 : (size_t)(t + 2) * kstep, k3 = k2 + kstep;
;             const char* b2 = last ? nB : cB + (size_t)(t + 2) * kstep; const char* b3 = b2 + kstep;
;             PG8_LDB(B0, 0, 0); PG8_LDB(B1, 0, 1); PG8_SCHED; PG8_LDA(At, 0, 0); PG8_STA(PG8_SA(1, 1), false, 1, k1);
;             PG8_WAIT_V(8); PG8_WAIT_L(0); PG8_BAR; PG8_MMA(0, 0, At, B0); PG8_MMA(0, 1, At, B1); PG8_BAR; PG8_SCHED;
;             PG8_LDA(At, 0, 1); PG8_STAGE(PG8_SB(0, 0), b2, voffB); PG8_STAGE(PG8_SB(0, 1), b2 + hstep, voffB); PG8_STA(PG8_SA(0, 0), last, 0, k2);
;             PG8_WAIT_V(8); PG8_WAIT_L(0); PG8_BAR; PG8_MMA(1, 0, At, B0); PG8_MMA(1, 1, At, B1); PG8_BAR; PG8_SCHED;
;             PG8_LDB(B0, 1, 0); PG8_LDB(B1, 1, 1); PG8_SCHED; PG8_LDA(At, 1, 0); PG8_STA(PG8_SA(0, 1), last, 1, k2);
;             PG8_WAIT_V(8); PG8_WAIT_L(0); PG8_BAR; PG8_MMA(0, 0, At, B0); PG8_MMA(0, 1, At, B1); PG8_BAR; PG8_SCHED;
;             PG8_LDA(At, 1, 1); PG8_STAGE(PG8_SB(1, 0), b3, voffB); PG8_STAGE(PG8_SB(1, 1), b3 + hstep, voffB); PG8_STA(PG8_SA(1, 0), last, 0, k3);
;             PG8_WAIT_V(8); PG8_WAIT_L(0); PG8_BAR; PG8_MMA(1, 0, At, B0); PG8_MMA(1, 1, At, B1); PG8_BAR; PG8_SCHED;
;         }
	s_add_i32 s40, 0, 0x18000
	s_add_i32 s41, 0, 0x1c000
	v_add_u32_e32 v14, s40, v191
	v_add_u32_e32 v30, s41, v191
	ds_read_b128 v[2:5], v14
	ds_read_b128 v[6:9], v14 offset:1024
	ds_read_b128 v[10:13], v14 offset:2048
	ds_read_b128 v[14:17], v14 offset:3072
	ds_read_b128 v[18:21], v30
	ds_read_b128 v[22:25], v30 offset:1024
	ds_read_b128 v[26:29], v30 offset:2048
	ds_read_b128 v[30:33], v30 offset:3072
	s_add_u32 s38, s38, 0x40000
	s_addc_u32 s39, s39, 0
	s_mov_b32 m0, s44
	v_lshl_add_u64 v[230:231], s[38:39], 0, v[166:167]
	ds_read_b128 v[198:201], v196 offset:32768
	ds_read_b128 v[202:205], v196 offset:33792
	ds_read_b128 v[206:209], v196 offset:34816
	ds_read_b128 v[210:213], v196 offset:35840
	ds_read_b128 v[214:217], v196 offset:36864
	ds_read_b128 v[218:221], v196 offset:37888
	ds_read_b128 v[222:225], v196 offset:38912
	ds_read_b128 v[226:229], v196 offset:39936
	global_load_lds_dwordx4 v[230:231], off
	v_lshl_add_u64 v[230:231], s[38:39], 0, v[168:169]
	s_mov_b32 m0, s45
	s_nop 0
	global_load_lds_dwordx4 v[230:231], off
	s_waitcnt vmcnt(8)
	s_waitcnt lgkmcnt(0)
	s_barrier
	s_waitcnt lgkmcnt(0)
	v_mfma_scale_f32_16x16x128_f8f6f4 v[158:161], v[2:9], v[198:205], v[158:161], v190, v190 op_sel_hi:[0,0,0]
	v_mfma_scale_f32_16x16x128_f8f6f4 v[154:157], v[10:17], v[198:205], v[154:157], v190, v190 op_sel_hi:[0,0,0]
	v_mfma_scale_f32_16x16x128_f8f6f4 v[150:153], v[2:9], v[206:213], v[150:153], v190, v190 op_sel_hi:[0,0,0]
	v_mfma_scale_f32_16x16x128_f8f6f4 v[142:145], v[10:17], v[206:213], v[142:145], v190, v190 op_sel_hi:[0,0,0]
	v_mfma_scale_f32_16x16x128_f8f6f4 v[134:137], v[2:9], v[214:221], v[134:137], v190, v190 op_sel_hi:[0,0,0]
	v_mfma_scale_f32_16x16x128_f8f6f4 v[126:129], v[10:17], v[214:221], v[126:129], v190, v190 op_sel_hi:[0,0,0]
	v_mfma_scale_f32_16x16x128_f8f6f4 v[118:121], v[2:9], v[222:229], v[118:121], v190, v190 op_sel_hi:[0,0,0]
	v_mfma_scale_f32_16x16x128_f8f6f4 v[110:113], v[10:17], v[222:229], v[110:113], v190, v190 op_sel_hi:[0,0,0]
	v_mfma_scale_f32_16x16x128_f8f6f4 v[146:149], v[18:25], v[198:205], v[146:149], v190, v190 op_sel_hi:[0,0,0]
	v_mfma_scale_f32_16x16x128_f8f6f4 v[138:141], v[26:33], v[198:205], v[138:141], v190, v190 op_sel_hi:[0,0,0]
	v_mfma_scale_f32_16x16x128_f8f6f4 v[130:133], v[18:25], v[206:213], v[130:133], v190, v190 op_sel_hi:[0,0,0]
	v_mfma_scale_f32_16x16x128_f8f6f4 v[122:125], v[26:33], v[206:213], v[122:125], v190, v190 op_sel_hi:[0,0,0]
	v_mfma_scale_f32_16x16x128_f8f6f4 v[114:117], v[18:25], v[214:221], v[114:117], v190, v190 op_sel_hi:[0,0,0]
	v_mfma_scale_f32_16x16x128_f8f6f4 v[106:109], v[26:33], v[214:221], v[106:109], v190, v190 op_sel_hi:[0,0,0]
	v_mfma_scale_f32_16x16x128_f8f6f4 v[102:105], v[18:25], v[222:229], v[102:105], v190, v190 op_sel_hi:[0,0,0]
	v_mfma_scale_f32_16x16x128_f8f6f4 v[98:101], v[26:33], v[222:229], v[98:101], v190, v190 op_sel_hi:[0,0,0]
	s_barrier
	s_add_i32 s38, s40, s42
	v_lshl_add_u64 v[182:183], v[182:183], 0, s[10:11]
	s_mov_b32 m0, s38
	ds_read_b128 v[198:201], v196 offset:49152
	ds_read_b128 v[202:205], v196 offset:50176
	ds_read_b128 v[206:209], v196 offset:51200
	ds_read_b128 v[210:213], v196 offset:52224
	ds_read_b128 v[214:217], v196 offset:53248
	ds_read_b128 v[218:221], v196 offset:54272
	ds_read_b128 v[222:225], v196 offset:55296
	ds_read_b128 v[226:229], v196 offset:56320
	global_load_lds_dwordx4 v[182:183], off
	s_add_i32 m0, s38, 0x2000
	s_add_u32 s36, s36, 0x40080
	v_lshl_add_u64 v[182:183], v[184:185], 0, s[10:11]
	s_addc_u32 s37, s37, 0
	s_add_i32 s38, s41, s42
	global_load_lds_dwordx4 v[182:183], off
	v_lshl_add_u64 v[182:183], s[36:37], 0, v[162:163]
	s_mov_b32 m0, s38
	s_nop 0
	global_load_lds_dwordx4 v[182:183], off
	v_lshl_add_u64 v[182:183], s[36:37], 0, v[164:165]
	s_add_i32 m0, s38, 0x2000
	s_nop 0
	global_load_lds_dwordx4 v[182:183], off
	v_lshl_add_u64 v[182:183], v[186:187], 0, s[10:11]
	s_mov_b32 m0, s47
	s_nop 0
	global_load_lds_dwordx4 v[182:183], off
	v_lshl_add_u64 v[182:183], v[188:189], 0, s[10:11]
	s_mov_b32 m0, s49
	s_nop 0
	global_load_lds_dwordx4 v[182:183], off
	s_waitcnt vmcnt(8)
	s_waitcnt lgkmcnt(0)
	s_barrier
	s_waitcnt lgkmcnt(0)
	v_mfma_scale_f32_16x16x128_f8f6f4 v[94:97], v[2:9], v[198:205], v[94:97], v190, v190 op_sel_hi:[0,0,0]
	v_mfma_scale_f32_16x16x128_f8f6f4 v[90:93], v[10:17], v[198:205], v[90:93], v190, v190 op_sel_hi:[0,0,0]
	v_mfma_scale_f32_16x16x128_f8f6f4 v[86:89], v[2:9], v[206:213], v[86:89], v190, v190 op_sel_hi:[0,0,0]
	v_mfma_scale_f32_16x16x128_f8f6f4 v[78:81], v[10:17], v[206:213], v[78:81], v190, v190 op_sel_hi:[0,0,0]
	v_mfma_scale_f32_16x16x128_f8f6f4 v[62:65], v[2:9], v[214:221], v[62:65], v190, v190 op_sel_hi:[0,0,0]
	v_mfma_scale_f32_16x16x128_f8f6f4 v[54:57], v[10:17], v[214:221], v[54:57], v190, v190 op_sel_hi:[0,0,0]
	v_mfma_scale_f32_16x16x128_f8f6f4 v[46:49], v[2:9], v[222:229], v[46:49], v190, v190 op_sel_hi:[0,0,0]
	v_mfma_scale_f32_16x16x128_f8f6f4 v[38:41], v[10:17], v[222:229], v[38:41], v190, v190 op_sel_hi:[0,0,0]
	v_mfma_scale_f32_16x16x128_f8f6f4 v[82:85], v[18:25], v[198:205], v[82:85], v190, v190 op_sel_hi:[0,0,0]
	v_mfma_scale_f32_16x16x128_f8f6f4 v[74:77], v[26:33], v[198:205], v[74:77], v190, v190 op_sel_hi:[0,0,0]
	v_mfma_scale_f32_16x16x128_f8f6f4 v[58:61], v[18:25], v[206:213], v[58:61], v190, v190 op_sel_hi:[0,0,0]
	v_mfma_scale_f32_16x16x128_f8f6f4 v[50:53], v[26:33], v[206:213], v[50:53], v190, v190 op_sel_hi:[0,0,0]
	v_mfma_scale_f32_16x16x128_f8f6f4 v[42:45], v[18:25], v[214:221], v[42:45], v190, v190 op_sel_hi:[0,0,0]
	v_mfma_scale_f32_16x16x128_f8f6f4 v[34:37], v[26:33], v[214:221], v[34:37], v190, v190 op_sel_hi:[0,0,0]
	v_mfma_scale_f32_16x16x128_f8f6f4 v[70:73], v[18:25], v[222:229], v[70:73], v190, v190 op_sel_hi:[0,0,0]
	v_mfma_scale_f32_16x16x128_f8f6f4 v[66:69], v[26:33], v[222:229], v[66:69], v190, v190 op_sel_hi:[0,0,0]
	s_barrier
	s_add_i32 s67, s67, 2
	s_cmp_gt_u32 s67, 13
	s_mov_b64 s[38:39], s[34:35]
	s_cbranch_scc0 .LBB0_1018
	s_and_b64 vcc, exec, s[12:13]
	s_cbranch_vccz .LBB0_1021
	s_barrier

; #define PG8_STAGE(bufoff, gbase, voff) do { _Pragma("unroll") for (int _i = 0; _i < 2; ++_i) \
;         __builtin_amdgcn_global_load_lds((const unsigned*)((const char*)(gbase) + (voff)[_i]), (LAS unsigned*)(lds + (bufoff) + ldsw + _i * 8192), 16, 0, 0); } while (0)
; #define PG8_LDA(dst, b, h) do { _Pragma("unroll") for (int m = 0; m < 4; ++m) dst[m] = PG8_LD32(lds + PG8_SA(b, h) + aoff + m * 2048); } while (0)
; #define PG8_LDB(dst, b, h) do { _Pragma("unroll") for (int n = 0; n < 2; ++n) dst[n] = PG8_LD32(lds + PG8_SB(b, h) + boff + n * 2048); } while (0)
; #define PG8_WAIT_V(n) asm volatile("s_waitcnt vmcnt(" #n ")" ::: "memory")
; #define PG8_WAIT_L(n) asm volatile("s_waitcnt lgkmcnt(" #n ")" ::: "memory")
; #define PG8_BAR __builtin_amdgcn_s_barrier()
; #define PG8_SCHED __builtin_amdgcn_sched_barrier(0)
; template <class Epi, class Sched, bool ALIGN_EPI, int DT>
; __device__ __forceinline__ void gemm_phase(LAS unsigned char* lds, const int KB, const Sched& S, const Epi& E) {
;     ...
;             const size_t k1 = (size_t)(t + 1) * kstep, k2 = last ? 0 : (size_t)(t + 2) * kstep, k3 = k2 + kstep;
;             const char* b2 = last ? nB : cB + (size_t)(t + 2) * kstep; const char* b3 = b2 + kstep;
;             PG8_LDB(B0, 0, 0); PG8_LDB(B1, 0, 1); PG8_SCHED; PG8_LDA(At, 0, 0); PG8_STA(PG8_SA(1, 1), false, 1, k1);
;             PG8_WAIT_V(8); PG8_WAIT_L(0); PG8_BAR; PG8_MMA(0, 0, At, B0); PG8_MMA(0, 1, At, B1); PG8_BAR; PG8_SCHED;
;             PG8_LDA(At, 0, 1); PG8_STAGE(PG8_SB(0, 0), b2, voffB); PG8_STAGE(PG8_SB(0, 1), b2 + hstep, voffB); PG8_STA(PG8_SA(0, 0), last, 0, k2);
;             PG8_WAIT_V(8); PG8_WAIT_L(0); PG8_BAR; PG8_MMA(1, 0, At, B0); PG8_MMA(1, 1, At, B1); PG8_BAR; PG8_SCHED;
;             PG8_LDB(B0, 1, 0); PG8_LDB(B1, 1, 1); PG8_SCHED; PG8_LDA(At, 1, 0); PG8_STA(PG8_SA(0, 1), last, 1, k2);
;             PG8_WAIT_V(8); PG8_WAIT_L(0); PG8_BAR; PG8_MMA(0, 0, At, B0); PG8_MMA(0, 1, At, B1); PG8_BAR; PG8_SCHED;
;             PG8_LDA(At, 1, 1); PG8_STAGE(PG8_SB(1, 0), b3, voffB); PG8_STAGE(PG8_SB(1, 1), b3 + hstep, voffB); PG8_STA(PG8_SA(1, 0), last, 0, k3);
;             PG8_WAIT_V(8); PG8_WAIT_L(0); PG8_BAR; PG8_MMA(1, 0, At, B0); PG8_MMA(1, 1, At, B1); PG8_BAR; PG8_SCHED;
;         }
.LBB0_1154:
	ds_read_b128 v[70:73], v167
	ds_read_b128 v[156:159], v167 offset:1024
	ds_read_b128 v[160:163], v167 offset:2048
	ds_read_b128 v[172:175], v167 offset:3072
	ds_read_b128 v[176:179], v168
	ds_read_b128 v[180:183], v168 offset:1024
	ds_read_b128 v[184:187], v168 offset:2048
	ds_read_b128 v[188:191], v168 offset:3072
	s_add_u32 s30, s28, 0x100
	s_addc_u32 s31, s29, 0
	s_add_u32 s63, s56, s28
	s_addc_u32 s66, s57, s29
	s_cmp_eq_u32 s62, 12
	s_cselect_b64 s[36:37], -1, 0
	s_and_b64 s[34:35], s[36:37], exec
	s_cselect_b32 s67, 0, s30
	s_cselect_b32 s35, s17, s66
	s_cselect_b32 s34, s19, s63
	v_lshl_add_u64 v[192:193], v[66:67], 0, s[28:29]
	s_add_i32 m0, s25, 0xc000
	ds_read_b128 v[196:199], v169
	ds_read_b128 v[200:203], v169 offset:1024
	ds_read_b128 v[204:207], v169 offset:2048
	ds_read_b128 v[208:211], v169 offset:3072
	ds_read_b128 v[212:215], v169 offset:4096
	ds_read_b128 v[216:219], v169 offset:5120
	ds_read_b128 v[220:223], v169 offset:6144
	ds_read_b128 v[224:227], v169 offset:7168
	global_load_lds_dwordx4 v[192:193], off
	v_lshl_add_u64 v[192:193], v[68:69], 0, s[28:29]
	s_add_i32 m0, s25, 0xe000
	s_nop 0
	global_load_lds_dwordx4 v[192:193], off
	s_waitcnt vmcnt(8)
	s_waitcnt lgkmcnt(0)
	s_barrier
	s_waitcnt lgkmcnt(0)
	v_mfma_i32_16x16x64_i8 v[134:137], v[70:73], v[196:199], v[134:137]
	v_mfma_i32_16x16x64_i8 v[126:129], v[160:163], v[196:199], v[126:129]
	v_mfma_i32_16x16x64_i8 v[118:121], v[70:73], v[204:207], v[118:121]
	v_mfma_i32_16x16x64_i8 v[110:113], v[160:163], v[204:207], v[110:113]
	v_mfma_i32_16x16x64_i8 v[102:105], v[70:73], v[212:215], v[102:105]
	v_mfma_i32_16x16x64_i8 v[94:97], v[160:163], v[212:215], v[94:97]
	v_mfma_i32_16x16x64_i8 v[86:89], v[70:73], v[220:223], v[86:89]
	v_mfma_i32_16x16x64_i8 v[78:81], v[160:163], v[220:223], v[78:81]
	v_mfma_i32_16x16x64_i8 v[134:137], v[156:159], v[200:203], v[134:137]
	v_mfma_i32_16x16x64_i8 v[126:129], v[172:175], v[200:203], v[126:129]
	v_mfma_i32_16x16x64_i8 v[118:121], v[156:159], v[208:211], v[118:121]
	v_mfma_i32_16x16x64_i8 v[110:113], v[172:175], v[208:211], v[110:113]
	v_mfma_i32_16x16x64_i8 v[102:105], v[156:159], v[216:219], v[102:105]
	v_mfma_i32_16x16x64_i8 v[94:97], v[172:175], v[216:219], v[94:97]
	v_mfma_i32_16x16x64_i8 v[86:89], v[156:159], v[224:227], v[86:89]
	v_mfma_i32_16x16x64_i8 v[78:81], v[172:175], v[224:227], v[78:81]
	v_mfma_i32_16x16x64_i8 v[130:133], v[176:179], v[196:199], v[130:133]
	v_mfma_i32_16x16x64_i8 v[122:125], v[184:187], v[196:199], v[122:125]
	v_mfma_i32_16x16x64_i8 v[114:117], v[176:179], v[204:207], v[114:117]
	v_mfma_i32_16x16x64_i8 v[106:109], v[184:187], v[204:207], v[106:109]
	v_mfma_i32_16x16x64_i8 v[98:101], v[176:179], v[212:215], v[98:101]
	v_mfma_i32_16x16x64_i8 v[90:93], v[184:187], v[212:215], v[90:93]
	v_mfma_i32_16x16x64_i8 v[82:85], v[176:179], v[220:223], v[82:85]
	v_mfma_i32_16x16x64_i8 v[74:77], v[184:187], v[220:223], v[74:77]
	v_mfma_i32_16x16x64_i8 v[130:133], v[180:183], v[200:203], v[130:133]
	v_mfma_i32_16x16x64_i8 v[122:125], v[188:191], v[200:203], v[122:125]
	v_mfma_i32_16x16x64_i8 v[114:117], v[180:183], v[208:211], v[114:117]
	v_mfma_i32_16x16x64_i8 v[106:109], v[188:191], v[208:211], v[106:109]
	v_mfma_i32_16x16x64_i8 v[98:101], v[180:183], v[216:219], v[98:101]
	v_mfma_i32_16x16x64_i8 v[90:93], v[188:191], v[216:219], v[90:93]
	v_mfma_i32_16x16x64_i8 v[82:85], v[180:183], v[224:227], v[82:85]
	v_mfma_i32_16x16x64_i8 v[74:77], v[188:191], v[224:227], v[74:77]
	s_barrier
	s_add_i32 s28, s49, s38
	v_lshl_add_u64 v[192:193], s[34:35], 0, v[140:141]
	s_mov_b32 m0, s28
	ds_read_b128 v[196:199], v169 offset:16384
	ds_read_b128 v[200:203], v169 offset:17408
	ds_read_b128 v[204:207], v169 offset:18432
	ds_read_b128 v[208:211], v169 offset:19456
	ds_read_b128 v[212:215], v169 offset:20480
	ds_read_b128 v[216:219], v169 offset:21504
	ds_read_b128 v[220:223], v169 offset:22528
	ds_read_b128 v[224:227], v169 offset:23552
	global_load_lds_dwordx4 v[192:193], off
	s_add_i32 m0, s28, 0x2000
	s_add_u32 s28, s34, 0x40000
	v_lshl_add_u64 v[228:229], s[34:35], 0, v[138:139]
	s_addc_u32 s29, s35, 0
	s_add_i32 s63, s52, s38
	global_load_lds_dwordx4 v[228:229], off
	v_lshl_add_u64 v[230:231], s[28:29], 0, v[140:141]
	s_mov_b32 m0, s63
	s_nop 0
	global_load_lds_dwordx4 v[230:231], off
	v_lshl_add_u64 v[230:231], s[28:29], 0, v[138:139]
	s_add_i32 m0, s63, 0x2000
	s_and_b64 s[28:29], s[6:7], s[36:37]
	s_and_b64 s[28:29], s[28:29], exec
	s_cselect_b32 s28, s20, s26
	s_cselect_b32 s29, s21, s27
	s_add_u32 s28, s28, s67
	s_addc_u32 s29, s29, 0
	global_load_lds_dwordx4 v[230:231], off
	v_lshl_add_u64 v[230:231], s[28:29], 0, v[142:143]
	s_mov_b32 m0, s25
	v_lshl_add_u64 v[232:233], s[28:29], 0, v[144:145]
	global_load_lds_dwordx4 v[230:231], off
	s_mov_b32 m0, s41
	s_nop 0
	global_load_lds_dwordx4 v[232:233], off
	s_waitcnt vmcnt(8)
	s_waitcnt lgkmcnt(0)
	s_barrier
; #define PG8_STAGE(bufoff, gbase, voff) do { _Pragma("unroll") for (int _i = 0; _i < 2; ++_i) \
;         __builtin_amdgcn_global_load_lds((const unsigned*)((const char*)(gbase) + (voff)[_i]), (LAS unsigned*)(lds + (bufoff) + ldsw + _i * 8192), 16, 0, 0); } while (0)
; #define PG8_LDA(dst, b, h) do { _Pragma("unroll") for (int m = 0; m < 4; ++m) dst[m] = PG8_LD32(lds + PG8_SA(b, h) + aoff + m * 2048); } while (0)
; #define PG8_LDB(dst, b, h) do { _Pragma("unroll") for (int n = 0; n < 2; ++n) dst[n] = PG8_LD32(lds + PG8_SB(b, h) + boff + n * 2048); } while (0)
; #define PG8_WAIT_V(n) asm volatile("s_waitcnt vmcnt(" #n ")" ::: "memory")
; #define PG8_WAIT_L(n) asm volatile("s_waitcnt lgkmcnt(" #n ")" ::: "memory")
; #define PG8_BAR __builtin_amdgcn_s_barrier()
; #define PG8_SCHED __builtin_amdgcn_sched_barrier(0)
; template <class Epi, class Sched, bool ALIGN_EPI, int DT>
; __device__ __forceinline__ void gemm_phase(LAS unsigned char* lds, const int KB, const Sched& S, const Epi& E) {
;     ...
;             const size_t k1 = (size_t)(t + 1) * kstep, k2 = last ? 0 : (size_t)(t + 2) * kstep, k3 = k2 + kstep;
;             const char* b2 = last ? nB : cB + (size_t)(t + 2) * kstep; const char* b3 = b2 + kstep;
;             PG8_LDB(B0, 0, 0); PG8_LDB(B1, 0, 1); PG8_SCHED; PG8_LDA(At, 0, 0); PG8_STA(PG8_SA(1, 1), false, 1, k1);
;             PG8_WAIT_V(8); PG8_WAIT_L(0); PG8_BAR; PG8_MMA(0, 0, At, B0); PG8_MMA(0, 1, At, B1); PG8_BAR; PG8_SCHED;
;             PG8_LDA(At, 0, 1); PG8_STAGE(PG8_SB(0, 0), b2, voffB); PG8_STAGE(PG8_SB(0, 1), b2 + hstep, voffB); PG8_STA(PG8_SA(0, 0), last, 0, k2);
;             PG8_WAIT_V(8); PG8_WAIT_L(0); PG8_BAR; PG8_MMA(1, 0, At, B0); PG8_MMA(1, 1, At, B1); PG8_BAR; PG8_SCHED;
;             PG8_LDB(B0, 1, 0); PG8_LDB(B1, 1, 1); PG8_SCHED; PG8_LDA(At, 1, 0); PG8_STA(PG8_SA(0, 1), last, 1, k2);
;             PG8_WAIT_V(8); PG8_WAIT_L(0); PG8_BAR; PG8_MMA(0, 0, At, B0); PG8_MMA(0, 1, At, B1); PG8_BAR; PG8_SCHED;
;             PG8_LDA(At, 1, 1); PG8_STAGE(PG8_SB(1, 0), b3, voffB); PG8_STAGE(PG8_SB(1, 1), b3 + hstep, voffB); PG8_STA(PG8_SA(1, 0), last, 0, k3);
;             PG8_WAIT_V(8); PG8_WAIT_L(0); PG8_BAR; PG8_MMA(1, 0, At, B0); PG8_MMA(1, 1, At, B1); PG8_BAR; PG8_SCHED;
;         }
	s_waitcnt lgkmcnt(0)
	v_mfma_i32_16x16x64_i8 v[62:65], v[70:73], v[196:199], v[62:65]
	v_mfma_i32_16x16x64_i8 v[54:57], v[160:163], v[196:199], v[54:57]
	v_mfma_i32_16x16x64_i8 v[46:49], v[70:73], v[204:207], v[46:49]
	v_mfma_i32_16x16x64_i8 v[38:41], v[160:163], v[204:207], v[38:41]
	v_mfma_i32_16x16x64_i8 v[30:33], v[70:73], v[212:215], v[30:33]
	v_mfma_i32_16x16x64_i8 v[22:25], v[160:163], v[212:215], v[22:25]
	v_mfma_i32_16x16x64_i8 v[6:9], v[70:73], v[220:223], v[6:9]
	v_mfma_i32_16x16x64_i8 v[2:5], v[160:163], v[220:223], v[2:5]
	v_mfma_i32_16x16x64_i8 v[62:65], v[156:159], v[200:203], v[62:65]
	v_mfma_i32_16x16x64_i8 v[54:57], v[172:175], v[200:203], v[54:57]
	v_mfma_i32_16x16x64_i8 v[46:49], v[156:159], v[208:211], v[46:49]
	v_mfma_i32_16x16x64_i8 v[38:41], v[172:175], v[208:211], v[38:41]
	v_mfma_i32_16x16x64_i8 v[30:33], v[156:159], v[216:219], v[30:33]
	v_mfma_i32_16x16x64_i8 v[22:25], v[172:175], v[216:219], v[22:25]
	v_mfma_i32_16x16x64_i8 v[6:9], v[156:159], v[224:227], v[6:9]
	v_mfma_i32_16x16x64_i8 v[2:5], v[172:175], v[224:227], v[2:5]
	v_mfma_i32_16x16x64_i8 v[58:61], v[176:179], v[196:199], v[58:61]
	v_mfma_i32_16x16x64_i8 v[50:53], v[184:187], v[196:199], v[50:53]
	v_mfma_i32_16x16x64_i8 v[42:45], v[176:179], v[204:207], v[42:45]
	v_mfma_i32_16x16x64_i8 v[34:37], v[184:187], v[204:207], v[34:37]
	v_mfma_i32_16x16x64_i8 v[26:29], v[176:179], v[212:215], v[26:29]
	v_mfma_i32_16x16x64_i8 v[18:21], v[184:187], v[212:215], v[18:21]
	v_mfma_i32_16x16x64_i8 v[14:17], v[176:179], v[220:223], v[14:17]
	v_mfma_i32_16x16x64_i8 v[10:13], v[184:187], v[220:223], v[10:13]
	v_mfma_i32_16x16x64_i8 v[58:61], v[180:183], v[200:203], v[58:61]
	v_mfma_i32_16x16x64_i8 v[50:53], v[188:191], v[200:203], v[50:53]
	v_mfma_i32_16x16x64_i8 v[42:45], v[180:183], v[208:211], v[42:45]
	v_mfma_i32_16x16x64_i8 v[34:37], v[188:191], v[208:211], v[34:37]
	v_mfma_i32_16x16x64_i8 v[26:29], v[180:183], v[216:219], v[26:29]
	v_mfma_i32_16x16x64_i8 v[18:21], v[188:191], v[216:219], v[18:21]
	v_mfma_i32_16x16x64_i8 v[14:17], v[180:183], v[224:227], v[14:17]
	v_mfma_i32_16x16x64_i8 v[10:13], v[188:191], v[224:227], v[10:13]
	s_barrier
	s_add_i32 s36, 0, 0x18000
	v_add_u32_e32 v1, s36, v165
	s_add_i32 s37, 0, 0x1c000
	ds_read_b128 v[70:73], v1
	ds_read_b128 v[156:159], v1 offset:1024
	ds_read_b128 v[160:163], v1 offset:2048
	ds_read_b128 v[172:175], v1 offset:3072
	v_add_u32_e32 v1, s37, v165
	ds_read_b128 v[176:179], v1
	ds_read_b128 v[180:183], v1 offset:1024
	ds_read_b128 v[184:187], v1 offset:2048
	ds_read_b128 v[188:191], v1 offset:3072
	s_add_u32 s28, s28, 0x40000
	s_addc_u32 s29, s29, 0
	s_mov_b32 m0, s42
	v_lshl_add_u64 v[234:235], s[28:29], 0, v[142:143]
	ds_read_b128 v[196:199], v169 offset:32768
	ds_read_b128 v[200:203], v169 offset:33792
	ds_read_b128 v[204:207], v169 offset:34816
	ds_read_b128 v[208:211], v169 offset:35840
	ds_read_b128 v[212:215], v169 offset:36864
	ds_read_b128 v[216:219], v169 offset:37888
	ds_read_b128 v[220:223], v169 offset:38912
	ds_read_b128 v[224:227], v169 offset:39936
	global_load_lds_dwordx4 v[234:235], off
	v_lshl_add_u64 v[234:235], s[28:29], 0, v[144:145]
	s_mov_b32 m0, s43
	s_nop 0
	global_load_lds_dwordx4 v[234:235], off
	s_waitcnt vmcnt(8)
	s_waitcnt lgkmcnt(0)
	s_barrier
	s_waitcnt lgkmcnt(0)
	v_mfma_i32_16x16x64_i8 v[134:137], v[70:73], v[196:199], v[134:137]
	v_mfma_i32_16x16x64_i8 v[126:129], v[160:163], v[196:199], v[126:129]
	v_mfma_i32_16x16x64_i8 v[118:121], v[70:73], v[204:207], v[118:121]
	v_mfma_i32_16x16x64_i8 v[110:113], v[160:163], v[204:207], v[110:113]
	v_mfma_i32_16x16x64_i8 v[102:105], v[70:73], v[212:215], v[102:105]
	v_mfma_i32_16x16x64_i8 v[94:97], v[160:163], v[212:215], v[94:97]
	v_mfma_i32_16x16x64_i8 v[86:89], v[70:73], v[220:223], v[86:89]
	v_mfma_i32_16x16x64_i8 v[78:81], v[160:163], v[220:223], v[78:81]
	v_mfma_i32_16x16x64_i8 v[134:137], v[156:159], v[200:203], v[134:137]
	v_mfma_i32_16x16x64_i8 v[126:129], v[172:175], v[200:203], v[126:129]
	v_mfma_i32_16x16x64_i8 v[118:121], v[156:159], v[208:211], v[118:121]
	v_mfma_i32_16x16x64_i8 v[110:113], v[172:175], v[208:211], v[110:113]
	v_mfma_i32_16x16x64_i8 v[102:105], v[156:159], v[216:219], v[102:105]
	v_mfma_i32_16x16x64_i8 v[94:97], v[172:175], v[216:219], v[94:97]
	v_mfma_i32_16x16x64_i8 v[86:89], v[156:159], v[224:227], v[86:89]
	v_mfma_i32_16x16x64_i8 v[78:81], v[172:175], v[224:227], v[78:81]
	v_mfma_i32_16x16x64_i8 v[130:133], v[176:179], v[196:199], v[130:133]
	v_mfma_i32_16x16x64_i8 v[122:125], v[184:187], v[196:199], v[122:125]
	v_mfma_i32_16x16x64_i8 v[114:117], v[176:179], v[204:207], v[114:117]
	v_mfma_i32_16x16x64_i8 v[106:109], v[184:187], v[204:207], v[106:109]
	v_mfma_i32_16x16x64_i8 v[98:101], v[176:179], v[212:215], v[98:101]
	v_mfma_i32_16x16x64_i8 v[90:93], v[184:187], v[212:215], v[90:93]
	v_mfma_i32_16x16x64_i8 v[82:85], v[176:179], v[220:223], v[82:85]
	v_mfma_i32_16x16x64_i8 v[74:77], v[184:187], v[220:223], v[74:77]
	v_mfma_i32_16x16x64_i8 v[130:133], v[180:183], v[200:203], v[130:133]
	v_mfma_i32_16x16x64_i8 v[122:125], v[188:191], v[200:203], v[122:125]
	v_mfma_i32_16x16x64_i8 v[114:117], v[180:183], v[208:211], v[114:117]
	v_mfma_i32_16x16x64_i8 v[106:109], v[188:191], v[208:211], v[106:109]
	v_mfma_i32_16x16x64_i8 v[98:101], v[180:183], v[216:219], v[98:101]
	v_mfma_i32_16x16x64_i8 v[90:93], v[188:191], v[216:219], v[90:93]
	v_mfma_i32_16x16x64_i8 v[82:85], v[180:183], v[224:227], v[82:85]
	v_mfma_i32_16x16x64_i8 v[74:77], v[188:191], v[224:227], v[74:77]
	s_barrier
; #define PG8_STAGE(bufoff, gbase, voff) do { _Pragma("unroll") for (int _i = 0; _i < 2; ++_i) \
;         __builtin_amdgcn_global_load_lds((const unsigned*)((const char*)(gbase) + (voff)[_i]), (LAS unsigned*)(lds + (bufoff) + ldsw + _i * 8192), 16, 0, 0); } while (0)
; #define PG8_LDA(dst, b, h) do { _Pragma("unroll") for (int m = 0; m < 4; ++m) dst[m] = PG8_LD32(lds + PG8_SA(b, h) + aoff + m * 2048); } while (0)
; #define PG8_LDB(dst, b, h) do { _Pragma("unroll") for (int n = 0; n < 2; ++n) dst[n] = PG8_LD32(lds + PG8_SB(b, h) + boff + n * 2048); } while (0)
; #define PG8_WAIT_V(n) asm volatile("s_waitcnt vmcnt(" #n ")" ::: "memory")
; #define PG8_WAIT_L(n) asm volatile("s_waitcnt lgkmcnt(" #n ")" ::: "memory")
; #define PG8_BAR __builtin_amdgcn_s_barrier()
; #define PG8_SCHED __builtin_amdgcn_sched_barrier(0)
; template <class Epi, class Sched, bool ALIGN_EPI, int DT>
; __device__ __forceinline__ void gemm_phase(LAS unsigned char* lds, const int KB, const Sched& S, const Epi& E) {
;     ...
;             const size_t k1 = (size_t)(t + 1) * kstep, k2 = last ? 0 : (size_t)(t + 2) * kstep, k3 = k2 + kstep;
;             const char* b2 = last ? nB : cB + (size_t)(t + 2) * kstep; const char* b3 = b2 + kstep;
;             PG8_LDB(B0, 0, 0); PG8_LDB(B1, 0, 1); PG8_SCHED; PG8_LDA(At, 0, 0); PG8_STA(PG8_SA(1, 1), false, 1, k1);
;             PG8_WAIT_V(8); PG8_WAIT_L(0); PG8_BAR; PG8_MMA(0, 0, At, B0); PG8_MMA(0, 1, At, B1); PG8_BAR; PG8_SCHED;
;             PG8_LDA(At, 0, 1); PG8_STAGE(PG8_SB(0, 0), b2, voffB); PG8_STAGE(PG8_SB(0, 1), b2 + hstep, voffB); PG8_STA(PG8_SA(0, 0), last, 0, k2);
;             PG8_WAIT_V(8); PG8_WAIT_L(0); PG8_BAR; PG8_MMA(1, 0, At, B0); PG8_MMA(1, 1, At, B1); PG8_BAR; PG8_SCHED;
;             PG8_LDB(B0, 1, 0); PG8_LDB(B1, 1, 1); PG8_SCHED; PG8_LDA(At, 1, 0); PG8_STA(PG8_SA(0, 1), last, 1, k2);
;             PG8_WAIT_V(8); PG8_WAIT_L(0); PG8_BAR; PG8_MMA(0, 0, At, B0); PG8_MMA(0, 1, At, B1); PG8_BAR; PG8_SCHED;
;             PG8_LDA(At, 1, 1); PG8_STAGE(PG8_SB(1, 0), b3, voffB); PG8_STAGE(PG8_SB(1, 1), b3 + hstep, voffB); PG8_STA(PG8_SA(1, 0), last, 0, k3);
;             PG8_WAIT_V(8); PG8_WAIT_L(0); PG8_BAR; PG8_MMA(1, 0, At, B0); PG8_MMA(1, 1, At, B1); PG8_BAR; PG8_SCHED;
;         }
	s_add_i32 s28, s36, s38
	v_lshl_add_u64 v[192:193], v[192:193], 0, s[12:13]
	s_mov_b32 m0, s28
	ds_read_b128 v[196:199], v169 offset:49152
	ds_read_b128 v[200:203], v169 offset:50176
	ds_read_b128 v[204:207], v169 offset:51200
	ds_read_b128 v[208:211], v169 offset:52224
	ds_read_b128 v[212:215], v169 offset:53248
	ds_read_b128 v[216:219], v169 offset:54272
	ds_read_b128 v[220:223], v169 offset:55296
	ds_read_b128 v[224:227], v169 offset:56320
	global_load_lds_dwordx4 v[192:193], off
	s_add_i32 m0, s28, 0x2000
	s_add_u32 s28, s34, 0x40080
	v_lshl_add_u64 v[192:193], v[228:229], 0, s[12:13]
	s_addc_u32 s29, s35, 0
	s_add_i32 s34, s37, s38
	global_load_lds_dwordx4 v[192:193], off
	v_lshl_add_u64 v[192:193], s[28:29], 0, v[140:141]
	s_mov_b32 m0, s34
	s_nop 0
	global_load_lds_dwordx4 v[192:193], off
	v_lshl_add_u64 v[192:193], s[28:29], 0, v[138:139]
	s_add_i32 m0, s34, 0x2000
	s_nop 0
	global_load_lds_dwordx4 v[192:193], off
	v_lshl_add_u64 v[192:193], v[230:231], 0, s[12:13]
	s_mov_b32 m0, s45
	s_nop 0
	global_load_lds_dwordx4 v[192:193], off
	v_lshl_add_u64 v[192:193], v[232:233], 0, s[12:13]
	s_mov_b32 m0, s46
	s_nop 0
	global_load_lds_dwordx4 v[192:193], off
	s_waitcnt vmcnt(8)
	s_waitcnt lgkmcnt(0)
	s_barrier
	s_waitcnt lgkmcnt(0)
	v_mfma_i32_16x16x64_i8 v[62:65], v[70:73], v[196:199], v[62:65]
	v_mfma_i32_16x16x64_i8 v[54:57], v[160:163], v[196:199], v[54:57]
	v_mfma_i32_16x16x64_i8 v[46:49], v[70:73], v[204:207], v[46:49]
	v_mfma_i32_16x16x64_i8 v[38:41], v[160:163], v[204:207], v[38:41]
	v_mfma_i32_16x16x64_i8 v[30:33], v[70:73], v[212:215], v[30:33]
	v_mfma_i32_16x16x64_i8 v[22:25], v[160:163], v[212:215], v[22:25]
	v_mfma_i32_16x16x64_i8 v[6:9], v[70:73], v[220:223], v[6:9]
	v_mfma_i32_16x16x64_i8 v[2:5], v[160:163], v[220:223], v[2:5]
	v_mfma_i32_16x16x64_i8 v[62:65], v[156:159], v[200:203], v[62:65]
	v_mfma_i32_16x16x64_i8 v[54:57], v[172:175], v[200:203], v[54:57]
	v_mfma_i32_16x16x64_i8 v[46:49], v[156:159], v[208:211], v[46:49]
	v_mfma_i32_16x16x64_i8 v[38:41], v[172:175], v[208:211], v[38:41]
	v_mfma_i32_16x16x64_i8 v[30:33], v[156:159], v[216:219], v[30:33]
	v_mfma_i32_16x16x64_i8 v[22:25], v[172:175], v[216:219], v[22:25]
	v_mfma_i32_16x16x64_i8 v[6:9], v[156:159], v[224:227], v[6:9]
	v_mfma_i32_16x16x64_i8 v[2:5], v[172:175], v[224:227], v[2:5]
	v_mfma_i32_16x16x64_i8 v[58:61], v[176:179], v[196:199], v[58:61]
	v_mfma_i32_16x16x64_i8 v[50:53], v[184:187], v[196:199], v[50:53]
	v_mfma_i32_16x16x64_i8 v[42:45], v[176:179], v[204:207], v[42:45]
	v_mfma_i32_16x16x64_i8 v[34:37], v[184:187], v[204:207], v[34:37]
	v_mfma_i32_16x16x64_i8 v[26:29], v[176:179], v[212:215], v[26:29]
	v_mfma_i32_16x16x64_i8 v[18:21], v[184:187], v[212:215], v[18:21]
	v_mfma_i32_16x16x64_i8 v[14:17], v[176:179], v[220:223], v[14:17]
	v_mfma_i32_16x16x64_i8 v[10:13], v[184:187], v[220:223], v[10:13]
	v_mfma_i32_16x16x64_i8 v[58:61], v[180:183], v[200:203], v[58:61]
	v_mfma_i32_16x16x64_i8 v[50:53], v[188:191], v[200:203], v[50:53]
	v_mfma_i32_16x16x64_i8 v[42:45], v[180:183], v[208:211], v[42:45]
	v_mfma_i32_16x16x64_i8 v[34:37], v[188:191], v[208:211], v[34:37]
	v_mfma_i32_16x16x64_i8 v[26:29], v[180:183], v[216:219], v[26:29]
	v_mfma_i32_16x16x64_i8 v[18:21], v[188:191], v[216:219], v[18:21]
	v_mfma_i32_16x16x64_i8 v[14:17], v[180:183], v[224:227], v[14:17]
	v_mfma_i32_16x16x64_i8 v[10:13], v[188:191], v[224:227], v[10:13]
	s_barrier
	s_add_i32 s62, s62, 2
	s_cmp_gt_u32 s62, 13
	s_mov_b64 s[28:29], s[30:31]
	s_cbranch_scc0 .LBB0_1154
	s_and_b64 vcc, exec, s[14:15]
	s_cbranch_vccz .LBB0_1157
	s_barrier

; #define PG8_STAGE(bufoff, gbase, voff) do { _Pragma("unroll") for (int _i = 0; _i < 2; ++_i) \
;         __builtin_amdgcn_global_load_lds((const unsigned*)((const char*)(gbase) + (voff)[_i]), (LAS unsigned*)(lds + (bufoff) + ldsw + _i * 8192), 16, 0, 0); } while (0)
; #define PG8_LDA(dst, b, h) do { _Pragma("unroll") for (int m = 0; m < 4; ++m) dst[m] = PG8_LD32(lds + PG8_SA(b, h) + aoff + m * 2048); } while (0)
; #define PG8_LDB(dst, b, h) do { _Pragma("unroll") for (int n = 0; n < 2; ++n) dst[n] = PG8_LD32(lds + PG8_SB(b, h) + boff + n * 2048); } while (0)
; #define PG8_WAIT_V(n) asm volatile("s_waitcnt vmcnt(" #n ")" ::: "memory")
; #define PG8_WAIT_L(n) asm volatile("s_waitcnt lgkmcnt(" #n ")" ::: "memory")
; #define PG8_BAR __builtin_amdgcn_s_barrier()
; #define PG8_SCHED __builtin_amdgcn_sched_barrier(0)
; template <class Epi, class Sched, bool ALIGN_EPI, int DT>
; __device__ __forceinline__ void gemm_phase(LAS unsigned char* lds, const int KB, const Sched& S, const Epi& E) {
;     ...
;             const size_t k1 = (size_t)(t + 1) * kstep, k2 = last ? 0 : (size_t)(t + 2) * kstep, k3 = k2 + kstep;
;             const char* b2 = last ? nB : cB + (size_t)(t + 2) * kstep; const char* b3 = b2 + kstep;
;             PG8_LDB(B0, 0, 0); PG8_LDB(B1, 0, 1); PG8_SCHED; PG8_LDA(At, 0, 0); PG8_STA(PG8_SA(1, 1), false, 1, k1);
;             PG8_WAIT_V(8); PG8_WAIT_L(0); PG8_BAR; PG8_MMA(0, 0, At, B0); PG8_MMA(0, 1, At, B1); PG8_BAR; PG8_SCHED;
;             PG8_LDA(At, 0, 1); PG8_STAGE(PG8_SB(0, 0), b2, voffB); PG8_STAGE(PG8_SB(0, 1), b2 + hstep, voffB); PG8_STA(PG8_SA(0, 0), last, 0, k2);
;             PG8_WAIT_V(8); PG8_WAIT_L(0); PG8_BAR; PG8_MMA(1, 0, At, B0); PG8_MMA(1, 1, At, B1); PG8_BAR; PG8_SCHED;
;             PG8_LDB(B0, 1, 0); PG8_LDB(B1, 1, 1); PG8_SCHED; PG8_LDA(At, 1, 0); PG8_STA(PG8_SA(0, 1), last, 1, k2);
;             PG8_WAIT_V(8); PG8_WAIT_L(0); PG8_BAR; PG8_MMA(0, 0, At, B0); PG8_MMA(0, 1, At, B1); PG8_BAR; PG8_SCHED;
;             PG8_LDA(At, 1, 1); PG8_STAGE(PG8_SB(1, 0), b3, voffB); PG8_STAGE(PG8_SB(1, 1), b3 + hstep, voffB); PG8_STA(PG8_SA(1, 0), last, 0, k3);
;             PG8_WAIT_V(8); PG8_WAIT_L(0); PG8_BAR; PG8_MMA(1, 0, At, B0); PG8_MMA(1, 1, At, B1); PG8_BAR; PG8_SCHED;
;         }
.LBB0_1237:
	ds_read_b128 v[18:21], v193
	ds_read_b128 v[22:25], v193 offset:1024
	ds_read_b128 v[26:29], v193 offset:2048
	ds_read_b128 v[30:33], v193 offset:3072
	ds_read_b128 v[2:5], v195
	ds_read_b128 v[6:9], v195 offset:1024
	ds_read_b128 v[10:13], v195 offset:2048
	ds_read_b128 v[14:17], v195 offset:3072
	s_add_u32 s26, s30, 0x100
	s_addc_u32 s27, s31, 0
	s_add_u32 s28, s56, s30
	s_addc_u32 s29, s57, s31
	s_add_i32 s68, s43, s34
	s_add_i32 m0, s35, 0xc000
	s_add_i32 s69, s35, 0xe000
	s_add_i32 s63, s68, 0x2000
	s_cmp_eq_u32 s62, 40
	s_cselect_b32 s29, s23, s29
	s_cselect_b32 s28, s22, s28
	s_cselect_b32 s66, 0, s27
	s_cselect_b32 s67, 0, s26
	v_lshl_add_u64 v[222:223], v[178:179], 0, s[30:31]
	ds_read_b128 v[182:185], v196
	ds_read_b128 v[186:189], v196 offset:1024
	ds_read_b128 v[198:201], v196 offset:2048
	ds_read_b128 v[202:205], v196 offset:3072
	ds_read_b128 v[206:209], v196 offset:4096
	ds_read_b128 v[210:213], v196 offset:5120
	ds_read_b128 v[214:217], v196 offset:6144
	ds_read_b128 v[218:221], v196 offset:7168
	global_load_lds_dwordx4 v[222:223], off
	v_lshl_add_u64 v[222:223], v[180:181], 0, s[30:31]
	s_mov_b32 m0, s69
	s_nop 0
	global_load_lds_dwordx4 v[222:223], off
	s_waitcnt vmcnt(8)
	s_waitcnt lgkmcnt(0)
	s_barrier
	s_waitcnt lgkmcnt(0)
	v_mfma_scale_f32_16x16x128_f8f6f4 v[158:161], v[18:25], v[182:189], v[158:161], v190, v190 op_sel_hi:[0,0,0]
	v_mfma_scale_f32_16x16x128_f8f6f4 v[154:157], v[26:33], v[182:189], v[154:157], v190, v190 op_sel_hi:[0,0,0]
	v_mfma_scale_f32_16x16x128_f8f6f4 v[150:153], v[18:25], v[198:205], v[150:153], v190, v190 op_sel_hi:[0,0,0]
	v_mfma_scale_f32_16x16x128_f8f6f4 v[142:145], v[26:33], v[198:205], v[142:145], v190, v190 op_sel_hi:[0,0,0]
	v_mfma_scale_f32_16x16x128_f8f6f4 v[134:137], v[18:25], v[206:213], v[134:137], v190, v190 op_sel_hi:[0,0,0]
	v_mfma_scale_f32_16x16x128_f8f6f4 v[126:129], v[26:33], v[206:213], v[126:129], v190, v190 op_sel_hi:[0,0,0]
	v_mfma_scale_f32_16x16x128_f8f6f4 v[118:121], v[18:25], v[214:221], v[118:121], v190, v190 op_sel_hi:[0,0,0]
	v_mfma_scale_f32_16x16x128_f8f6f4 v[110:113], v[26:33], v[214:221], v[110:113], v190, v190 op_sel_hi:[0,0,0]
	v_mfma_scale_f32_16x16x128_f8f6f4 v[146:149], v[2:9], v[182:189], v[146:149], v190, v190 op_sel_hi:[0,0,0]
	v_mfma_scale_f32_16x16x128_f8f6f4 v[138:141], v[10:17], v[182:189], v[138:141], v190, v190 op_sel_hi:[0,0,0]
	v_mfma_scale_f32_16x16x128_f8f6f4 v[130:133], v[2:9], v[198:205], v[130:133], v190, v190 op_sel_hi:[0,0,0]
	v_mfma_scale_f32_16x16x128_f8f6f4 v[122:125], v[10:17], v[198:205], v[122:125], v190, v190 op_sel_hi:[0,0,0]
	v_mfma_scale_f32_16x16x128_f8f6f4 v[114:117], v[2:9], v[206:213], v[114:117], v190, v190 op_sel_hi:[0,0,0]
	v_mfma_scale_f32_16x16x128_f8f6f4 v[106:109], v[10:17], v[206:213], v[106:109], v190, v190 op_sel_hi:[0,0,0]
	v_mfma_scale_f32_16x16x128_f8f6f4 v[102:105], v[2:9], v[214:221], v[102:105], v190, v190 op_sel_hi:[0,0,0]
	v_mfma_scale_f32_16x16x128_f8f6f4 v[98:101], v[10:17], v[214:221], v[98:101], v190, v190 op_sel_hi:[0,0,0]
	s_barrier
	s_mov_b32 m0, s68
	v_lshl_add_u64 v[184:185], s[28:29], 0, v[162:163]
	ds_read_b128 v[198:201], v196 offset:16384
	ds_read_b128 v[202:205], v196 offset:17408
	ds_read_b128 v[206:209], v196 offset:18432
	ds_read_b128 v[210:213], v196 offset:19456
	ds_read_b128 v[214:217], v196 offset:20480
	ds_read_b128 v[218:221], v196 offset:21504
	ds_read_b128 v[222:225], v196 offset:22528
	ds_read_b128 v[226:229], v196 offset:23552
	global_load_lds_dwordx4 v[184:185], off
	s_mov_b32 m0, s63
	s_cselect_b32 s63, s9, s25
	s_cselect_b32 s68, s8, s24
	s_add_u32 s30, s28, 0xb0000
	v_lshl_add_u64 v[182:183], s[28:29], 0, v[164:165]
	s_addc_u32 s31, s29, 0
	s_add_i32 s69, s44, s34
	global_load_lds_dwordx4 v[182:183], off
	v_lshl_add_u64 v[186:187], s[30:31], 0, v[162:163]
	s_mov_b32 m0, s69
	s_nop 0
	global_load_lds_dwordx4 v[186:187], off
	s_add_i32 m0, s69, 0x2000
	v_lshl_add_u64 v[186:187], s[30:31], 0, v[164:165]
	s_add_u32 s30, s68, s67
	s_addc_u32 s31, s63, s66
	global_load_lds_dwordx4 v[186:187], off
	v_lshl_add_u64 v[186:187], s[30:31], 0, v[166:167]
	s_mov_b32 m0, s35
	v_lshl_add_u64 v[188:189], s[30:31], 0, v[168:169]
	global_load_lds_dwordx4 v[186:187], off
	s_mov_b32 m0, s36
	s_nop 0
	global_load_lds_dwordx4 v[188:189], off
	s_waitcnt vmcnt(8)
	s_waitcnt lgkmcnt(0)
	s_barrier
	s_waitcnt lgkmcnt(0)
	v_mfma_scale_f32_16x16x128_f8f6f4 v[94:97], v[18:25], v[198:205], v[94:97], v190, v190 op_sel_hi:[0,0,0]
	v_mfma_scale_f32_16x16x128_f8f6f4 v[90:93], v[26:33], v[198:205], v[90:93], v190, v190 op_sel_hi:[0,0,0]
	v_mfma_scale_f32_16x16x128_f8f6f4 v[86:89], v[18:25], v[206:213], v[86:89], v190, v190 op_sel_hi:[0,0,0]
	v_mfma_scale_f32_16x16x128_f8f6f4 v[78:81], v[26:33], v[206:213], v[78:81], v190, v190 op_sel_hi:[0,0,0]
	v_mfma_scale_f32_16x16x128_f8f6f4 v[62:65], v[18:25], v[214:221], v[62:65], v190, v190 op_sel_hi:[0,0,0]
	v_mfma_scale_f32_16x16x128_f8f6f4 v[54:57], v[26:33], v[214:221], v[54:57], v190, v190 op_sel_hi:[0,0,0]
	v_mfma_scale_f32_16x16x128_f8f6f4 v[46:49], v[18:25], v[222:229], v[46:49], v190, v190 op_sel_hi:[0,0,0]
	v_mfma_scale_f32_16x16x128_f8f6f4 v[38:41], v[26:33], v[222:229], v[38:41], v190, v190 op_sel_hi:[0,0,0]
	v_mfma_scale_f32_16x16x128_f8f6f4 v[82:85], v[2:9], v[198:205], v[82:85], v190, v190 op_sel_hi:[0,0,0]
	v_mfma_scale_f32_16x16x128_f8f6f4 v[74:77], v[10:17], v[198:205], v[74:77], v190, v190 op_sel_hi:[0,0,0]
	v_mfma_scale_f32_16x16x128_f8f6f4 v[58:61], v[2:9], v[206:213], v[58:61], v190, v190 op_sel_hi:[0,0,0]
	v_mfma_scale_f32_16x16x128_f8f6f4 v[50:53], v[10:17], v[206:213], v[50:53], v190, v190 op_sel_hi:[0,0,0]
	v_mfma_scale_f32_16x16x128_f8f6f4 v[42:45], v[2:9], v[214:221], v[42:45], v190, v190 op_sel_hi:[0,0,0]
	v_mfma_scale_f32_16x16x128_f8f6f4 v[34:37], v[10:17], v[214:221], v[34:37], v190, v190 op_sel_hi:[0,0,0]
	v_mfma_scale_f32_16x16x128_f8f6f4 v[70:73], v[2:9], v[222:229], v[70:73], v190, v190 op_sel_hi:[0,0,0]
	v_mfma_scale_f32_16x16x128_f8f6f4 v[66:69], v[10:17], v[222:229], v[66:69], v190, v190 op_sel_hi:[0,0,0]
	s_barrier
; #define PG8_STAGE(bufoff, gbase, voff) do { _Pragma("unroll") for (int _i = 0; _i < 2; ++_i) \
;         __builtin_amdgcn_global_load_lds((const unsigned*)((const char*)(gbase) + (voff)[_i]), (LAS unsigned*)(lds + (bufoff) + ldsw + _i * 8192), 16, 0, 0); } while (0)
; #define PG8_LDA(dst, b, h) do { _Pragma("unroll") for (int m = 0; m < 4; ++m) dst[m] = PG8_LD32(lds + PG8_SA(b, h) + aoff + m * 2048); } while (0)
; #define PG8_LDB(dst, b, h) do { _Pragma("unroll") for (int n = 0; n < 2; ++n) dst[n] = PG8_LD32(lds + PG8_SB(b, h) + boff + n * 2048); } while (0)
; #define PG8_WAIT_V(n) asm volatile("s_waitcnt vmcnt(" #n ")" ::: "memory")
; #define PG8_WAIT_L(n) asm volatile("s_waitcnt lgkmcnt(" #n ")" ::: "memory")
; #define PG8_BAR __builtin_amdgcn_s_barrier()
; #define PG8_SCHED __builtin_amdgcn_sched_barrier(0)
; template <class Epi, class Sched, bool ALIGN_EPI, int DT>
; __device__ __forceinline__ void gemm_phase(LAS unsigned char* lds, const int KB, const Sched& S, const Epi& E) {
;     ...
;             const size_t k1 = (size_t)(t + 1) * kstep, k2 = last ? 0 : (size_t)(t + 2) * kstep, k3 = k2 + kstep;
;             const char* b2 = last ? nB : cB + (size_t)(t + 2) * kstep; const char* b3 = b2 + kstep;
;             PG8_LDB(B0, 0, 0); PG8_LDB(B1, 0, 1); PG8_SCHED; PG8_LDA(At, 0, 0); PG8_STA(PG8_SA(1, 1), false, 1, k1);
;             PG8_WAIT_V(8); PG8_WAIT_L(0); PG8_BAR; PG8_MMA(0, 0, At, B0); PG8_MMA(0, 1, At, B1); PG8_BAR; PG8_SCHED;
;             PG8_LDA(At, 0, 1); PG8_STAGE(PG8_SB(0, 0), b2, voffB); PG8_STAGE(PG8_SB(0, 1), b2 + hstep, voffB); PG8_STA(PG8_SA(0, 0), last, 0, k2);
;             PG8_WAIT_V(8); PG8_WAIT_L(0); PG8_BAR; PG8_MMA(1, 0, At, B0); PG8_MMA(1, 1, At, B1); PG8_BAR; PG8_SCHED;
;             PG8_LDB(B0, 1, 0); PG8_LDB(B1, 1, 1); PG8_SCHED; PG8_LDA(At, 1, 0); PG8_STA(PG8_SA(0, 1), last, 1, k2);
;             PG8_WAIT_V(8); PG8_WAIT_L(0); PG8_BAR; PG8_MMA(0, 0, At, B0); PG8_MMA(0, 1, At, B1); PG8_BAR; PG8_SCHED;
;             PG8_LDA(At, 1, 1); PG8_STAGE(PG8_SB(1, 0), b3, voffB); PG8_STAGE(PG8_SB(1, 1), b3 + hstep, voffB); PG8_STA(PG8_SA(1, 0), last, 0, k3);
;             PG8_WAIT_V(8); PG8_WAIT_L(0); PG8_BAR; PG8_MMA(1, 0, At, B0); PG8_MMA(1, 1, At, B1); PG8_BAR; PG8_SCHED;
;         }
	s_add_i32 s63, 0, 0x18000
	s_add_i32 s66, 0, 0x1c000
	v_add_u32_e32 v14, s63, v191
	v_add_u32_e32 v30, s66, v191
	ds_read_b128 v[2:5], v14
	ds_read_b128 v[6:9], v14 offset:1024
	ds_read_b128 v[10:13], v14 offset:2048
	ds_read_b128 v[14:17], v14 offset:3072
	ds_read_b128 v[18:21], v30
	ds_read_b128 v[22:25], v30 offset:1024
	ds_read_b128 v[26:29], v30 offset:2048
	ds_read_b128 v[30:33], v30 offset:3072
	s_add_u32 s30, s30, 0xb0000
	s_addc_u32 s31, s31, 0
	s_mov_b32 m0, s37
	v_lshl_add_u64 v[230:231], s[30:31], 0, v[166:167]
	ds_read_b128 v[198:201], v196 offset:32768
	ds_read_b128 v[202:205], v196 offset:33792
	ds_read_b128 v[206:209], v196 offset:34816
	ds_read_b128 v[210:213], v196 offset:35840
	ds_read_b128 v[214:217], v196 offset:36864
	ds_read_b128 v[218:221], v196 offset:37888
	ds_read_b128 v[222:225], v196 offset:38912
	ds_read_b128 v[226:229], v196 offset:39936
	global_load_lds_dwordx4 v[230:231], off
	v_lshl_add_u64 v[230:231], s[30:31], 0, v[168:169]
	s_mov_b32 m0, s38
	s_nop 0
	global_load_lds_dwordx4 v[230:231], off
	s_waitcnt vmcnt(8)
	s_waitcnt lgkmcnt(0)
	s_barrier
	s_waitcnt lgkmcnt(0)
	v_mfma_scale_f32_16x16x128_f8f6f4 v[158:161], v[2:9], v[198:205], v[158:161], v190, v190 op_sel_hi:[0,0,0]
	v_mfma_scale_f32_16x16x128_f8f6f4 v[154:157], v[10:17], v[198:205], v[154:157], v190, v190 op_sel_hi:[0,0,0]
	v_mfma_scale_f32_16x16x128_f8f6f4 v[150:153], v[2:9], v[206:213], v[150:153], v190, v190 op_sel_hi:[0,0,0]
	v_mfma_scale_f32_16x16x128_f8f6f4 v[142:145], v[10:17], v[206:213], v[142:145], v190, v190 op_sel_hi:[0,0,0]
	v_mfma_scale_f32_16x16x128_f8f6f4 v[134:137], v[2:9], v[214:221], v[134:137], v190, v190 op_sel_hi:[0,0,0]
	v_mfma_scale_f32_16x16x128_f8f6f4 v[126:129], v[10:17], v[214:221], v[126:129], v190, v190 op_sel_hi:[0,0,0]
	v_mfma_scale_f32_16x16x128_f8f6f4 v[118:121], v[2:9], v[222:229], v[118:121], v190, v190 op_sel_hi:[0,0,0]
	v_mfma_scale_f32_16x16x128_f8f6f4 v[110:113], v[10:17], v[222:229], v[110:113], v190, v190 op_sel_hi:[0,0,0]
	v_mfma_scale_f32_16x16x128_f8f6f4 v[146:149], v[18:25], v[198:205], v[146:149], v190, v190 op_sel_hi:[0,0,0]
	v_mfma_scale_f32_16x16x128_f8f6f4 v[138:141], v[26:33], v[198:205], v[138:141], v190, v190 op_sel_hi:[0,0,0]
	v_mfma_scale_f32_16x16x128_f8f6f4 v[130:133], v[18:25], v[206:213], v[130:133], v190, v190 op_sel_hi:[0,0,0]
	v_mfma_scale_f32_16x16x128_f8f6f4 v[122:125], v[26:33], v[206:213], v[122:125], v190, v190 op_sel_hi:[0,0,0]
	v_mfma_scale_f32_16x16x128_f8f6f4 v[114:117], v[18:25], v[214:221], v[114:117], v190, v190 op_sel_hi:[0,0,0]
	v_mfma_scale_f32_16x16x128_f8f6f4 v[106:109], v[26:33], v[214:221], v[106:109], v190, v190 op_sel_hi:[0,0,0]
	v_mfma_scale_f32_16x16x128_f8f6f4 v[102:105], v[18:25], v[222:229], v[102:105], v190, v190 op_sel_hi:[0,0,0]
	v_mfma_scale_f32_16x16x128_f8f6f4 v[98:101], v[26:33], v[222:229], v[98:101], v190, v190 op_sel_hi:[0,0,0]
	s_barrier
	s_add_i32 s30, s63, s34
	v_lshl_add_u64 v[184:185], v[184:185], 0, s[12:13]
	s_mov_b32 m0, s30
	ds_read_b128 v[198:201], v196 offset:49152
	ds_read_b128 v[202:205], v196 offset:50176
	ds_read_b128 v[206:209], v196 offset:51200
	ds_read_b128 v[210:213], v196 offset:52224
	ds_read_b128 v[214:217], v196 offset:53248
	ds_read_b128 v[218:221], v196 offset:54272
	ds_read_b128 v[222:225], v196 offset:55296
	ds_read_b128 v[226:229], v196 offset:56320
	global_load_lds_dwordx4 v[184:185], off
	s_add_i32 m0, s30, 0x2000
	s_add_u32 s28, s28, 0xb0080
	v_lshl_add_u64 v[182:183], v[182:183], 0, s[12:13]
	s_addc_u32 s29, s29, 0
	s_add_i32 s30, s66, s34
	global_load_lds_dwordx4 v[182:183], off
	v_lshl_add_u64 v[182:183], s[28:29], 0, v[162:163]
	s_mov_b32 m0, s30
	s_nop 0
	global_load_lds_dwordx4 v[182:183], off
	v_lshl_add_u64 v[182:183], s[28:29], 0, v[164:165]
	s_add_i32 m0, s30, 0x2000
	s_nop 0
	global_load_lds_dwordx4 v[182:183], off
	v_lshl_add_u64 v[182:183], v[186:187], 0, s[12:13]
	s_mov_b32 m0, s40
	s_nop 0
	global_load_lds_dwordx4 v[182:183], off
	v_lshl_add_u64 v[182:183], v[188:189], 0, s[12:13]
	s_mov_b32 m0, s41
	s_nop 0
	global_load_lds_dwordx4 v[182:183], off
	s_waitcnt vmcnt(8)
	s_waitcnt lgkmcnt(0)
	s_barrier
	s_waitcnt lgkmcnt(0)
	v_mfma_scale_f32_16x16x128_f8f6f4 v[94:97], v[2:9], v[198:205], v[94:97], v190, v190 op_sel_hi:[0,0,0]
	v_mfma_scale_f32_16x16x128_f8f6f4 v[90:93], v[10:17], v[198:205], v[90:93], v190, v190 op_sel_hi:[0,0,0]
	v_mfma_scale_f32_16x16x128_f8f6f4 v[86:89], v[2:9], v[206:213], v[86:89], v190, v190 op_sel_hi:[0,0,0]
	v_mfma_scale_f32_16x16x128_f8f6f4 v[78:81], v[10:17], v[206:213], v[78:81], v190, v190 op_sel_hi:[0,0,0]
	v_mfma_scale_f32_16x16x128_f8f6f4 v[62:65], v[2:9], v[214:221], v[62:65], v190, v190 op_sel_hi:[0,0,0]
	v_mfma_scale_f32_16x16x128_f8f6f4 v[54:57], v[10:17], v[214:221], v[54:57], v190, v190 op_sel_hi:[0,0,0]
	v_mfma_scale_f32_16x16x128_f8f6f4 v[46:49], v[2:9], v[222:229], v[46:49], v190, v190 op_sel_hi:[0,0,0]
	v_mfma_scale_f32_16x16x128_f8f6f4 v[38:41], v[10:17], v[222:229], v[38:41], v190, v190 op_sel_hi:[0,0,0]
	v_mfma_scale_f32_16x16x128_f8f6f4 v[82:85], v[18:25], v[198:205], v[82:85], v190, v190 op_sel_hi:[0,0,0]
	v_mfma_scale_f32_16x16x128_f8f6f4 v[74:77], v[26:33], v[198:205], v[74:77], v190, v190 op_sel_hi:[0,0,0]
	v_mfma_scale_f32_16x16x128_f8f6f4 v[58:61], v[18:25], v[206:213], v[58:61], v190, v190 op_sel_hi:[0,0,0]
	v_mfma_scale_f32_16x16x128_f8f6f4 v[50:53], v[26:33], v[206:213], v[50:53], v190, v190 op_sel_hi:[0,0,0]
	v_mfma_scale_f32_16x16x128_f8f6f4 v[42:45], v[18:25], v[214:221], v[42:45], v190, v190 op_sel_hi:[0,0,0]
	v_mfma_scale_f32_16x16x128_f8f6f4 v[34:37], v[26:33], v[214:221], v[34:37], v190, v190 op_sel_hi:[0,0,0]
	v_mfma_scale_f32_16x16x128_f8f6f4 v[70:73], v[18:25], v[222:229], v[70:73], v190, v190 op_sel_hi:[0,0,0]
	v_mfma_scale_f32_16x16x128_f8f6f4 v[66:69], v[26:33], v[222:229], v[66:69], v190, v190 op_sel_hi:[0,0,0]
	s_barrier
	s_add_i32 s62, s62, 2
	s_cmp_gt_u32 s62, 41
	s_mov_b64 s[30:31], s[26:27]
	s_cbranch_scc0 .LBB0_1237
	s_and_b64 vcc, exec, s[14:15]
	s_cbranch_vccz .LBB0_1240
	s_barrier

; #define PG8_STAGE(bufoff, gbase, voff) do { _Pragma("unroll") for (int _i = 0; _i < 2; ++_i) \
;         __builtin_amdgcn_global_load_lds((const unsigned*)((const char*)(gbase) + (voff)[_i]), (LAS unsigned*)(lds + (bufoff) + ldsw + _i * 8192), 16, 0, 0); } while (0)
; #define PG8_LDA(dst, b, h) do { _Pragma("unroll") for (int m = 0; m < 4; ++m) dst[m] = PG8_LD32(lds + PG8_SA(b, h) + aoff + m * 2048); } while (0)
; #define PG8_LDB(dst, b, h) do { _Pragma("unroll") for (int n = 0; n < 2; ++n) dst[n] = PG8_LD32(lds + PG8_SB(b, h) + boff + n * 2048); } while (0)
; #define PG8_WAIT_V(n) asm volatile("s_waitcnt vmcnt(" #n ")" ::: "memory")
; #define PG8_WAIT_L(n) asm volatile("s_waitcnt lgkmcnt(" #n ")" ::: "memory")
; #define PG8_BAR __builtin_amdgcn_s_barrier()
; #define PG8_SCHED __builtin_amdgcn_sched_barrier(0)
; template <class Epi, class Sched, bool ALIGN_EPI, int DT>
; __device__ __forceinline__ void gemm_phase(LAS unsigned char* lds, const int KB, const Sched& S, const Epi& E) {
;     ...
;             const size_t k1 = (size_t)(t + 1) * kstep, k2 = last ? 0 : (size_t)(t + 2) * kstep, k3 = k2 + kstep;
;             const char* b2 = last ? nB : cB + (size_t)(t + 2) * kstep; const char* b3 = b2 + kstep;
;             PG8_LDB(B0, 0, 0); PG8_LDB(B1, 0, 1); PG8_SCHED; PG8_LDA(At, 0, 0); PG8_STA(PG8_SA(1, 1), false, 1, k1);
;             PG8_WAIT_V(8); PG8_WAIT_L(0); PG8_BAR; PG8_MMA(0, 0, At, B0); PG8_MMA(0, 1, At, B1); PG8_BAR; PG8_SCHED;
;             PG8_LDA(At, 0, 1); PG8_STAGE(PG8_SB(0, 0), b2, voffB); PG8_STAGE(PG8_SB(0, 1), b2 + hstep, voffB); PG8_STA(PG8_SA(0, 0), last, 0, k2);
;             PG8_WAIT_V(8); PG8_WAIT_L(0); PG8_BAR; PG8_MMA(1, 0, At, B0); PG8_MMA(1, 1, At, B1); PG8_BAR; PG8_SCHED;
;             PG8_LDB(B0, 1, 0); PG8_LDB(B1, 1, 1); PG8_SCHED; PG8_LDA(At, 1, 0); PG8_STA(PG8_SA(0, 1), last, 1, k2);
;             PG8_WAIT_V(8); PG8_WAIT_L(0); PG8_BAR; PG8_MMA(0, 0, At, B0); PG8_MMA(0, 1, At, B1); PG8_BAR; PG8_SCHED;
;             PG8_LDA(At, 1, 1); PG8_STAGE(PG8_SB(1, 0), b3, voffB); PG8_STAGE(PG8_SB(1, 1), b3 + hstep, voffB); PG8_STA(PG8_SA(1, 0), last, 0, k3);
;             PG8_WAIT_V(8); PG8_WAIT_L(0); PG8_BAR; PG8_MMA(1, 0, At, B0); PG8_MMA(1, 1, At, B1); PG8_BAR; PG8_SCHED;
;         }
.LBB0_1385:
	ds_read_b128 v[152:155], v174
	ds_read_b128 v[156:159], v174 offset:1024
	ds_read_b128 v[160:163], v174 offset:2048
	ds_read_b128 v[164:167], v174 offset:3072
	ds_read_b128 v[168:171], v175
	ds_read_b128 v[180:183], v175 offset:1024
	ds_read_b128 v[184:187], v175 offset:2048
	ds_read_b128 v[188:191], v175 offset:3072
	s_add_u32 s38, s36, 0x100
	s_addc_u32 s39, s37, 0
	s_add_u32 s74, s25, s36
	s_addc_u32 s75, s70, s37
	s_cmp_eq_u32 s71, 12
	s_cselect_b64 s[42:43], -1, 0
	s_and_b64 s[40:41], s[42:43], exec
	s_cselect_b32 s76, 0, s38
	s_cselect_b32 s41, s0, s75
	s_cselect_b32 s40, s23, s74
	v_lshl_add_u64 v[192:193], v[148:149], 0, s[36:37]
	s_add_i32 m0, s47, 0xc000
	ds_read_b128 v[196:199], v176
	ds_read_b128 v[200:203], v176 offset:1024
	ds_read_b128 v[204:207], v176 offset:2048
	ds_read_b128 v[208:211], v176 offset:3072
	ds_read_b128 v[212:215], v176 offset:4096
	ds_read_b128 v[216:219], v176 offset:5120
	ds_read_b128 v[220:223], v176 offset:6144
	ds_read_b128 v[224:227], v176 offset:7168
	global_load_lds_dwordx4 v[192:193], off
	v_lshl_add_u64 v[192:193], v[150:151], 0, s[36:37]
	s_add_i32 m0, s47, 0xe000
	s_nop 0
	global_load_lds_dwordx4 v[192:193], off
	s_waitcnt vmcnt(8)
	s_waitcnt lgkmcnt(0)
	s_barrier
	s_waitcnt lgkmcnt(0)
	v_mfma_i32_16x16x64_i8 v[126:129], v[152:155], v[196:199], v[126:129]
	v_mfma_i32_16x16x64_i8 v[122:125], v[160:163], v[196:199], v[122:125]
	v_mfma_i32_16x16x64_i8 v[110:113], v[152:155], v[204:207], v[110:113]
	v_mfma_i32_16x16x64_i8 v[106:109], v[160:163], v[204:207], v[106:109]
	v_mfma_i32_16x16x64_i8 v[94:97], v[152:155], v[212:215], v[94:97]
	v_mfma_i32_16x16x64_i8 v[90:93], v[160:163], v[212:215], v[90:93]
	v_mfma_i32_16x16x64_i8 v[78:81], v[152:155], v[220:223], v[78:81]
	v_mfma_i32_16x16x64_i8 v[74:77], v[160:163], v[220:223], v[74:77]
	v_mfma_i32_16x16x64_i8 v[126:129], v[156:159], v[200:203], v[126:129]
	v_mfma_i32_16x16x64_i8 v[122:125], v[164:167], v[200:203], v[122:125]
	v_mfma_i32_16x16x64_i8 v[110:113], v[156:159], v[208:211], v[110:113]
	v_mfma_i32_16x16x64_i8 v[106:109], v[164:167], v[208:211], v[106:109]
	v_mfma_i32_16x16x64_i8 v[94:97], v[156:159], v[216:219], v[94:97]
	v_mfma_i32_16x16x64_i8 v[90:93], v[164:167], v[216:219], v[90:93]
	v_mfma_i32_16x16x64_i8 v[78:81], v[156:159], v[224:227], v[78:81]
	v_mfma_i32_16x16x64_i8 v[74:77], v[164:167], v[224:227], v[74:77]
	v_mfma_i32_16x16x64_i8 v[118:121], v[168:171], v[196:199], v[118:121]
	v_mfma_i32_16x16x64_i8 v[114:117], v[184:187], v[196:199], v[114:117]
	v_mfma_i32_16x16x64_i8 v[102:105], v[168:171], v[204:207], v[102:105]
	v_mfma_i32_16x16x64_i8 v[98:101], v[184:187], v[204:207], v[98:101]
	v_mfma_i32_16x16x64_i8 v[86:89], v[168:171], v[212:215], v[86:89]
	v_mfma_i32_16x16x64_i8 v[82:85], v[184:187], v[212:215], v[82:85]
	v_mfma_i32_16x16x64_i8 v[70:73], v[168:171], v[220:223], v[70:73]
	v_mfma_i32_16x16x64_i8 v[66:69], v[184:187], v[220:223], v[66:69]
	v_mfma_i32_16x16x64_i8 v[118:121], v[180:183], v[200:203], v[118:121]
	v_mfma_i32_16x16x64_i8 v[114:117], v[188:191], v[200:203], v[114:117]
	v_mfma_i32_16x16x64_i8 v[102:105], v[180:183], v[208:211], v[102:105]
	v_mfma_i32_16x16x64_i8 v[98:101], v[188:191], v[208:211], v[98:101]
	v_mfma_i32_16x16x64_i8 v[86:89], v[180:183], v[216:219], v[86:89]
	v_mfma_i32_16x16x64_i8 v[82:85], v[188:191], v[216:219], v[82:85]
	v_mfma_i32_16x16x64_i8 v[70:73], v[180:183], v[224:227], v[70:73]
	v_mfma_i32_16x16x64_i8 v[66:69], v[188:191], v[224:227], v[66:69]
	s_barrier
	s_add_i32 s36, s66, s44
	v_lshl_add_u64 v[192:193], s[40:41], 0, v[134:135]
	s_mov_b32 m0, s36
	ds_read_b128 v[196:199], v176 offset:16384
	ds_read_b128 v[200:203], v176 offset:17408
	ds_read_b128 v[204:207], v176 offset:18432
	ds_read_b128 v[208:211], v176 offset:19456
	ds_read_b128 v[212:215], v176 offset:20480
	ds_read_b128 v[216:219], v176 offset:21504
	ds_read_b128 v[220:223], v176 offset:22528
	ds_read_b128 v[224:227], v176 offset:23552
	global_load_lds_dwordx4 v[192:193], off
	s_add_i32 m0, s36, 0x2000
	s_add_u32 s36, s40, 0x40000
	v_lshl_add_u64 v[228:229], s[40:41], 0, v[132:133]
	s_addc_u32 s37, s41, 0
	s_add_i32 s74, s67, s44
	global_load_lds_dwordx4 v[228:229], off
	v_lshl_add_u64 v[230:231], s[36:37], 0, v[134:135]
	s_mov_b32 m0, s74
	s_nop 0
	global_load_lds_dwordx4 v[230:231], off
	v_lshl_add_u64 v[230:231], s[36:37], 0, v[132:133]
	s_add_i32 m0, s74, 0x2000
	s_and_b64 s[36:37], s[8:9], s[42:43]
	s_and_b64 s[36:37], s[36:37], exec
	s_cselect_b32 s36, s26, s34
	s_cselect_b32 s37, s27, s35
	s_add_u32 s36, s36, s76
	s_addc_u32 s37, s37, 0
	global_load_lds_dwordx4 v[230:231], off
	v_lshl_add_u64 v[230:231], s[36:37], 0, v[136:137]
	s_mov_b32 m0, s47
	v_lshl_add_u64 v[232:233], s[36:37], 0, v[138:139]
	global_load_lds_dwordx4 v[230:231], off
	s_mov_b32 m0, s49
	s_nop 0
	global_load_lds_dwordx4 v[232:233], off
	s_waitcnt vmcnt(8)
	s_waitcnt lgkmcnt(0)
	s_barrier
; #define PG8_STAGE(bufoff, gbase, voff) do { _Pragma("unroll") for (int _i = 0; _i < 2; ++_i) \
;         __builtin_amdgcn_global_load_lds((const unsigned*)((const char*)(gbase) + (voff)[_i]), (LAS unsigned*)(lds + (bufoff) + ldsw + _i * 8192), 16, 0, 0); } while (0)
; #define PG8_LDA(dst, b, h) do { _Pragma("unroll") for (int m = 0; m < 4; ++m) dst[m] = PG8_LD32(lds + PG8_SA(b, h) + aoff + m * 2048); } while (0)
; #define PG8_LDB(dst, b, h) do { _Pragma("unroll") for (int n = 0; n < 2; ++n) dst[n] = PG8_LD32(lds + PG8_SB(b, h) + boff + n * 2048); } while (0)
; #define PG8_WAIT_V(n) asm volatile("s_waitcnt vmcnt(" #n ")" ::: "memory")
; #define PG8_WAIT_L(n) asm volatile("s_waitcnt lgkmcnt(" #n ")" ::: "memory")
; #define PG8_BAR __builtin_amdgcn_s_barrier()
; #define PG8_SCHED __builtin_amdgcn_sched_barrier(0)
; template <class Epi, class Sched, bool ALIGN_EPI, int DT>
; __device__ __forceinline__ void gemm_phase(LAS unsigned char* lds, const int KB, const Sched& S, const Epi& E) {
;     ...
;             const size_t k1 = (size_t)(t + 1) * kstep, k2 = last ? 0 : (size_t)(t + 2) * kstep, k3 = k2 + kstep;
;             const char* b2 = last ? nB : cB + (size_t)(t + 2) * kstep; const char* b3 = b2 + kstep;
;             PG8_LDB(B0, 0, 0); PG8_LDB(B1, 0, 1); PG8_SCHED; PG8_LDA(At, 0, 0); PG8_STA(PG8_SA(1, 1), false, 1, k1);
;             PG8_WAIT_V(8); PG8_WAIT_L(0); PG8_BAR; PG8_MMA(0, 0, At, B0); PG8_MMA(0, 1, At, B1); PG8_BAR; PG8_SCHED;
;             PG8_LDA(At, 0, 1); PG8_STAGE(PG8_SB(0, 0), b2, voffB); PG8_STAGE(PG8_SB(0, 1), b2 + hstep, voffB); PG8_STA(PG8_SA(0, 0), last, 0, k2);
;             PG8_WAIT_V(8); PG8_WAIT_L(0); PG8_BAR; PG8_MMA(1, 0, At, B0); PG8_MMA(1, 1, At, B1); PG8_BAR; PG8_SCHED;
;             PG8_LDB(B0, 1, 0); PG8_LDB(B1, 1, 1); PG8_SCHED; PG8_LDA(At, 1, 0); PG8_STA(PG8_SA(0, 1), last, 1, k2);
;             PG8_WAIT_V(8); PG8_WAIT_L(0); PG8_BAR; PG8_MMA(0, 0, At, B0); PG8_MMA(0, 1, At, B1); PG8_BAR; PG8_SCHED;
;             PG8_LDA(At, 1, 1); PG8_STAGE(PG8_SB(1, 0), b3, voffB); PG8_STAGE(PG8_SB(1, 1), b3 + hstep, voffB); PG8_STA(PG8_SA(1, 0), last, 0, k3);
;             PG8_WAIT_V(8); PG8_WAIT_L(0); PG8_BAR; PG8_MMA(1, 0, At, B0); PG8_MMA(1, 1, At, B1); PG8_BAR; PG8_SCHED;
;         }
	s_waitcnt lgkmcnt(0)
	v_mfma_i32_16x16x64_i8 v[62:65], v[152:155], v[196:199], v[62:65]
	v_mfma_i32_16x16x64_i8 v[58:61], v[160:163], v[196:199], v[58:61]
	v_mfma_i32_16x16x64_i8 v[46:49], v[152:155], v[204:207], v[46:49]
	v_mfma_i32_16x16x64_i8 v[42:45], v[160:163], v[204:207], v[42:45]
	v_mfma_i32_16x16x64_i8 v[30:33], v[152:155], v[212:215], v[30:33]
	v_mfma_i32_16x16x64_i8 v[26:29], v[160:163], v[212:215], v[26:29]
	v_mfma_i32_16x16x64_i8 v[6:9], v[152:155], v[220:223], v[6:9]
	v_mfma_i32_16x16x64_i8 v[2:5], v[160:163], v[220:223], v[2:5]
	v_mfma_i32_16x16x64_i8 v[62:65], v[156:159], v[200:203], v[62:65]
	v_mfma_i32_16x16x64_i8 v[58:61], v[164:167], v[200:203], v[58:61]
	v_mfma_i32_16x16x64_i8 v[46:49], v[156:159], v[208:211], v[46:49]
	v_mfma_i32_16x16x64_i8 v[42:45], v[164:167], v[208:211], v[42:45]
	v_mfma_i32_16x16x64_i8 v[30:33], v[156:159], v[216:219], v[30:33]
	v_mfma_i32_16x16x64_i8 v[26:29], v[164:167], v[216:219], v[26:29]
	v_mfma_i32_16x16x64_i8 v[6:9], v[156:159], v[224:227], v[6:9]
	v_mfma_i32_16x16x64_i8 v[2:5], v[164:167], v[224:227], v[2:5]
	v_mfma_i32_16x16x64_i8 v[54:57], v[168:171], v[196:199], v[54:57]
	v_mfma_i32_16x16x64_i8 v[50:53], v[184:187], v[196:199], v[50:53]
	v_mfma_i32_16x16x64_i8 v[38:41], v[168:171], v[204:207], v[38:41]
	v_mfma_i32_16x16x64_i8 v[34:37], v[184:187], v[204:207], v[34:37]
	v_mfma_i32_16x16x64_i8 v[14:17], v[168:171], v[212:215], v[14:17]
	v_mfma_i32_16x16x64_i8 v[10:13], v[184:187], v[212:215], v[10:13]
	v_mfma_i32_16x16x64_i8 v[22:25], v[168:171], v[220:223], v[22:25]
	v_mfma_i32_16x16x64_i8 v[18:21], v[184:187], v[220:223], v[18:21]
	v_mfma_i32_16x16x64_i8 v[54:57], v[180:183], v[200:203], v[54:57]
	v_mfma_i32_16x16x64_i8 v[50:53], v[188:191], v[200:203], v[50:53]
	v_mfma_i32_16x16x64_i8 v[38:41], v[180:183], v[208:211], v[38:41]
	v_mfma_i32_16x16x64_i8 v[34:37], v[188:191], v[208:211], v[34:37]
	v_mfma_i32_16x16x64_i8 v[14:17], v[180:183], v[216:219], v[14:17]
	v_mfma_i32_16x16x64_i8 v[10:13], v[188:191], v[216:219], v[10:13]
	v_mfma_i32_16x16x64_i8 v[22:25], v[180:183], v[224:227], v[22:25]
	v_mfma_i32_16x16x64_i8 v[18:21], v[188:191], v[224:227], v[18:21]
	s_barrier
	s_add_i32 s42, 0, 0x18000
	v_add_u32_e32 v1, s42, v172
	s_add_i32 s43, 0, 0x1c000
	ds_read_b128 v[152:155], v1
	ds_read_b128 v[156:159], v1 offset:1024
	ds_read_b128 v[160:163], v1 offset:2048
	ds_read_b128 v[164:167], v1 offset:3072
	v_add_u32_e32 v1, s43, v172
	ds_read_b128 v[168:171], v1
	ds_read_b128 v[180:183], v1 offset:1024
	ds_read_b128 v[184:187], v1 offset:2048
	ds_read_b128 v[188:191], v1 offset:3072
	s_add_u32 s36, s36, 0x40000
	s_addc_u32 s37, s37, 0
	s_mov_b32 m0, s52
	v_lshl_add_u64 v[234:235], s[36:37], 0, v[136:137]
	ds_read_b128 v[196:199], v176 offset:32768
	ds_read_b128 v[200:203], v176 offset:33792
	ds_read_b128 v[204:207], v176 offset:34816
	ds_read_b128 v[208:211], v176 offset:35840
	ds_read_b128 v[212:215], v176 offset:36864
	ds_read_b128 v[216:219], v176 offset:37888
	ds_read_b128 v[220:223], v176 offset:38912
	ds_read_b128 v[224:227], v176 offset:39936
	global_load_lds_dwordx4 v[234:235], off
	v_lshl_add_u64 v[234:235], s[36:37], 0, v[138:139]
	s_mov_b32 m0, s53
	s_nop 0
	global_load_lds_dwordx4 v[234:235], off
	s_waitcnt vmcnt(8)
	s_waitcnt lgkmcnt(0)
	s_barrier
	s_waitcnt lgkmcnt(0)
	v_mfma_i32_16x16x64_i8 v[126:129], v[152:155], v[196:199], v[126:129]
	v_mfma_i32_16x16x64_i8 v[122:125], v[160:163], v[196:199], v[122:125]
	v_mfma_i32_16x16x64_i8 v[110:113], v[152:155], v[204:207], v[110:113]
	v_mfma_i32_16x16x64_i8 v[106:109], v[160:163], v[204:207], v[106:109]
	v_mfma_i32_16x16x64_i8 v[94:97], v[152:155], v[212:215], v[94:97]
	v_mfma_i32_16x16x64_i8 v[90:93], v[160:163], v[212:215], v[90:93]
	v_mfma_i32_16x16x64_i8 v[78:81], v[152:155], v[220:223], v[78:81]
	v_mfma_i32_16x16x64_i8 v[74:77], v[160:163], v[220:223], v[74:77]
	v_mfma_i32_16x16x64_i8 v[126:129], v[156:159], v[200:203], v[126:129]
	v_mfma_i32_16x16x64_i8 v[122:125], v[164:167], v[200:203], v[122:125]
	v_mfma_i32_16x16x64_i8 v[110:113], v[156:159], v[208:211], v[110:113]
	v_mfma_i32_16x16x64_i8 v[106:109], v[164:167], v[208:211], v[106:109]
	v_mfma_i32_16x16x64_i8 v[94:97], v[156:159], v[216:219], v[94:97]
	v_mfma_i32_16x16x64_i8 v[90:93], v[164:167], v[216:219], v[90:93]
	v_mfma_i32_16x16x64_i8 v[78:81], v[156:159], v[224:227], v[78:81]
	v_mfma_i32_16x16x64_i8 v[74:77], v[164:167], v[224:227], v[74:77]
	v_mfma_i32_16x16x64_i8 v[118:121], v[168:171], v[196:199], v[118:121]
	v_mfma_i32_16x16x64_i8 v[114:117], v[184:187], v[196:199], v[114:117]
	v_mfma_i32_16x16x64_i8 v[102:105], v[168:171], v[204:207], v[102:105]
	v_mfma_i32_16x16x64_i8 v[98:101], v[184:187], v[204:207], v[98:101]
	v_mfma_i32_16x16x64_i8 v[86:89], v[168:171], v[212:215], v[86:89]
	v_mfma_i32_16x16x64_i8 v[82:85], v[184:187], v[212:215], v[82:85]
	v_mfma_i32_16x16x64_i8 v[70:73], v[168:171], v[220:223], v[70:73]
	v_mfma_i32_16x16x64_i8 v[66:69], v[184:187], v[220:223], v[66:69]
	v_mfma_i32_16x16x64_i8 v[118:121], v[180:183], v[200:203], v[118:121]
	v_mfma_i32_16x16x64_i8 v[114:117], v[188:191], v[200:203], v[114:117]
	v_mfma_i32_16x16x64_i8 v[102:105], v[180:183], v[208:211], v[102:105]
	v_mfma_i32_16x16x64_i8 v[98:101], v[188:191], v[208:211], v[98:101]
	v_mfma_i32_16x16x64_i8 v[86:89], v[180:183], v[216:219], v[86:89]
	v_mfma_i32_16x16x64_i8 v[82:85], v[188:191], v[216:219], v[82:85]
	v_mfma_i32_16x16x64_i8 v[70:73], v[180:183], v[224:227], v[70:73]
	v_mfma_i32_16x16x64_i8 v[66:69], v[188:191], v[224:227], v[66:69]
	s_barrier
; #define PG8_STAGE(bufoff, gbase, voff) do { _Pragma("unroll") for (int _i = 0; _i < 2; ++_i) \
;         __builtin_amdgcn_global_load_lds((const unsigned*)((const char*)(gbase) + (voff)[_i]), (LAS unsigned*)(lds + (bufoff) + ldsw + _i * 8192), 16, 0, 0); } while (0)
; #define PG8_LDA(dst, b, h) do { _Pragma("unroll") for (int m = 0; m < 4; ++m) dst[m] = PG8_LD32(lds + PG8_SA(b, h) + aoff + m * 2048); } while (0)
; #define PG8_LDB(dst, b, h) do { _Pragma("unroll") for (int n = 0; n < 2; ++n) dst[n] = PG8_LD32(lds + PG8_SB(b, h) + boff + n * 2048); } while (0)
; #define PG8_WAIT_V(n) asm volatile("s_waitcnt vmcnt(" #n ")" ::: "memory")
; #define PG8_WAIT_L(n) asm volatile("s_waitcnt lgkmcnt(" #n ")" ::: "memory")
; #define PG8_BAR __builtin_amdgcn_s_barrier()
; #define PG8_SCHED __builtin_amdgcn_sched_barrier(0)
; template <class Epi, class Sched, bool ALIGN_EPI, int DT>
; __device__ __forceinline__ void gemm_phase(LAS unsigned char* lds, const int KB, const Sched& S, const Epi& E) {
;     ...
;             const size_t k1 = (size_t)(t + 1) * kstep, k2 = last ? 0 : (size_t)(t + 2) * kstep, k3 = k2 + kstep;
;             const char* b2 = last ? nB : cB + (size_t)(t + 2) * kstep; const char* b3 = b2 + kstep;
;             PG8_LDB(B0, 0, 0); PG8_LDB(B1, 0, 1); PG8_SCHED; PG8_LDA(At, 0, 0); PG8_STA(PG8_SA(1, 1), false, 1, k1);
;             PG8_WAIT_V(8); PG8_WAIT_L(0); PG8_BAR; PG8_MMA(0, 0, At, B0); PG8_MMA(0, 1, At, B1); PG8_BAR; PG8_SCHED;
;             PG8_LDA(At, 0, 1); PG8_STAGE(PG8_SB(0, 0), b2, voffB); PG8_STAGE(PG8_SB(0, 1), b2 + hstep, voffB); PG8_STA(PG8_SA(0, 0), last, 0, k2);
;             PG8_WAIT_V(8); PG8_WAIT_L(0); PG8_BAR; PG8_MMA(1, 0, At, B0); PG8_MMA(1, 1, At, B1); PG8_BAR; PG8_SCHED;
;             PG8_LDB(B0, 1, 0); PG8_LDB(B1, 1, 1); PG8_SCHED; PG8_LDA(At, 1, 0); PG8_STA(PG8_SA(0, 1), last, 1, k2);
;             PG8_WAIT_V(8); PG8_WAIT_L(0); PG8_BAR; PG8_MMA(0, 0, At, B0); PG8_MMA(0, 1, At, B1); PG8_BAR; PG8_SCHED;
;             PG8_LDA(At, 1, 1); PG8_STAGE(PG8_SB(1, 0), b3, voffB); PG8_STAGE(PG8_SB(1, 1), b3 + hstep, voffB); PG8_STA(PG8_SA(1, 0), last, 0, k3);
;             PG8_WAIT_V(8); PG8_WAIT_L(0); PG8_BAR; PG8_MMA(1, 0, At, B0); PG8_MMA(1, 1, At, B1); PG8_BAR; PG8_SCHED;
;         }
	s_add_i32 s36, s42, s44
	v_lshl_add_u64 v[192:193], v[192:193], 0, s[18:19]
	s_mov_b32 m0, s36
	ds_read_b128 v[196:199], v176 offset:49152
	ds_read_b128 v[200:203], v176 offset:50176
	ds_read_b128 v[204:207], v176 offset:51200
	ds_read_b128 v[208:211], v176 offset:52224
	ds_read_b128 v[212:215], v176 offset:53248
	ds_read_b128 v[216:219], v176 offset:54272
	ds_read_b128 v[220:223], v176 offset:55296
	ds_read_b128 v[224:227], v176 offset:56320
	global_load_lds_dwordx4 v[192:193], off
	s_add_i32 m0, s36, 0x2000
	s_add_u32 s36, s40, 0x40080
	v_lshl_add_u64 v[192:193], v[228:229], 0, s[18:19]
	s_addc_u32 s37, s41, 0
	s_add_i32 s40, s43, s44
	global_load_lds_dwordx4 v[192:193], off
	v_lshl_add_u64 v[192:193], s[36:37], 0, v[134:135]
	s_mov_b32 m0, s40
	s_nop 0
	global_load_lds_dwordx4 v[192:193], off
	v_lshl_add_u64 v[192:193], s[36:37], 0, v[132:133]
	s_add_i32 m0, s40, 0x2000
	s_nop 0
	global_load_lds_dwordx4 v[192:193], off
	v_lshl_add_u64 v[192:193], v[230:231], 0, s[18:19]
	s_mov_b32 m0, s57
	s_nop 0
	global_load_lds_dwordx4 v[192:193], off
	v_lshl_add_u64 v[192:193], v[232:233], 0, s[18:19]
	s_mov_b32 m0, s62
	s_nop 0
	global_load_lds_dwordx4 v[192:193], off
	s_waitcnt vmcnt(8)
	s_waitcnt lgkmcnt(0)
	s_barrier
	s_waitcnt lgkmcnt(0)
	v_mfma_i32_16x16x64_i8 v[62:65], v[152:155], v[196:199], v[62:65]
	v_mfma_i32_16x16x64_i8 v[58:61], v[160:163], v[196:199], v[58:61]
	v_mfma_i32_16x16x64_i8 v[46:49], v[152:155], v[204:207], v[46:49]
	v_mfma_i32_16x16x64_i8 v[42:45], v[160:163], v[204:207], v[42:45]
	v_mfma_i32_16x16x64_i8 v[30:33], v[152:155], v[212:215], v[30:33]
	v_mfma_i32_16x16x64_i8 v[26:29], v[160:163], v[212:215], v[26:29]
	v_mfma_i32_16x16x64_i8 v[6:9], v[152:155], v[220:223], v[6:9]
	v_mfma_i32_16x16x64_i8 v[2:5], v[160:163], v[220:223], v[2:5]
	v_mfma_i32_16x16x64_i8 v[62:65], v[156:159], v[200:203], v[62:65]
	v_mfma_i32_16x16x64_i8 v[58:61], v[164:167], v[200:203], v[58:61]
	v_mfma_i32_16x16x64_i8 v[46:49], v[156:159], v[208:211], v[46:49]
	v_mfma_i32_16x16x64_i8 v[42:45], v[164:167], v[208:211], v[42:45]
	v_mfma_i32_16x16x64_i8 v[30:33], v[156:159], v[216:219], v[30:33]
	v_mfma_i32_16x16x64_i8 v[26:29], v[164:167], v[216:219], v[26:29]
	v_mfma_i32_16x16x64_i8 v[6:9], v[156:159], v[224:227], v[6:9]
	v_mfma_i32_16x16x64_i8 v[2:5], v[164:167], v[224:227], v[2:5]
	v_mfma_i32_16x16x64_i8 v[54:57], v[168:171], v[196:199], v[54:57]
	v_mfma_i32_16x16x64_i8 v[50:53], v[184:187], v[196:199], v[50:53]
	v_mfma_i32_16x16x64_i8 v[38:41], v[168:171], v[204:207], v[38:41]
	v_mfma_i32_16x16x64_i8 v[34:37], v[184:187], v[204:207], v[34:37]
	v_mfma_i32_16x16x64_i8 v[14:17], v[168:171], v[212:215], v[14:17]
	v_mfma_i32_16x16x64_i8 v[10:13], v[184:187], v[212:215], v[10:13]
	v_mfma_i32_16x16x64_i8 v[22:25], v[168:171], v[220:223], v[22:25]
	v_mfma_i32_16x16x64_i8 v[18:21], v[184:187], v[220:223], v[18:21]
	v_mfma_i32_16x16x64_i8 v[54:57], v[180:183], v[200:203], v[54:57]
	v_mfma_i32_16x16x64_i8 v[50:53], v[188:191], v[200:203], v[50:53]
	v_mfma_i32_16x16x64_i8 v[38:41], v[180:183], v[208:211], v[38:41]
	v_mfma_i32_16x16x64_i8 v[34:37], v[188:191], v[208:211], v[34:37]
	v_mfma_i32_16x16x64_i8 v[14:17], v[180:183], v[216:219], v[14:17]
	v_mfma_i32_16x16x64_i8 v[10:13], v[188:191], v[216:219], v[10:13]
	v_mfma_i32_16x16x64_i8 v[22:25], v[180:183], v[224:227], v[22:25]
	v_mfma_i32_16x16x64_i8 v[18:21], v[188:191], v[224:227], v[18:21]
	s_barrier
	s_add_i32 s71, s71, 2
	s_cmp_gt_u32 s71, 13
	s_mov_b64 s[36:37], s[38:39]
	s_cbranch_scc0 .LBB0_1385
	s_and_b64 vcc, exec, s[20:21]
	s_cbranch_vccz .LBB0_1388
	s_barrier

; #define PG8_STAGE(bufoff, gbase, voff) do { _Pragma("unroll") for (int _i = 0; _i < 2; ++_i) \
;         __builtin_amdgcn_global_load_lds((const unsigned*)((const char*)(gbase) + (voff)[_i]), (LAS unsigned*)(lds + (bufoff) + ldsw + _i * 8192), 16, 0, 0); } while (0)
; #define PG8_LDA(dst, b, h) do { _Pragma("unroll") for (int m = 0; m < 4; ++m) dst[m] = PG8_LD32(lds + PG8_SA(b, h) + aoff + m * 2048); } while (0)
; #define PG8_LDB(dst, b, h) do { _Pragma("unroll") for (int n = 0; n < 2; ++n) dst[n] = PG8_LD32(lds + PG8_SB(b, h) + boff + n * 2048); } while (0)
; #define PG8_WAIT_V(n) asm volatile("s_waitcnt vmcnt(" #n ")" ::: "memory")
; #define PG8_WAIT_L(n) asm volatile("s_waitcnt lgkmcnt(" #n ")" ::: "memory")
; #define PG8_BAR __builtin_amdgcn_s_barrier()
; #define PG8_SCHED __builtin_amdgcn_sched_barrier(0)
; template <class Epi, class Sched, bool ALIGN_EPI, int DT>
; __device__ __forceinline__ void gemm_phase(LAS unsigned char* lds, const int KB, const Sched& S, const Epi& E) {
;     ...
;             const size_t k1 = (size_t)(t + 1) * kstep, k2 = last ? 0 : (size_t)(t + 2) * kstep, k3 = k2 + kstep;
;             const char* b2 = last ? nB : cB + (size_t)(t + 2) * kstep; const char* b3 = b2 + kstep;
;             PG8_LDB(B0, 0, 0); PG8_LDB(B1, 0, 1); PG8_SCHED; PG8_LDA(At, 0, 0); PG8_STA(PG8_SA(1, 1), false, 1, k1);
;             PG8_WAIT_V(8); PG8_WAIT_L(0); PG8_BAR; PG8_MMA(0, 0, At, B0); PG8_MMA(0, 1, At, B1); PG8_BAR; PG8_SCHED;
;             PG8_LDA(At, 0, 1); PG8_STAGE(PG8_SB(0, 0), b2, voffB); PG8_STAGE(PG8_SB(0, 1), b2 + hstep, voffB); PG8_STA(PG8_SA(0, 0), last, 0, k2);
;             PG8_WAIT_V(8); PG8_WAIT_L(0); PG8_BAR; PG8_MMA(1, 0, At, B0); PG8_MMA(1, 1, At, B1); PG8_BAR; PG8_SCHED;
;             PG8_LDB(B0, 1, 0); PG8_LDB(B1, 1, 1); PG8_SCHED; PG8_LDA(At, 1, 0); PG8_STA(PG8_SA(0, 1), last, 1, k2);
;             PG8_WAIT_V(8); PG8_WAIT_L(0); PG8_BAR; PG8_MMA(0, 0, At, B0); PG8_MMA(0, 1, At, B1); PG8_BAR; PG8_SCHED;
;             PG8_LDA(At, 1, 1); PG8_STAGE(PG8_SB(1, 0), b3, voffB); PG8_STAGE(PG8_SB(1, 1), b3 + hstep, voffB); PG8_STA(PG8_SA(1, 0), last, 0, k3);
;             PG8_WAIT_V(8); PG8_WAIT_L(0); PG8_BAR; PG8_MMA(1, 0, At, B0); PG8_MMA(1, 1, At, B1); PG8_BAR; PG8_SCHED;
;         }
.LBB0_2108:
	ds_read_b128 v[18:21], v193
	ds_read_b128 v[22:25], v193 offset:1024
	ds_read_b128 v[26:29], v193 offset:2048
	ds_read_b128 v[30:33], v193 offset:3072
	ds_read_b128 v[2:5], v195
	ds_read_b128 v[6:9], v195 offset:1024
	ds_read_b128 v[10:13], v195 offset:2048
	ds_read_b128 v[14:17], v195 offset:3072
	s_add_u32 s38, s42, 0x100
	s_addc_u32 s39, s43, 0
	s_add_u32 s71, s68, s42
	s_addc_u32 s74, s69, s43
	s_cmp_eq_u32 s70, 12
	s_cselect_b64 s[44:45], -1, 0
	s_and_b64 s[40:41], s[44:45], exec
	s_cselect_b32 s41, s25, s74
	s_cselect_b32 s40, s27, s71
	s_cselect_b32 s71, 0, s39
	s_cselect_b32 s74, 0, s38
	v_lshl_add_u64 v[222:223], v[178:179], 0, s[42:43]
	s_add_i32 m0, s35, 0xc000
	ds_read_b128 v[182:185], v196
	ds_read_b128 v[186:189], v196 offset:1024
	ds_read_b128 v[198:201], v196 offset:2048
	ds_read_b128 v[202:205], v196 offset:3072
	ds_read_b128 v[206:209], v196 offset:4096
	ds_read_b128 v[210:213], v196 offset:5120
	ds_read_b128 v[214:217], v196 offset:6144
	ds_read_b128 v[218:221], v196 offset:7168
	global_load_lds_dwordx4 v[222:223], off
	v_lshl_add_u64 v[222:223], v[180:181], 0, s[42:43]
	s_add_i32 m0, s35, 0xe000
	s_nop 0
	global_load_lds_dwordx4 v[222:223], off
	s_waitcnt vmcnt(8)
	s_waitcnt lgkmcnt(0)
	s_barrier
	s_waitcnt lgkmcnt(0)
	v_mfma_scale_f32_16x16x128_f8f6f4 v[158:161], v[18:25], v[182:189], v[158:161], v1, v1 op_sel_hi:[0,0,0]
	v_mfma_scale_f32_16x16x128_f8f6f4 v[154:157], v[26:33], v[182:189], v[154:157], v1, v1 op_sel_hi:[0,0,0]
	v_mfma_scale_f32_16x16x128_f8f6f4 v[150:153], v[18:25], v[198:205], v[150:153], v1, v1 op_sel_hi:[0,0,0]
	v_mfma_scale_f32_16x16x128_f8f6f4 v[142:145], v[26:33], v[198:205], v[142:145], v1, v1 op_sel_hi:[0,0,0]
	v_mfma_scale_f32_16x16x128_f8f6f4 v[134:137], v[18:25], v[206:213], v[134:137], v1, v1 op_sel_hi:[0,0,0]
	v_mfma_scale_f32_16x16x128_f8f6f4 v[126:129], v[26:33], v[206:213], v[126:129], v1, v1 op_sel_hi:[0,0,0]
	v_mfma_scale_f32_16x16x128_f8f6f4 v[118:121], v[18:25], v[214:221], v[118:121], v1, v1 op_sel_hi:[0,0,0]
	v_mfma_scale_f32_16x16x128_f8f6f4 v[110:113], v[26:33], v[214:221], v[110:113], v1, v1 op_sel_hi:[0,0,0]
	v_mfma_scale_f32_16x16x128_f8f6f4 v[146:149], v[2:9], v[182:189], v[146:149], v1, v1 op_sel_hi:[0,0,0]
	v_mfma_scale_f32_16x16x128_f8f6f4 v[138:141], v[10:17], v[182:189], v[138:141], v1, v1 op_sel_hi:[0,0,0]
	v_mfma_scale_f32_16x16x128_f8f6f4 v[130:133], v[2:9], v[198:205], v[130:133], v1, v1 op_sel_hi:[0,0,0]
	v_mfma_scale_f32_16x16x128_f8f6f4 v[122:125], v[10:17], v[198:205], v[122:125], v1, v1 op_sel_hi:[0,0,0]
	v_mfma_scale_f32_16x16x128_f8f6f4 v[114:117], v[2:9], v[206:213], v[114:117], v1, v1 op_sel_hi:[0,0,0]
	v_mfma_scale_f32_16x16x128_f8f6f4 v[106:109], v[10:17], v[206:213], v[106:109], v1, v1 op_sel_hi:[0,0,0]
	v_mfma_scale_f32_16x16x128_f8f6f4 v[102:105], v[2:9], v[214:221], v[102:105], v1, v1 op_sel_hi:[0,0,0]
	v_mfma_scale_f32_16x16x128_f8f6f4 v[98:101], v[10:17], v[214:221], v[98:101], v1, v1 op_sel_hi:[0,0,0]
	s_barrier
	s_add_i32 s42, s57, s46
	v_lshl_add_u64 v[182:183], s[40:41], 0, v[162:163]
	s_mov_b32 m0, s42
	ds_read_b128 v[198:201], v196 offset:16384
	ds_read_b128 v[202:205], v196 offset:17408
	ds_read_b128 v[206:209], v196 offset:18432
	ds_read_b128 v[210:213], v196 offset:19456
	ds_read_b128 v[214:217], v196 offset:20480
	ds_read_b128 v[218:221], v196 offset:21504
	ds_read_b128 v[222:225], v196 offset:22528
	ds_read_b128 v[226:229], v196 offset:23552
	global_load_lds_dwordx4 v[182:183], off
	s_add_i32 m0, s42, 0x2000
	s_add_u32 s42, s40, 0x40000
	v_lshl_add_u64 v[184:185], s[40:41], 0, v[164:165]
	s_addc_u32 s43, s41, 0
	s_add_i32 s75, s62, s46
	global_load_lds_dwordx4 v[184:185], off
	v_lshl_add_u64 v[186:187], s[42:43], 0, v[162:163]
	s_mov_b32 m0, s75
	s_nop 0
	global_load_lds_dwordx4 v[186:187], off
	v_lshl_add_u64 v[186:187], s[42:43], 0, v[164:165]
	s_add_i32 m0, s75, 0x2000
	s_and_b64 s[42:43], s[6:7], s[44:45]
	s_and_b64 s[42:43], s[42:43], exec
	s_cselect_b32 s42, s28, s36
	s_cselect_b32 s43, s29, s37
	s_add_u32 s42, s42, s74
	s_addc_u32 s43, s43, s71
	global_load_lds_dwordx4 v[186:187], off
	v_lshl_add_u64 v[186:187], s[42:43], 0, v[166:167]
	s_mov_b32 m0, s35
	v_lshl_add_u64 v[188:189], s[42:43], 0, v[168:169]
	global_load_lds_dwordx4 v[186:187], off
	s_mov_b32 m0, s47
	s_nop 0
	global_load_lds_dwordx4 v[188:189], off
	s_waitcnt vmcnt(8)
	s_waitcnt lgkmcnt(0)
	s_barrier
	s_waitcnt lgkmcnt(0)
	v_mfma_scale_f32_16x16x128_f8f6f4 v[94:97], v[18:25], v[198:205], v[94:97], v1, v1 op_sel_hi:[0,0,0]
	v_mfma_scale_f32_16x16x128_f8f6f4 v[90:93], v[26:33], v[198:205], v[90:93], v1, v1 op_sel_hi:[0,0,0]
	v_mfma_scale_f32_16x16x128_f8f6f4 v[86:89], v[18:25], v[206:213], v[86:89], v1, v1 op_sel_hi:[0,0,0]
	v_mfma_scale_f32_16x16x128_f8f6f4 v[78:81], v[26:33], v[206:213], v[78:81], v1, v1 op_sel_hi:[0,0,0]
	v_mfma_scale_f32_16x16x128_f8f6f4 v[62:65], v[18:25], v[214:221], v[62:65], v1, v1 op_sel_hi:[0,0,0]
	v_mfma_scale_f32_16x16x128_f8f6f4 v[54:57], v[26:33], v[214:221], v[54:57], v1, v1 op_sel_hi:[0,0,0]
	v_mfma_scale_f32_16x16x128_f8f6f4 v[46:49], v[18:25], v[222:229], v[46:49], v1, v1 op_sel_hi:[0,0,0]
	v_mfma_scale_f32_16x16x128_f8f6f4 v[38:41], v[26:33], v[222:229], v[38:41], v1, v1 op_sel_hi:[0,0,0]
	v_mfma_scale_f32_16x16x128_f8f6f4 v[82:85], v[2:9], v[198:205], v[82:85], v1, v1 op_sel_hi:[0,0,0]
	v_mfma_scale_f32_16x16x128_f8f6f4 v[74:77], v[10:17], v[198:205], v[74:77], v1, v1 op_sel_hi:[0,0,0]
	v_mfma_scale_f32_16x16x128_f8f6f4 v[58:61], v[2:9], v[206:213], v[58:61], v1, v1 op_sel_hi:[0,0,0]
	v_mfma_scale_f32_16x16x128_f8f6f4 v[50:53], v[10:17], v[206:213], v[50:53], v1, v1 op_sel_hi:[0,0,0]
	v_mfma_scale_f32_16x16x128_f8f6f4 v[42:45], v[2:9], v[214:221], v[42:45], v1, v1 op_sel_hi:[0,0,0]
	v_mfma_scale_f32_16x16x128_f8f6f4 v[34:37], v[10:17], v[214:221], v[34:37], v1, v1 op_sel_hi:[0,0,0]
	v_mfma_scale_f32_16x16x128_f8f6f4 v[70:73], v[2:9], v[222:229], v[70:73], v1, v1 op_sel_hi:[0,0,0]
	v_mfma_scale_f32_16x16x128_f8f6f4 v[66:69], v[10:17], v[222:229], v[66:69], v1, v1 op_sel_hi:[0,0,0]
	s_barrier
; #define PG8_STAGE(bufoff, gbase, voff) do { _Pragma("unroll") for (int _i = 0; _i < 2; ++_i) \
;         __builtin_amdgcn_global_load_lds((const unsigned*)((const char*)(gbase) + (voff)[_i]), (LAS unsigned*)(lds + (bufoff) + ldsw + _i * 8192), 16, 0, 0); } while (0)
; #define PG8_LDA(dst, b, h) do { _Pragma("unroll") for (int m = 0; m < 4; ++m) dst[m] = PG8_LD32(lds + PG8_SA(b, h) + aoff + m * 2048); } while (0)
; #define PG8_LDB(dst, b, h) do { _Pragma("unroll") for (int n = 0; n < 2; ++n) dst[n] = PG8_LD32(lds + PG8_SB(b, h) + boff + n * 2048); } while (0)
; #define PG8_WAIT_V(n) asm volatile("s_waitcnt vmcnt(" #n ")" ::: "memory")
; #define PG8_WAIT_L(n) asm volatile("s_waitcnt lgkmcnt(" #n ")" ::: "memory")
; #define PG8_BAR __builtin_amdgcn_s_barrier()
; #define PG8_SCHED __builtin_amdgcn_sched_barrier(0)
; template <class Epi, class Sched, bool ALIGN_EPI, int DT>
; __device__ __forceinline__ void gemm_phase(LAS unsigned char* lds, const int KB, const Sched& S, const Epi& E) {
;     ...
;             const size_t k1 = (size_t)(t + 1) * kstep, k2 = last ? 0 : (size_t)(t + 2) * kstep, k3 = k2 + kstep;
;             const char* b2 = last ? nB : cB + (size_t)(t + 2) * kstep; const char* b3 = b2 + kstep;
;             PG8_LDB(B0, 0, 0); PG8_LDB(B1, 0, 1); PG8_SCHED; PG8_LDA(At, 0, 0); PG8_STA(PG8_SA(1, 1), false, 1, k1);
;             PG8_WAIT_V(8); PG8_WAIT_L(0); PG8_BAR; PG8_MMA(0, 0, At, B0); PG8_MMA(0, 1, At, B1); PG8_BAR; PG8_SCHED;
;             PG8_LDA(At, 0, 1); PG8_STAGE(PG8_SB(0, 0), b2, voffB); PG8_STAGE(PG8_SB(0, 1), b2 + hstep, voffB); PG8_STA(PG8_SA(0, 0), last, 0, k2);
;             PG8_WAIT_V(8); PG8_WAIT_L(0); PG8_BAR; PG8_MMA(1, 0, At, B0); PG8_MMA(1, 1, At, B1); PG8_BAR; PG8_SCHED;
;             PG8_LDB(B0, 1, 0); PG8_LDB(B1, 1, 1); PG8_SCHED; PG8_LDA(At, 1, 0); PG8_STA(PG8_SA(0, 1), last, 1, k2);
;             PG8_WAIT_V(8); PG8_WAIT_L(0); PG8_BAR; PG8_MMA(0, 0, At, B0); PG8_MMA(0, 1, At, B1); PG8_BAR; PG8_SCHED;
;             PG8_LDA(At, 1, 1); PG8_STAGE(PG8_SB(1, 0), b3, voffB); PG8_STAGE(PG8_SB(1, 1), b3 + hstep, voffB); PG8_STA(PG8_SA(1, 0), last, 0, k3);
;             PG8_WAIT_V(8); PG8_WAIT_L(0); PG8_BAR; PG8_MMA(1, 0, At, B0); PG8_MMA(1, 1, At, B1); PG8_BAR; PG8_SCHED;
;         }
	s_add_i32 s44, 0, 0x18000
	s_add_i32 s45, 0, 0x1c000
	v_add_u32_e32 v14, s44, v191
	v_add_u32_e32 v30, s45, v191
	ds_read_b128 v[2:5], v14
	ds_read_b128 v[6:9], v14 offset:1024
	ds_read_b128 v[10:13], v14 offset:2048
	ds_read_b128 v[14:17], v14 offset:3072
	ds_read_b128 v[18:21], v30
	ds_read_b128 v[22:25], v30 offset:1024
	ds_read_b128 v[26:29], v30 offset:2048
	ds_read_b128 v[30:33], v30 offset:3072
	s_add_u32 s42, s42, 0x40000
	s_addc_u32 s43, s43, 0
	s_mov_b32 m0, s49
	v_lshl_add_u64 v[230:231], s[42:43], 0, v[166:167]
	ds_read_b128 v[198:201], v196 offset:32768
	ds_read_b128 v[202:205], v196 offset:33792
	ds_read_b128 v[206:209], v196 offset:34816
	ds_read_b128 v[210:213], v196 offset:35840
	ds_read_b128 v[214:217], v196 offset:36864
	ds_read_b128 v[218:221], v196 offset:37888
	ds_read_b128 v[222:225], v196 offset:38912
	ds_read_b128 v[226:229], v196 offset:39936
	global_load_lds_dwordx4 v[230:231], off
	v_lshl_add_u64 v[230:231], s[42:43], 0, v[168:169]
	s_mov_b32 m0, s52
	s_nop 0
	global_load_lds_dwordx4 v[230:231], off
	s_waitcnt vmcnt(8)
	s_waitcnt lgkmcnt(0)
	s_barrier
	s_waitcnt lgkmcnt(0)
	v_mfma_scale_f32_16x16x128_f8f6f4 v[158:161], v[2:9], v[198:205], v[158:161], v1, v1 op_sel_hi:[0,0,0]
	v_mfma_scale_f32_16x16x128_f8f6f4 v[154:157], v[10:17], v[198:205], v[154:157], v1, v1 op_sel_hi:[0,0,0]
	v_mfma_scale_f32_16x16x128_f8f6f4 v[150:153], v[2:9], v[206:213], v[150:153], v1, v1 op_sel_hi:[0,0,0]
	v_mfma_scale_f32_16x16x128_f8f6f4 v[142:145], v[10:17], v[206:213], v[142:145], v1, v1 op_sel_hi:[0,0,0]
	v_mfma_scale_f32_16x16x128_f8f6f4 v[134:137], v[2:9], v[214:221], v[134:137], v1, v1 op_sel_hi:[0,0,0]
	v_mfma_scale_f32_16x16x128_f8f6f4 v[126:129], v[10:17], v[214:221], v[126:129], v1, v1 op_sel_hi:[0,0,0]
	v_mfma_scale_f32_16x16x128_f8f6f4 v[118:121], v[2:9], v[222:229], v[118:121], v1, v1 op_sel_hi:[0,0,0]
	v_mfma_scale_f32_16x16x128_f8f6f4 v[110:113], v[10:17], v[222:229], v[110:113], v1, v1 op_sel_hi:[0,0,0]
	v_mfma_scale_f32_16x16x128_f8f6f4 v[146:149], v[18:25], v[198:205], v[146:149], v1, v1 op_sel_hi:[0,0,0]
	v_mfma_scale_f32_16x16x128_f8f6f4 v[138:141], v[26:33], v[198:205], v[138:141], v1, v1 op_sel_hi:[0,0,0]
	v_mfma_scale_f32_16x16x128_f8f6f4 v[130:133], v[18:25], v[206:213], v[130:133], v1, v1 op_sel_hi:[0,0,0]
	v_mfma_scale_f32_16x16x128_f8f6f4 v[122:125], v[26:33], v[206:213], v[122:125], v1, v1 op_sel_hi:[0,0,0]
	v_mfma_scale_f32_16x16x128_f8f6f4 v[114:117], v[18:25], v[214:221], v[114:117], v1, v1 op_sel_hi:[0,0,0]
	v_mfma_scale_f32_16x16x128_f8f6f4 v[106:109], v[26:33], v[214:221], v[106:109], v1, v1 op_sel_hi:[0,0,0]
	v_mfma_scale_f32_16x16x128_f8f6f4 v[102:105], v[18:25], v[222:229], v[102:105], v1, v1 op_sel_hi:[0,0,0]
	v_mfma_scale_f32_16x16x128_f8f6f4 v[98:101], v[26:33], v[222:229], v[98:101], v1, v1 op_sel_hi:[0,0,0]
	s_barrier
	s_add_i32 s42, s44, s46
	v_lshl_add_u64 v[182:183], v[182:183], 0, s[10:11]
	s_mov_b32 m0, s42
	ds_read_b128 v[198:201], v196 offset:49152
	ds_read_b128 v[202:205], v196 offset:50176
	ds_read_b128 v[206:209], v196 offset:51200
	ds_read_b128 v[210:213], v196 offset:52224
	ds_read_b128 v[214:217], v196 offset:53248
	ds_read_b128 v[218:221], v196 offset:54272
	ds_read_b128 v[222:225], v196 offset:55296
	ds_read_b128 v[226:229], v196 offset:56320
	global_load_lds_dwordx4 v[182:183], off
	s_add_i32 m0, s42, 0x2000
	s_add_u32 s40, s40, 0x40080
	v_lshl_add_u64 v[182:183], v[184:185], 0, s[10:11]
	s_addc_u32 s41, s41, 0
	s_add_i32 s42, s45, s46
	global_load_lds_dwordx4 v[182:183], off
	v_lshl_add_u64 v[182:183], s[40:41], 0, v[162:163]
	s_mov_b32 m0, s42
	s_nop 0
	global_load_lds_dwordx4 v[182:183], off
	v_lshl_add_u64 v[182:183], s[40:41], 0, v[164:165]
	s_add_i32 m0, s42, 0x2000
	s_nop 0
	global_load_lds_dwordx4 v[182:183], off
	v_lshl_add_u64 v[182:183], v[186:187], 0, s[10:11]
	s_mov_b32 m0, s54
	s_nop 0
	global_load_lds_dwordx4 v[182:183], off
	v_lshl_add_u64 v[182:183], v[188:189], 0, s[10:11]
	s_mov_b32 m0, s55
	s_nop 0
	global_load_lds_dwordx4 v[182:183], off
	s_waitcnt vmcnt(8)
	s_waitcnt lgkmcnt(0)
	s_barrier
	s_waitcnt lgkmcnt(0)
	v_mfma_scale_f32_16x16x128_f8f6f4 v[94:97], v[2:9], v[198:205], v[94:97], v1, v1 op_sel_hi:[0,0,0]
	v_mfma_scale_f32_16x16x128_f8f6f4 v[90:93], v[10:17], v[198:205], v[90:93], v1, v1 op_sel_hi:[0,0,0]
	v_mfma_scale_f32_16x16x128_f8f6f4 v[86:89], v[2:9], v[206:213], v[86:89], v1, v1 op_sel_hi:[0,0,0]
	v_mfma_scale_f32_16x16x128_f8f6f4 v[78:81], v[10:17], v[206:213], v[78:81], v1, v1 op_sel_hi:[0,0,0]
	v_mfma_scale_f32_16x16x128_f8f6f4 v[62:65], v[2:9], v[214:221], v[62:65], v1, v1 op_sel_hi:[0,0,0]
	v_mfma_scale_f32_16x16x128_f8f6f4 v[54:57], v[10:17], v[214:221], v[54:57], v1, v1 op_sel_hi:[0,0,0]
	v_mfma_scale_f32_16x16x128_f8f6f4 v[46:49], v[2:9], v[222:229], v[46:49], v1, v1 op_sel_hi:[0,0,0]
	v_mfma_scale_f32_16x16x128_f8f6f4 v[38:41], v[10:17], v[222:229], v[38:41], v1, v1 op_sel_hi:[0,0,0]
	v_mfma_scale_f32_16x16x128_f8f6f4 v[82:85], v[18:25], v[198:205], v[82:85], v1, v1 op_sel_hi:[0,0,0]
	v_mfma_scale_f32_16x16x128_f8f6f4 v[74:77], v[26:33], v[198:205], v[74:77], v1, v1 op_sel_hi:[0,0,0]
	v_mfma_scale_f32_16x16x128_f8f6f4 v[58:61], v[18:25], v[206:213], v[58:61], v1, v1 op_sel_hi:[0,0,0]
	v_mfma_scale_f32_16x16x128_f8f6f4 v[50:53], v[26:33], v[206:213], v[50:53], v1, v1 op_sel_hi:[0,0,0]
	v_mfma_scale_f32_16x16x128_f8f6f4 v[42:45], v[18:25], v[214:221], v[42:45], v1, v1 op_sel_hi:[0,0,0]
	v_mfma_scale_f32_16x16x128_f8f6f4 v[34:37], v[26:33], v[214:221], v[34:37], v1, v1 op_sel_hi:[0,0,0]
	v_mfma_scale_f32_16x16x128_f8f6f4 v[70:73], v[18:25], v[222:229], v[70:73], v1, v1 op_sel_hi:[0,0,0]
	v_mfma_scale_f32_16x16x128_f8f6f4 v[66:69], v[26:33], v[222:229], v[66:69], v1, v1 op_sel_hi:[0,0,0]
	s_barrier
	s_add_i32 s70, s70, 2
	s_cmp_gt_u32 s70, 13
	s_mov_b64 s[42:43], s[38:39]
	s_cbranch_scc0 .LBB0_2108
	s_and_b64 vcc, exec, s[12:13]
	s_cbranch_vccz .LBB0_2111
	s_barrier

; #define PG8_STAGE(bufoff, gbase, voff) do { _Pragma("unroll") for (int _i = 0; _i < 2; ++_i) \
;         __builtin_amdgcn_global_load_lds((const unsigned*)((const char*)(gbase) + (voff)[_i]), (LAS unsigned*)(lds + (bufoff) + ldsw + _i * 8192), 16, 0, 0); } while (0)
; #define PG8_LDA(dst, b, h) do { _Pragma("unroll") for (int m = 0; m < 4; ++m) dst[m] = PG8_LD32(lds + PG8_SA(b, h) + aoff + m * 2048); } while (0)
; #define PG8_LDB(dst, b, h) do { _Pragma("unroll") for (int n = 0; n < 2; ++n) dst[n] = PG8_LD32(lds + PG8_SB(b, h) + boff + n * 2048); } while (0)
; #define PG8_WAIT_V(n) asm volatile("s_waitcnt vmcnt(" #n ")" ::: "memory")
; #define PG8_WAIT_L(n) asm volatile("s_waitcnt lgkmcnt(" #n ")" ::: "memory")
; #define PG8_BAR __builtin_amdgcn_s_barrier()
; #define PG8_SCHED __builtin_amdgcn_sched_barrier(0)
; template <class Epi, class Sched, bool ALIGN_EPI, int DT>
; __device__ __forceinline__ void gemm_phase(LAS unsigned char* lds, const int KB, const Sched& S, const Epi& E) {
;     ...
;             const size_t k1 = (size_t)(t + 1) * kstep, k2 = last ? 0 : (size_t)(t + 2) * kstep, k3 = k2 + kstep;
;             const char* b2 = last ? nB : cB + (size_t)(t + 2) * kstep; const char* b3 = b2 + kstep;
;             PG8_LDB(B0, 0, 0); PG8_LDB(B1, 0, 1); PG8_SCHED; PG8_LDA(At, 0, 0); PG8_STA(PG8_SA(1, 1), false, 1, k1);
;             PG8_WAIT_V(8); PG8_WAIT_L(0); PG8_BAR; PG8_MMA(0, 0, At, B0); PG8_MMA(0, 1, At, B1); PG8_BAR; PG8_SCHED;
;             PG8_LDA(At, 0, 1); PG8_STAGE(PG8_SB(0, 0), b2, voffB); PG8_STAGE(PG8_SB(0, 1), b2 + hstep, voffB); PG8_STA(PG8_SA(0, 0), last, 0, k2);
;             PG8_WAIT_V(8); PG8_WAIT_L(0); PG8_BAR; PG8_MMA(1, 0, At, B0); PG8_MMA(1, 1, At, B1); PG8_BAR; PG8_SCHED;
;             PG8_LDB(B0, 1, 0); PG8_LDB(B1, 1, 1); PG8_SCHED; PG8_LDA(At, 1, 0); PG8_STA(PG8_SA(0, 1), last, 1, k2);
;             PG8_WAIT_V(8); PG8_WAIT_L(0); PG8_BAR; PG8_MMA(0, 0, At, B0); PG8_MMA(0, 1, At, B1); PG8_BAR; PG8_SCHED;
;             PG8_LDA(At, 1, 1); PG8_STAGE(PG8_SB(1, 0), b3, voffB); PG8_STAGE(PG8_SB(1, 1), b3 + hstep, voffB); PG8_STA(PG8_SA(1, 0), last, 0, k3);
;             PG8_WAIT_V(8); PG8_WAIT_L(0); PG8_BAR; PG8_MMA(1, 0, At, B0); PG8_MMA(1, 1, At, B1); PG8_BAR; PG8_SCHED;
;         }
.LBB0_2294:
	v_add_u32_e32 v79, s65, v167
	ds_read_b128 v[142:145], v79
	ds_read_b128 v[156:159], v79 offset:1024
	ds_read_b128 v[178:181], v79 offset:2048
	ds_read_b128 v[182:185], v79 offset:3072
	v_add_u32_e32 v79, s66, v167
	ds_read_b128 v[186:189], v79
	ds_read_b128 v[190:193], v79 offset:1024
	ds_read_b128 v[196:199], v79 offset:2048
	ds_read_b128 v[200:203], v79 offset:3072
	s_add_u32 s40, s8, 0x100
	s_addc_u32 s41, s9, 0
	s_cmpk_eq_i32 s8, 0x700
	s_cselect_b64 vcc, -1, 0
	v_lshl_add_u64 v[160:161], v[88:89], 0, s[8:9]
	s_and_b64 s[76:77], vcc, exec
	v_cndmask_b32_e32 v161, v161, v155, vcc
	s_cselect_b32 s75, 0, s40
	v_cndmask_b32_e32 v160, v160, v154, vcc
	v_lshl_add_u64 v[236:237], v[140:141], 0, s[8:9]
	s_add_i32 m0, s42, 0xc000
	ds_read_b128 v[204:207], v169
	ds_read_b128 v[208:211], v169 offset:1024
	ds_read_b128 v[212:215], v169 offset:2048
	ds_read_b128 v[216:219], v169 offset:3072
	ds_read_b128 v[220:223], v169 offset:4096
	ds_read_b128 v[224:227], v169 offset:5120
	ds_read_b128 v[228:231], v169 offset:6144
	ds_read_b128 v[232:235], v169 offset:7168
	global_load_lds_dwordx4 v[236:237], off
	v_lshl_add_u64 v[236:237], v[138:139], 0, s[8:9]
	s_add_i32 m0, s42, 0xe000
	s_nop 0
	global_load_lds_dwordx4 v[236:237], off
	s_waitcnt vmcnt(8)
	s_waitcnt lgkmcnt(0)
	s_barrier
	s_waitcnt lgkmcnt(0)
	v_mfma_i32_16x16x64_i8 v[134:137], v[142:145], v[204:207], v[134:137]
	v_mfma_i32_16x16x64_i8 v[126:129], v[178:181], v[204:207], v[126:129]
	v_mfma_i32_16x16x64_i8 v[118:121], v[142:145], v[212:215], v[118:121]
	v_mfma_i32_16x16x64_i8 v[110:113], v[178:181], v[212:215], v[110:113]
	v_mfma_i32_16x16x64_i8 v[102:105], v[142:145], v[220:223], v[102:105]
	v_mfma_i32_16x16x64_i8 v[94:97], v[178:181], v[220:223], v[94:97]
	v_mfma_i32_16x16x64_i8 v[82:85], v[142:145], v[228:231], v[82:85]
	v_mfma_i32_16x16x64_i8 v[70:73], v[178:181], v[228:231], v[70:73]
	v_mfma_i32_16x16x64_i8 v[134:137], v[156:159], v[208:211], v[134:137]
	v_mfma_i32_16x16x64_i8 v[126:129], v[182:185], v[208:211], v[126:129]
	v_mfma_i32_16x16x64_i8 v[118:121], v[156:159], v[216:219], v[118:121]
	v_mfma_i32_16x16x64_i8 v[110:113], v[182:185], v[216:219], v[110:113]
	v_mfma_i32_16x16x64_i8 v[102:105], v[156:159], v[224:227], v[102:105]
	v_mfma_i32_16x16x64_i8 v[94:97], v[182:185], v[224:227], v[94:97]
	v_mfma_i32_16x16x64_i8 v[82:85], v[156:159], v[232:235], v[82:85]
	v_mfma_i32_16x16x64_i8 v[70:73], v[182:185], v[232:235], v[70:73]
	v_mfma_i32_16x16x64_i8 v[130:133], v[186:189], v[204:207], v[130:133]
	v_mfma_i32_16x16x64_i8 v[122:125], v[196:199], v[204:207], v[122:125]
	v_mfma_i32_16x16x64_i8 v[114:117], v[186:189], v[212:215], v[114:117]
	v_mfma_i32_16x16x64_i8 v[106:109], v[196:199], v[212:215], v[106:109]
	v_mfma_i32_16x16x64_i8 v[98:101], v[186:189], v[220:223], v[98:101]
	v_mfma_i32_16x16x64_i8 v[90:93], v[196:199], v[220:223], v[90:93]
	v_mfma_i32_16x16x64_i8 v[74:77], v[186:189], v[228:231], v[74:77]
	v_mfma_i32_16x16x64_i8 v[66:69], v[196:199], v[228:231], v[66:69]
	v_mfma_i32_16x16x64_i8 v[130:133], v[190:193], v[208:211], v[130:133]
	v_mfma_i32_16x16x64_i8 v[122:125], v[200:203], v[208:211], v[122:125]
	v_mfma_i32_16x16x64_i8 v[114:117], v[190:193], v[216:219], v[114:117]
	v_mfma_i32_16x16x64_i8 v[106:109], v[200:203], v[216:219], v[106:109]
	v_mfma_i32_16x16x64_i8 v[98:101], v[190:193], v[224:227], v[98:101]
	v_mfma_i32_16x16x64_i8 v[90:93], v[200:203], v[224:227], v[90:93]
	v_mfma_i32_16x16x64_i8 v[74:77], v[190:193], v[232:235], v[74:77]
	v_mfma_i32_16x16x64_i8 v[66:69], v[200:203], v[232:235], v[66:69]
	s_barrier
	s_add_i32 s8, s65, s33
	v_lshl_add_u64 v[236:237], v[160:161], 0, v[148:149]
	s_mov_b32 m0, s8
	ds_read_b128 v[204:207], v169 offset:16384
	ds_read_b128 v[208:211], v169 offset:17408
	ds_read_b128 v[212:215], v169 offset:18432
	ds_read_b128 v[216:219], v169 offset:19456
	ds_read_b128 v[220:223], v169 offset:20480
	ds_read_b128 v[224:227], v169 offset:21504
	ds_read_b128 v[228:231], v169 offset:22528
	ds_read_b128 v[232:235], v169 offset:23552
	global_load_lds_dwordx4 v[236:237], off
	v_lshl_add_u64 v[238:239], v[160:161], 0, v[150:151]
	s_add_i32 m0, s8, 0x2000
	v_lshl_add_u64 v[240:241], v[160:161], 0, s[10:11]
	s_add_i32 s8, s66, s33
	global_load_lds_dwordx4 v[238:239], off
	v_lshl_add_u64 v[242:243], v[240:241], 0, v[148:149]
	s_mov_b32 m0, s8
	v_lshl_add_u64 v[240:241], v[240:241], 0, v[150:151]
	global_load_lds_dwordx4 v[242:243], off
	s_add_i32 m0, s8, 0x2000
	s_add_u32 s8, s60, s75
	global_load_lds_dwordx4 v[240:241], off
	v_cndmask_b32_e32 v146, v81, v173, vcc
	s_addc_u32 s9, s61, 0
	s_mov_b32 m0, s42
	v_cndmask_b32_e32 v240, v80, v174, vcc
	global_load_lds_dwordx4 v146, s[8:9]
	s_mov_b32 m0, s43
	v_mov_b32_e32 v241, v147
	global_load_lds_dwordx4 v240, s[8:9]
	s_waitcnt vmcnt(8)
	s_waitcnt lgkmcnt(0)
	v_lshl_add_u64 v[242:243], s[8:9], 0, v[146:147]
	v_lshl_add_u64 v[240:241], s[8:9], 0, v[240:241]
	s_barrier
; #define PG8_STAGE(bufoff, gbase, voff) do { _Pragma("unroll") for (int _i = 0; _i < 2; ++_i) \
;         __builtin_amdgcn_global_load_lds((const unsigned*)((const char*)(gbase) + (voff)[_i]), (LAS unsigned*)(lds + (bufoff) + ldsw + _i * 8192), 16, 0, 0); } while (0)
; #define PG8_LDA(dst, b, h) do { _Pragma("unroll") for (int m = 0; m < 4; ++m) dst[m] = PG8_LD32(lds + PG8_SA(b, h) + aoff + m * 2048); } while (0)
; #define PG8_LDB(dst, b, h) do { _Pragma("unroll") for (int n = 0; n < 2; ++n) dst[n] = PG8_LD32(lds + PG8_SB(b, h) + boff + n * 2048); } while (0)
; #define PG8_WAIT_V(n) asm volatile("s_waitcnt vmcnt(" #n ")" ::: "memory")
; #define PG8_WAIT_L(n) asm volatile("s_waitcnt lgkmcnt(" #n ")" ::: "memory")
; #define PG8_BAR __builtin_amdgcn_s_barrier()
; #define PG8_SCHED __builtin_amdgcn_sched_barrier(0)
; template <class Epi, class Sched, bool ALIGN_EPI, int DT>
; __device__ __forceinline__ void gemm_phase(LAS unsigned char* lds, const int KB, const Sched& S, const Epi& E) {
;     ...
;             const size_t k1 = (size_t)(t + 1) * kstep, k2 = last ? 0 : (size_t)(t + 2) * kstep, k3 = k2 + kstep;
;             const char* b2 = last ? nB : cB + (size_t)(t + 2) * kstep; const char* b3 = b2 + kstep;
;             PG8_LDB(B0, 0, 0); PG8_LDB(B1, 0, 1); PG8_SCHED; PG8_LDA(At, 0, 0); PG8_STA(PG8_SA(1, 1), false, 1, k1);
;             PG8_WAIT_V(8); PG8_WAIT_L(0); PG8_BAR; PG8_MMA(0, 0, At, B0); PG8_MMA(0, 1, At, B1); PG8_BAR; PG8_SCHED;
;             PG8_LDA(At, 0, 1); PG8_STAGE(PG8_SB(0, 0), b2, voffB); PG8_STAGE(PG8_SB(0, 1), b2 + hstep, voffB); PG8_STA(PG8_SA(0, 0), last, 0, k2);
;             PG8_WAIT_V(8); PG8_WAIT_L(0); PG8_BAR; PG8_MMA(1, 0, At, B0); PG8_MMA(1, 1, At, B1); PG8_BAR; PG8_SCHED;
;             PG8_LDB(B0, 1, 0); PG8_LDB(B1, 1, 1); PG8_SCHED; PG8_LDA(At, 1, 0); PG8_STA(PG8_SA(0, 1), last, 1, k2);
;             PG8_WAIT_V(8); PG8_WAIT_L(0); PG8_BAR; PG8_MMA(0, 0, At, B0); PG8_MMA(0, 1, At, B1); PG8_BAR; PG8_SCHED;
;             PG8_LDA(At, 1, 1); PG8_STAGE(PG8_SB(1, 0), b3, voffB); PG8_STAGE(PG8_SB(1, 1), b3 + hstep, voffB); PG8_STA(PG8_SA(1, 0), last, 0, k3);
;             PG8_WAIT_V(8); PG8_WAIT_L(0); PG8_BAR; PG8_MMA(1, 0, At, B0); PG8_MMA(1, 1, At, B1); PG8_BAR; PG8_SCHED;
;         }
	s_waitcnt lgkmcnt(0)
	v_mfma_i32_16x16x64_i8 v[54:57], v[142:145], v[204:207], v[54:57]
	v_mfma_i32_16x16x64_i8 v[50:53], v[178:181], v[204:207], v[50:53]
	v_mfma_i32_16x16x64_i8 v[42:45], v[142:145], v[212:215], v[42:45]
	v_mfma_i32_16x16x64_i8 v[34:37], v[178:181], v[212:215], v[34:37]
	v_mfma_i32_16x16x64_i8 v[26:29], v[142:145], v[220:223], v[26:29]
	v_mfma_i32_16x16x64_i8 v[18:21], v[178:181], v[220:223], v[18:21]
	v_mfma_i32_16x16x64_i8 v[10:13], v[142:145], v[228:231], v[10:13]
	v_mfma_i32_16x16x64_i8 v[2:5], v[178:181], v[228:231], v[2:5]
	v_mfma_i32_16x16x64_i8 v[54:57], v[156:159], v[208:211], v[54:57]
	v_mfma_i32_16x16x64_i8 v[50:53], v[182:185], v[208:211], v[50:53]
	v_mfma_i32_16x16x64_i8 v[42:45], v[156:159], v[216:219], v[42:45]
	v_mfma_i32_16x16x64_i8 v[34:37], v[182:185], v[216:219], v[34:37]
	v_mfma_i32_16x16x64_i8 v[26:29], v[156:159], v[224:227], v[26:29]
	v_mfma_i32_16x16x64_i8 v[18:21], v[182:185], v[224:227], v[18:21]
	v_mfma_i32_16x16x64_i8 v[10:13], v[156:159], v[232:235], v[10:13]
	v_mfma_i32_16x16x64_i8 v[2:5], v[182:185], v[232:235], v[2:5]
	v_mfma_i32_16x16x64_i8 v[62:65], v[186:189], v[204:207], v[62:65]
	v_mfma_i32_16x16x64_i8 v[58:61], v[196:199], v[204:207], v[58:61]
	v_mfma_i32_16x16x64_i8 v[46:49], v[186:189], v[212:215], v[46:49]
	v_mfma_i32_16x16x64_i8 v[38:41], v[196:199], v[212:215], v[38:41]
	v_mfma_i32_16x16x64_i8 v[30:33], v[186:189], v[220:223], v[30:33]
	v_mfma_i32_16x16x64_i8 v[22:25], v[196:199], v[220:223], v[22:25]
	v_mfma_i32_16x16x64_i8 v[14:17], v[186:189], v[228:231], v[14:17]
	v_mfma_i32_16x16x64_i8 v[6:9], v[196:199], v[228:231], v[6:9]
	v_mfma_i32_16x16x64_i8 v[62:65], v[190:193], v[208:211], v[62:65]
	v_mfma_i32_16x16x64_i8 v[58:61], v[200:203], v[208:211], v[58:61]
	v_mfma_i32_16x16x64_i8 v[46:49], v[190:193], v[216:219], v[46:49]
	v_mfma_i32_16x16x64_i8 v[38:41], v[200:203], v[216:219], v[38:41]
	v_mfma_i32_16x16x64_i8 v[30:33], v[190:193], v[224:227], v[30:33]
	v_mfma_i32_16x16x64_i8 v[22:25], v[200:203], v[224:227], v[22:25]
	v_mfma_i32_16x16x64_i8 v[14:17], v[190:193], v[232:235], v[14:17]
	v_mfma_i32_16x16x64_i8 v[6:9], v[200:203], v[232:235], v[6:9]
	s_barrier
	s_add_i32 s75, 0, 0x18000
	v_add_u32_e32 v79, s75, v167
	s_add_i32 s76, 0, 0x1c000
	ds_read_b128 v[142:145], v79
	ds_read_b128 v[156:159], v79 offset:1024
	ds_read_b128 v[178:181], v79 offset:2048
	ds_read_b128 v[182:185], v79 offset:3072
	v_add_u32_e32 v79, s76, v167
	ds_read_b128 v[186:189], v79
	ds_read_b128 v[190:193], v79 offset:1024
	ds_read_b128 v[196:199], v79 offset:2048
	ds_read_b128 v[200:203], v79 offset:3072
	s_mov_b32 m0, s44
	v_cndmask_b32_e32 v79, v78, v175, vcc
	ds_read_b128 v[204:207], v169 offset:32768
	ds_read_b128 v[208:211], v169 offset:33792
	ds_read_b128 v[212:215], v169 offset:34816
	ds_read_b128 v[216:219], v169 offset:35840
	ds_read_b128 v[220:223], v169 offset:36864
	ds_read_b128 v[224:227], v169 offset:37888
	ds_read_b128 v[228:231], v169 offset:38912
	ds_read_b128 v[232:235], v169 offset:39936
	v_cndmask_b32_e32 v87, v86, v176, vcc
	global_load_lds_dwordx4 v79, s[8:9]
	s_mov_b32 m0, s45
	s_nop 0
	global_load_lds_dwordx4 v87, s[8:9]
	s_waitcnt vmcnt(8)
	s_waitcnt lgkmcnt(0)
	s_barrier
	s_waitcnt lgkmcnt(0)
	v_mfma_i32_16x16x64_i8 v[134:137], v[142:145], v[204:207], v[134:137]
	v_mfma_i32_16x16x64_i8 v[126:129], v[178:181], v[204:207], v[126:129]
	v_mfma_i32_16x16x64_i8 v[118:121], v[142:145], v[212:215], v[118:121]
	v_mfma_i32_16x16x64_i8 v[110:113], v[178:181], v[212:215], v[110:113]
	v_mfma_i32_16x16x64_i8 v[102:105], v[142:145], v[220:223], v[102:105]
	v_mfma_i32_16x16x64_i8 v[94:97], v[178:181], v[220:223], v[94:97]
	v_mfma_i32_16x16x64_i8 v[82:85], v[142:145], v[228:231], v[82:85]
	v_mfma_i32_16x16x64_i8 v[70:73], v[178:181], v[228:231], v[70:73]
	v_mfma_i32_16x16x64_i8 v[134:137], v[156:159], v[208:211], v[134:137]
	v_mfma_i32_16x16x64_i8 v[126:129], v[182:185], v[208:211], v[126:129]
	v_mfma_i32_16x16x64_i8 v[118:121], v[156:159], v[216:219], v[118:121]
	v_mfma_i32_16x16x64_i8 v[110:113], v[182:185], v[216:219], v[110:113]
	v_mfma_i32_16x16x64_i8 v[102:105], v[156:159], v[224:227], v[102:105]
	v_mfma_i32_16x16x64_i8 v[94:97], v[182:185], v[224:227], v[94:97]
	v_mfma_i32_16x16x64_i8 v[82:85], v[156:159], v[232:235], v[82:85]
	v_mfma_i32_16x16x64_i8 v[70:73], v[182:185], v[232:235], v[70:73]
	v_mfma_i32_16x16x64_i8 v[130:133], v[186:189], v[204:207], v[130:133]
	v_mfma_i32_16x16x64_i8 v[122:125], v[196:199], v[204:207], v[122:125]
	v_mfma_i32_16x16x64_i8 v[114:117], v[186:189], v[212:215], v[114:117]
	v_mfma_i32_16x16x64_i8 v[106:109], v[196:199], v[212:215], v[106:109]
	v_mfma_i32_16x16x64_i8 v[98:101], v[186:189], v[220:223], v[98:101]
	v_mfma_i32_16x16x64_i8 v[90:93], v[196:199], v[220:223], v[90:93]
	v_mfma_i32_16x16x64_i8 v[74:77], v[186:189], v[228:231], v[74:77]
	v_mfma_i32_16x16x64_i8 v[66:69], v[196:199], v[228:231], v[66:69]
	v_mfma_i32_16x16x64_i8 v[130:133], v[190:193], v[208:211], v[130:133]
	v_mfma_i32_16x16x64_i8 v[122:125], v[200:203], v[208:211], v[122:125]
	v_mfma_i32_16x16x64_i8 v[114:117], v[190:193], v[216:219], v[114:117]
	v_mfma_i32_16x16x64_i8 v[106:109], v[200:203], v[216:219], v[106:109]
	v_mfma_i32_16x16x64_i8 v[98:101], v[190:193], v[224:227], v[98:101]
	v_mfma_i32_16x16x64_i8 v[90:93], v[200:203], v[224:227], v[90:93]
	v_mfma_i32_16x16x64_i8 v[74:77], v[190:193], v[232:235], v[74:77]
	v_mfma_i32_16x16x64_i8 v[66:69], v[200:203], v[232:235], v[66:69]
	s_barrier
; #define PG8_STAGE(bufoff, gbase, voff) do { _Pragma("unroll") for (int _i = 0; _i < 2; ++_i) \
;         __builtin_amdgcn_global_load_lds((const unsigned*)((const char*)(gbase) + (voff)[_i]), (LAS unsigned*)(lds + (bufoff) + ldsw + _i * 8192), 16, 0, 0); } while (0)
; #define PG8_LDA(dst, b, h) do { _Pragma("unroll") for (int m = 0; m < 4; ++m) dst[m] = PG8_LD32(lds + PG8_SA(b, h) + aoff + m * 2048); } while (0)
; #define PG8_LDB(dst, b, h) do { _Pragma("unroll") for (int n = 0; n < 2; ++n) dst[n] = PG8_LD32(lds + PG8_SB(b, h) + boff + n * 2048); } while (0)
; #define PG8_WAIT_V(n) asm volatile("s_waitcnt vmcnt(" #n ")" ::: "memory")
; #define PG8_WAIT_L(n) asm volatile("s_waitcnt lgkmcnt(" #n ")" ::: "memory")
; #define PG8_BAR __builtin_amdgcn_s_barrier()
; #define PG8_SCHED __builtin_amdgcn_sched_barrier(0)
; template <class Epi, class Sched, bool ALIGN_EPI, int DT>
; __device__ __forceinline__ void gemm_phase(LAS unsigned char* lds, const int KB, const Sched& S, const Epi& E) {
;     ...
;             const size_t k1 = (size_t)(t + 1) * kstep, k2 = last ? 0 : (size_t)(t + 2) * kstep, k3 = k2 + kstep;
;             const char* b2 = last ? nB : cB + (size_t)(t + 2) * kstep; const char* b3 = b2 + kstep;
;             PG8_LDB(B0, 0, 0); PG8_LDB(B1, 0, 1); PG8_SCHED; PG8_LDA(At, 0, 0); PG8_STA(PG8_SA(1, 1), false, 1, k1);
;             PG8_WAIT_V(8); PG8_WAIT_L(0); PG8_BAR; PG8_MMA(0, 0, At, B0); PG8_MMA(0, 1, At, B1); PG8_BAR; PG8_SCHED;
;             PG8_LDA(At, 0, 1); PG8_STAGE(PG8_SB(0, 0), b2, voffB); PG8_STAGE(PG8_SB(0, 1), b2 + hstep, voffB); PG8_STA(PG8_SA(0, 0), last, 0, k2);
;             PG8_WAIT_V(8); PG8_WAIT_L(0); PG8_BAR; PG8_MMA(1, 0, At, B0); PG8_MMA(1, 1, At, B1); PG8_BAR; PG8_SCHED;
;             PG8_LDB(B0, 1, 0); PG8_LDB(B1, 1, 1); PG8_SCHED; PG8_LDA(At, 1, 0); PG8_STA(PG8_SA(0, 1), last, 1, k2);
;             PG8_WAIT_V(8); PG8_WAIT_L(0); PG8_BAR; PG8_MMA(0, 0, At, B0); PG8_MMA(0, 1, At, B1); PG8_BAR; PG8_SCHED;
;             PG8_LDA(At, 1, 1); PG8_STAGE(PG8_SB(1, 0), b3, voffB); PG8_STAGE(PG8_SB(1, 1), b3 + hstep, voffB); PG8_STA(PG8_SA(1, 0), last, 0, k3);
;             PG8_WAIT_V(8); PG8_WAIT_L(0); PG8_BAR; PG8_MMA(1, 0, At, B0); PG8_MMA(1, 1, At, B1); PG8_BAR; PG8_SCHED;
;         }
	s_add_i32 s8, s75, s33
	v_lshl_add_u64 v[236:237], v[236:237], 0, s[20:21]
	s_mov_b32 m0, s8
	ds_read_b128 v[204:207], v169 offset:49152
	ds_read_b128 v[208:211], v169 offset:50176
	ds_read_b128 v[212:215], v169 offset:51200
	ds_read_b128 v[216:219], v169 offset:52224
	ds_read_b128 v[220:223], v169 offset:53248
	ds_read_b128 v[224:227], v169 offset:54272
	ds_read_b128 v[228:231], v169 offset:55296
	ds_read_b128 v[232:235], v169 offset:56320
	global_load_lds_dwordx4 v[236:237], off
	v_lshl_add_u64 v[236:237], v[238:239], 0, s[20:21]
	s_add_i32 m0, s8, 0x2000
	v_lshl_add_u64 v[160:161], v[160:161], 0, s[24:25]
	s_add_i32 s8, s76, s33
	global_load_lds_dwordx4 v[236:237], off
	v_lshl_add_u64 v[236:237], v[160:161], 0, v[148:149]
	s_mov_b32 m0, s8
	v_lshl_add_u64 v[160:161], v[160:161], 0, v[150:151]
	global_load_lds_dwordx4 v[236:237], off
	s_add_i32 m0, s8, 0x2000
	s_nop 0
	global_load_lds_dwordx4 v[160:161], off
	v_lshl_add_u64 v[160:161], v[242:243], 0, s[20:21]
	s_mov_b32 m0, s46
	s_nop 0
	global_load_lds_dwordx4 v[160:161], off
	v_lshl_add_u64 v[160:161], v[240:241], 0, s[20:21]
	s_mov_b32 m0, s47
	s_nop 0
	global_load_lds_dwordx4 v[160:161], off
	s_waitcnt vmcnt(8)
	s_waitcnt lgkmcnt(0)
	s_barrier
	s_waitcnt lgkmcnt(0)
	v_mfma_i32_16x16x64_i8 v[54:57], v[142:145], v[204:207], v[54:57]
	v_mfma_i32_16x16x64_i8 v[50:53], v[178:181], v[204:207], v[50:53]
	v_mfma_i32_16x16x64_i8 v[42:45], v[142:145], v[212:215], v[42:45]
	v_mfma_i32_16x16x64_i8 v[34:37], v[178:181], v[212:215], v[34:37]
	v_mfma_i32_16x16x64_i8 v[26:29], v[142:145], v[220:223], v[26:29]
	v_mfma_i32_16x16x64_i8 v[18:21], v[178:181], v[220:223], v[18:21]
	v_mfma_i32_16x16x64_i8 v[10:13], v[142:145], v[228:231], v[10:13]
	v_mfma_i32_16x16x64_i8 v[2:5], v[178:181], v[228:231], v[2:5]
	v_mfma_i32_16x16x64_i8 v[54:57], v[156:159], v[208:211], v[54:57]
	v_mfma_i32_16x16x64_i8 v[50:53], v[182:185], v[208:211], v[50:53]
	v_mfma_i32_16x16x64_i8 v[42:45], v[156:159], v[216:219], v[42:45]
	v_mfma_i32_16x16x64_i8 v[34:37], v[182:185], v[216:219], v[34:37]
	v_mfma_i32_16x16x64_i8 v[26:29], v[156:159], v[224:227], v[26:29]
	v_mfma_i32_16x16x64_i8 v[18:21], v[182:185], v[224:227], v[18:21]
	v_mfma_i32_16x16x64_i8 v[10:13], v[156:159], v[232:235], v[10:13]
	v_mfma_i32_16x16x64_i8 v[2:5], v[182:185], v[232:235], v[2:5]
	v_mfma_i32_16x16x64_i8 v[62:65], v[186:189], v[204:207], v[62:65]
	v_mfma_i32_16x16x64_i8 v[58:61], v[196:199], v[204:207], v[58:61]
	v_mfma_i32_16x16x64_i8 v[46:49], v[186:189], v[212:215], v[46:49]
	v_mfma_i32_16x16x64_i8 v[38:41], v[196:199], v[212:215], v[38:41]
	v_mfma_i32_16x16x64_i8 v[30:33], v[186:189], v[220:223], v[30:33]
	v_mfma_i32_16x16x64_i8 v[22:25], v[196:199], v[220:223], v[22:25]
	v_mfma_i32_16x16x64_i8 v[14:17], v[186:189], v[228:231], v[14:17]
	v_mfma_i32_16x16x64_i8 v[6:9], v[196:199], v[228:231], v[6:9]
	v_mfma_i32_16x16x64_i8 v[62:65], v[190:193], v[208:211], v[62:65]
	v_mfma_i32_16x16x64_i8 v[58:61], v[200:203], v[208:211], v[58:61]
	v_mfma_i32_16x16x64_i8 v[46:49], v[190:193], v[216:219], v[46:49]
	v_mfma_i32_16x16x64_i8 v[38:41], v[200:203], v[216:219], v[38:41]
	v_mfma_i32_16x16x64_i8 v[30:33], v[190:193], v[224:227], v[30:33]
	v_mfma_i32_16x16x64_i8 v[22:25], v[200:203], v[224:227], v[22:25]
	v_mfma_i32_16x16x64_i8 v[14:17], v[190:193], v[232:235], v[14:17]
	v_mfma_i32_16x16x64_i8 v[6:9], v[200:203], v[232:235], v[6:9]
	s_barrier
	s_add_i32 s37, s37, 2
	s_cmp_gt_u32 s37, 13
	s_mov_b64 s[8:9], s[40:41]
	s_cbranch_scc0 .LBB0_2294
	s_and_b64 vcc, exec, s[26:27]
	s_cbranch_vccz .LBB0_2297
	s_barrier

; #define PG8_STAGE(bufoff, gbase, voff) do { _Pragma("unroll") for (int _i = 0; _i < 2; ++_i) \
;         __builtin_amdgcn_global_load_lds((const unsigned*)((const char*)(gbase) + (voff)[_i]), (LAS unsigned*)(lds + (bufoff) + ldsw + _i * 8192), 16, 0, 0); } while (0)
; #define PG8_LDA(dst, b, h) do { _Pragma("unroll") for (int m = 0; m < 4; ++m) dst[m] = PG8_LD32(lds + PG8_SA(b, h) + aoff + m * 2048); } while (0)
; #define PG8_LDB(dst, b, h) do { _Pragma("unroll") for (int n = 0; n < 2; ++n) dst[n] = PG8_LD32(lds + PG8_SB(b, h) + boff + n * 2048); } while (0)
; #define PG8_WAIT_V(n) asm volatile("s_waitcnt vmcnt(" #n ")" ::: "memory")
; #define PG8_WAIT_L(n) asm volatile("s_waitcnt lgkmcnt(" #n ")" ::: "memory")
; #define PG8_BAR __builtin_amdgcn_s_barrier()
; #define PG8_SCHED __builtin_amdgcn_sched_barrier(0)
; template <class Epi, class Sched, bool ALIGN_EPI, int DT>
; __device__ __forceinline__ void gemm_phase(LAS unsigned char* lds, const int KB, const Sched& S, const Epi& E) {
;     ...
;             const size_t k1 = (size_t)(t + 1) * kstep, k2 = last ? 0 : (size_t)(t + 2) * kstep, k3 = k2 + kstep;
;             const char* b2 = last ? nB : cB + (size_t)(t + 2) * kstep; const char* b3 = b2 + kstep;
;             PG8_LDB(B0, 0, 0); PG8_LDB(B1, 0, 1); PG8_SCHED; PG8_LDA(At, 0, 0); PG8_STA(PG8_SA(1, 1), false, 1, k1);
;             PG8_WAIT_V(8); PG8_WAIT_L(0); PG8_BAR; PG8_MMA(0, 0, At, B0); PG8_MMA(0, 1, At, B1); PG8_BAR; PG8_SCHED;
;             PG8_LDA(At, 0, 1); PG8_STAGE(PG8_SB(0, 0), b2, voffB); PG8_STAGE(PG8_SB(0, 1), b2 + hstep, voffB); PG8_STA(PG8_SA(0, 0), last, 0, k2);
;             PG8_WAIT_V(8); PG8_WAIT_L(0); PG8_BAR; PG8_MMA(1, 0, At, B0); PG8_MMA(1, 1, At, B1); PG8_BAR; PG8_SCHED;
;             PG8_LDB(B0, 1, 0); PG8_LDB(B1, 1, 1); PG8_SCHED; PG8_LDA(At, 1, 0); PG8_STA(PG8_SA(0, 1), last, 1, k2);
;             PG8_WAIT_V(8); PG8_WAIT_L(0); PG8_BAR; PG8_MMA(0, 0, At, B0); PG8_MMA(0, 1, At, B1); PG8_BAR; PG8_SCHED;
;             PG8_LDA(At, 1, 1); PG8_STAGE(PG8_SB(1, 0), b3, voffB); PG8_STAGE(PG8_SB(1, 1), b3 + hstep, voffB); PG8_STA(PG8_SA(1, 0), last, 0, k3);
;             PG8_WAIT_V(8); PG8_WAIT_L(0); PG8_BAR; PG8_MMA(1, 0, At, B0); PG8_MMA(1, 1, At, B1); PG8_BAR; PG8_SCHED;
;         }
.LBB0_2387:
	ds_read_b128 v[18:21], v198
	ds_read_b128 v[22:25], v198 offset:1024
	ds_read_b128 v[26:29], v198 offset:2048
	ds_read_b128 v[30:33], v198 offset:3072
	ds_read_b128 v[2:5], v199
	ds_read_b128 v[6:9], v199 offset:1024
	ds_read_b128 v[10:13], v199 offset:2048
	ds_read_b128 v[14:17], v199 offset:3072
	s_add_u32 s42, s44, 0x100
	s_addc_u32 s43, s45, 0
	s_add_i32 s76, s63, s4
	s_add_i32 m0, s33, 0xc000
	s_add_i32 s77, s33, 0xe000
	s_add_i32 s74, s76, 0x2000
	s_cmp_eq_u32 s71, 18
	v_lshl_add_u64 v[184:185], v[178:179], 0, s[44:45]
	s_cselect_b64 vcc, -1, 0
	s_cselect_b32 s75, 0, s42
	v_cndmask_b32_e32 v185, v185, v177, vcc
	v_cndmask_b32_e32 v184, v184, v176, vcc
	v_lshl_add_u64 v[226:227], v[180:181], 0, s[44:45]
	ds_read_b128 v[186:189], v200
	ds_read_b128 v[190:193], v200 offset:1024
	ds_read_b128 v[202:205], v200 offset:2048
	ds_read_b128 v[206:209], v200 offset:3072
	ds_read_b128 v[210:213], v200 offset:4096
	ds_read_b128 v[214:217], v200 offset:5120
	ds_read_b128 v[218:221], v200 offset:6144
	ds_read_b128 v[222:225], v200 offset:7168
	global_load_lds_dwordx4 v[226:227], off
	v_lshl_add_u64 v[226:227], v[182:183], 0, s[44:45]
	s_mov_b32 m0, s77
	s_nop 0
	global_load_lds_dwordx4 v[226:227], off
	s_waitcnt vmcnt(8)
	s_waitcnt lgkmcnt(0)
	s_barrier
	s_waitcnt lgkmcnt(0)
	v_mfma_scale_f32_16x16x128_f8f6f4 v[158:161], v[18:25], v[186:193], v[158:161], v1, v1 op_sel_hi:[0,0,0]
	v_mfma_scale_f32_16x16x128_f8f6f4 v[154:157], v[26:33], v[186:193], v[154:157], v1, v1 op_sel_hi:[0,0,0]
	v_mfma_scale_f32_16x16x128_f8f6f4 v[150:153], v[18:25], v[202:209], v[150:153], v1, v1 op_sel_hi:[0,0,0]
	v_mfma_scale_f32_16x16x128_f8f6f4 v[142:145], v[26:33], v[202:209], v[142:145], v1, v1 op_sel_hi:[0,0,0]
	v_mfma_scale_f32_16x16x128_f8f6f4 v[134:137], v[18:25], v[210:217], v[134:137], v1, v1 op_sel_hi:[0,0,0]
	v_mfma_scale_f32_16x16x128_f8f6f4 v[126:129], v[26:33], v[210:217], v[126:129], v1, v1 op_sel_hi:[0,0,0]
	v_mfma_scale_f32_16x16x128_f8f6f4 v[118:121], v[18:25], v[218:225], v[118:121], v1, v1 op_sel_hi:[0,0,0]
	v_mfma_scale_f32_16x16x128_f8f6f4 v[110:113], v[26:33], v[218:225], v[110:113], v1, v1 op_sel_hi:[0,0,0]
	v_mfma_scale_f32_16x16x128_f8f6f4 v[146:149], v[2:9], v[186:193], v[146:149], v1, v1 op_sel_hi:[0,0,0]
	v_mfma_scale_f32_16x16x128_f8f6f4 v[138:141], v[10:17], v[186:193], v[138:141], v1, v1 op_sel_hi:[0,0,0]
	v_mfma_scale_f32_16x16x128_f8f6f4 v[130:133], v[2:9], v[202:209], v[130:133], v1, v1 op_sel_hi:[0,0,0]
	v_mfma_scale_f32_16x16x128_f8f6f4 v[122:125], v[10:17], v[202:209], v[122:125], v1, v1 op_sel_hi:[0,0,0]
	v_mfma_scale_f32_16x16x128_f8f6f4 v[114:117], v[2:9], v[210:217], v[114:117], v1, v1 op_sel_hi:[0,0,0]
	v_mfma_scale_f32_16x16x128_f8f6f4 v[106:109], v[10:17], v[210:217], v[106:109], v1, v1 op_sel_hi:[0,0,0]
	v_mfma_scale_f32_16x16x128_f8f6f4 v[102:105], v[2:9], v[218:225], v[102:105], v1, v1 op_sel_hi:[0,0,0]
	v_mfma_scale_f32_16x16x128_f8f6f4 v[98:101], v[10:17], v[218:225], v[98:101], v1, v1 op_sel_hi:[0,0,0]
	s_barrier
	s_mov_b32 m0, s76
	v_lshl_add_u64 v[188:189], v[184:185], 0, v[170:171]
	ds_read_b128 v[202:205], v200 offset:16384
	ds_read_b128 v[206:209], v200 offset:17408
	ds_read_b128 v[210:213], v200 offset:18432
	ds_read_b128 v[214:217], v200 offset:19456
	ds_read_b128 v[218:221], v200 offset:20480
	ds_read_b128 v[222:225], v200 offset:21504
	ds_read_b128 v[226:229], v200 offset:22528
	ds_read_b128 v[230:233], v200 offset:23552
	global_load_lds_dwordx4 v[188:189], off
	v_lshl_add_u64 v[186:187], v[184:185], 0, v[164:165]
	s_mov_b32 m0, s74
	s_cselect_b32 s45, s9, s41
	s_cselect_b32 s44, s8, s40
	v_lshl_add_u64 v[190:191], v[184:185], 0, s[12:13]
	s_add_i32 s74, s64, s4
	global_load_lds_dwordx4 v[186:187], off
	v_lshl_add_u64 v[192:193], v[190:191], 0, v[170:171]
	s_mov_b32 m0, s74
	v_lshl_add_u64 v[190:191], v[190:191], 0, v[164:165]
	global_load_lds_dwordx4 v[192:193], off
	s_add_i32 m0, s74, 0x2000
	s_add_u32 s44, s44, s75
	s_addc_u32 s45, s45, 0
	global_load_lds_dwordx4 v[190:191], off
	v_lshl_add_u64 v[190:191], s[44:45], 0, v[166:167]
	s_mov_b32 m0, s33
	v_lshl_add_u64 v[192:193], s[44:45], 0, v[168:169]
	global_load_lds_dwordx4 v[190:191], off
	s_mov_b32 m0, s39
	s_nop 0
	global_load_lds_dwordx4 v[192:193], off
	s_waitcnt vmcnt(8)
	s_waitcnt lgkmcnt(0)
	s_barrier
	s_waitcnt lgkmcnt(0)
	v_mfma_scale_f32_16x16x128_f8f6f4 v[94:97], v[18:25], v[202:209], v[94:97], v1, v1 op_sel_hi:[0,0,0]
	v_mfma_scale_f32_16x16x128_f8f6f4 v[90:93], v[26:33], v[202:209], v[90:93], v1, v1 op_sel_hi:[0,0,0]
	v_mfma_scale_f32_16x16x128_f8f6f4 v[86:89], v[18:25], v[210:217], v[86:89], v1, v1 op_sel_hi:[0,0,0]
	v_mfma_scale_f32_16x16x128_f8f6f4 v[78:81], v[26:33], v[210:217], v[78:81], v1, v1 op_sel_hi:[0,0,0]
	v_mfma_scale_f32_16x16x128_f8f6f4 v[62:65], v[18:25], v[218:225], v[62:65], v1, v1 op_sel_hi:[0,0,0]
	v_mfma_scale_f32_16x16x128_f8f6f4 v[54:57], v[26:33], v[218:225], v[54:57], v1, v1 op_sel_hi:[0,0,0]
	v_mfma_scale_f32_16x16x128_f8f6f4 v[46:49], v[18:25], v[226:233], v[46:49], v1, v1 op_sel_hi:[0,0,0]
	v_mfma_scale_f32_16x16x128_f8f6f4 v[38:41], v[26:33], v[226:233], v[38:41], v1, v1 op_sel_hi:[0,0,0]
	v_mfma_scale_f32_16x16x128_f8f6f4 v[82:85], v[2:9], v[202:209], v[82:85], v1, v1 op_sel_hi:[0,0,0]
	v_mfma_scale_f32_16x16x128_f8f6f4 v[74:77], v[10:17], v[202:209], v[74:77], v1, v1 op_sel_hi:[0,0,0]
	v_mfma_scale_f32_16x16x128_f8f6f4 v[58:61], v[2:9], v[210:217], v[58:61], v1, v1 op_sel_hi:[0,0,0]
	v_mfma_scale_f32_16x16x128_f8f6f4 v[50:53], v[10:17], v[210:217], v[50:53], v1, v1 op_sel_hi:[0,0,0]
	v_mfma_scale_f32_16x16x128_f8f6f4 v[42:45], v[2:9], v[218:225], v[42:45], v1, v1 op_sel_hi:[0,0,0]
	v_mfma_scale_f32_16x16x128_f8f6f4 v[34:37], v[10:17], v[218:225], v[34:37], v1, v1 op_sel_hi:[0,0,0]
	v_mfma_scale_f32_16x16x128_f8f6f4 v[70:73], v[2:9], v[226:233], v[70:73], v1, v1 op_sel_hi:[0,0,0]
	v_mfma_scale_f32_16x16x128_f8f6f4 v[66:69], v[10:17], v[226:233], v[66:69], v1, v1 op_sel_hi:[0,0,0]
	s_barrier
; #define PG8_STAGE(bufoff, gbase, voff) do { _Pragma("unroll") for (int _i = 0; _i < 2; ++_i) \
;         __builtin_amdgcn_global_load_lds((const unsigned*)((const char*)(gbase) + (voff)[_i]), (LAS unsigned*)(lds + (bufoff) + ldsw + _i * 8192), 16, 0, 0); } while (0)
; #define PG8_LDA(dst, b, h) do { _Pragma("unroll") for (int m = 0; m < 4; ++m) dst[m] = PG8_LD32(lds + PG8_SA(b, h) + aoff + m * 2048); } while (0)
; #define PG8_LDB(dst, b, h) do { _Pragma("unroll") for (int n = 0; n < 2; ++n) dst[n] = PG8_LD32(lds + PG8_SB(b, h) + boff + n * 2048); } while (0)
; #define PG8_WAIT_V(n) asm volatile("s_waitcnt vmcnt(" #n ")" ::: "memory")
; #define PG8_WAIT_L(n) asm volatile("s_waitcnt lgkmcnt(" #n ")" ::: "memory")
; #define PG8_BAR __builtin_amdgcn_s_barrier()
; #define PG8_SCHED __builtin_amdgcn_sched_barrier(0)
; template <class Epi, class Sched, bool ALIGN_EPI, int DT>
; __device__ __forceinline__ void gemm_phase(LAS unsigned char* lds, const int KB, const Sched& S, const Epi& E) {
;     ...
;             const size_t k1 = (size_t)(t + 1) * kstep, k2 = last ? 0 : (size_t)(t + 2) * kstep, k3 = k2 + kstep;
;             const char* b2 = last ? nB : cB + (size_t)(t + 2) * kstep; const char* b3 = b2 + kstep;
;             PG8_LDB(B0, 0, 0); PG8_LDB(B1, 0, 1); PG8_SCHED; PG8_LDA(At, 0, 0); PG8_STA(PG8_SA(1, 1), false, 1, k1);
;             PG8_WAIT_V(8); PG8_WAIT_L(0); PG8_BAR; PG8_MMA(0, 0, At, B0); PG8_MMA(0, 1, At, B1); PG8_BAR; PG8_SCHED;
;             PG8_LDA(At, 0, 1); PG8_STAGE(PG8_SB(0, 0), b2, voffB); PG8_STAGE(PG8_SB(0, 1), b2 + hstep, voffB); PG8_STA(PG8_SA(0, 0), last, 0, k2);
;             PG8_WAIT_V(8); PG8_WAIT_L(0); PG8_BAR; PG8_MMA(1, 0, At, B0); PG8_MMA(1, 1, At, B1); PG8_BAR; PG8_SCHED;
;             PG8_LDB(B0, 1, 0); PG8_LDB(B1, 1, 1); PG8_SCHED; PG8_LDA(At, 1, 0); PG8_STA(PG8_SA(0, 1), last, 1, k2);
;             PG8_WAIT_V(8); PG8_WAIT_L(0); PG8_BAR; PG8_MMA(0, 0, At, B0); PG8_MMA(0, 1, At, B1); PG8_BAR; PG8_SCHED;
;             PG8_LDA(At, 1, 1); PG8_STAGE(PG8_SB(1, 0), b3, voffB); PG8_STAGE(PG8_SB(1, 1), b3 + hstep, voffB); PG8_STA(PG8_SA(1, 0), last, 0, k3);
;             PG8_WAIT_V(8); PG8_WAIT_L(0); PG8_BAR; PG8_MMA(1, 0, At, B0); PG8_MMA(1, 1, At, B1); PG8_BAR; PG8_SCHED;
;         }
	s_add_i32 s74, 0, 0x18000
	s_add_i32 s75, 0, 0x1c000
	v_add_u32_e32 v14, s74, v196
	v_add_u32_e32 v30, s75, v196
	ds_read_b128 v[2:5], v14
	ds_read_b128 v[6:9], v14 offset:1024
	ds_read_b128 v[10:13], v14 offset:2048
	ds_read_b128 v[14:17], v14 offset:3072
	ds_read_b128 v[18:21], v30
	ds_read_b128 v[22:25], v30 offset:1024
	ds_read_b128 v[26:29], v30 offset:2048
	ds_read_b128 v[30:33], v30 offset:3072
	s_add_u32 s44, s44, 0x58000
	s_addc_u32 s45, s45, 0
	s_mov_b32 m0, s46
	v_lshl_add_u64 v[234:235], s[44:45], 0, v[166:167]
	ds_read_b128 v[202:205], v200 offset:32768
	ds_read_b128 v[206:209], v200 offset:33792
	ds_read_b128 v[210:213], v200 offset:34816
	ds_read_b128 v[214:217], v200 offset:35840
	ds_read_b128 v[218:221], v200 offset:36864
	ds_read_b128 v[222:225], v200 offset:37888
	ds_read_b128 v[226:229], v200 offset:38912
	ds_read_b128 v[230:233], v200 offset:39936
	global_load_lds_dwordx4 v[234:235], off
	v_lshl_add_u64 v[234:235], s[44:45], 0, v[168:169]
	s_mov_b32 m0, s47
	s_nop 0
	global_load_lds_dwordx4 v[234:235], off
	s_waitcnt vmcnt(8)
	s_waitcnt lgkmcnt(0)
	s_barrier
	s_waitcnt lgkmcnt(0)
	v_mfma_scale_f32_16x16x128_f8f6f4 v[158:161], v[2:9], v[202:209], v[158:161], v1, v1 op_sel_hi:[0,0,0]
	v_mfma_scale_f32_16x16x128_f8f6f4 v[154:157], v[10:17], v[202:209], v[154:157], v1, v1 op_sel_hi:[0,0,0]
	v_mfma_scale_f32_16x16x128_f8f6f4 v[150:153], v[2:9], v[210:217], v[150:153], v1, v1 op_sel_hi:[0,0,0]
	v_mfma_scale_f32_16x16x128_f8f6f4 v[142:145], v[10:17], v[210:217], v[142:145], v1, v1 op_sel_hi:[0,0,0]
	v_mfma_scale_f32_16x16x128_f8f6f4 v[134:137], v[2:9], v[218:225], v[134:137], v1, v1 op_sel_hi:[0,0,0]
	v_mfma_scale_f32_16x16x128_f8f6f4 v[126:129], v[10:17], v[218:225], v[126:129], v1, v1 op_sel_hi:[0,0,0]
	v_mfma_scale_f32_16x16x128_f8f6f4 v[118:121], v[2:9], v[226:233], v[118:121], v1, v1 op_sel_hi:[0,0,0]
	v_mfma_scale_f32_16x16x128_f8f6f4 v[110:113], v[10:17], v[226:233], v[110:113], v1, v1 op_sel_hi:[0,0,0]
	v_mfma_scale_f32_16x16x128_f8f6f4 v[146:149], v[18:25], v[202:209], v[146:149], v1, v1 op_sel_hi:[0,0,0]
	v_mfma_scale_f32_16x16x128_f8f6f4 v[138:141], v[26:33], v[202:209], v[138:141], v1, v1 op_sel_hi:[0,0,0]
	v_mfma_scale_f32_16x16x128_f8f6f4 v[130:133], v[18:25], v[210:217], v[130:133], v1, v1 op_sel_hi:[0,0,0]
	v_mfma_scale_f32_16x16x128_f8f6f4 v[122:125], v[26:33], v[210:217], v[122:125], v1, v1 op_sel_hi:[0,0,0]
	v_mfma_scale_f32_16x16x128_f8f6f4 v[114:117], v[18:25], v[218:225], v[114:117], v1, v1 op_sel_hi:[0,0,0]
	v_mfma_scale_f32_16x16x128_f8f6f4 v[106:109], v[26:33], v[218:225], v[106:109], v1, v1 op_sel_hi:[0,0,0]
	v_mfma_scale_f32_16x16x128_f8f6f4 v[102:105], v[18:25], v[226:233], v[102:105], v1, v1 op_sel_hi:[0,0,0]
	v_mfma_scale_f32_16x16x128_f8f6f4 v[98:101], v[26:33], v[226:233], v[98:101], v1, v1 op_sel_hi:[0,0,0]
	s_barrier
	s_add_i32 s44, s74, s4
	v_lshl_add_u64 v[188:189], v[188:189], 0, s[16:17]
	s_mov_b32 m0, s44
	ds_read_b128 v[202:205], v200 offset:49152
	ds_read_b128 v[206:209], v200 offset:50176
	ds_read_b128 v[210:213], v200 offset:51200
	ds_read_b128 v[214:217], v200 offset:52224
	ds_read_b128 v[218:221], v200 offset:53248
	ds_read_b128 v[222:225], v200 offset:54272
	ds_read_b128 v[226:229], v200 offset:55296
	ds_read_b128 v[230:233], v200 offset:56320
	global_load_lds_dwordx4 v[188:189], off
	v_lshl_add_u64 v[186:187], v[186:187], 0, s[16:17]
	s_add_i32 m0, s44, 0x2000
	v_lshl_add_u64 v[184:185], v[184:185], 0, s[18:19]
	s_add_i32 s44, s75, s4
	global_load_lds_dwordx4 v[186:187], off
	v_lshl_add_u64 v[186:187], v[184:185], 0, v[170:171]
	s_mov_b32 m0, s44
	v_lshl_add_u64 v[184:185], v[184:185], 0, v[164:165]
	global_load_lds_dwordx4 v[186:187], off
	s_add_i32 m0, s44, 0x2000
	s_nop 0
	global_load_lds_dwordx4 v[184:185], off
	v_lshl_add_u64 v[184:185], v[190:191], 0, s[16:17]
	s_mov_b32 m0, s52
	s_nop 0
	global_load_lds_dwordx4 v[184:185], off
	v_lshl_add_u64 v[184:185], v[192:193], 0, s[16:17]
	s_mov_b32 m0, s53
	s_nop 0
	global_load_lds_dwordx4 v[184:185], off
	s_waitcnt vmcnt(8)
	s_waitcnt lgkmcnt(0)
	s_barrier
	s_waitcnt lgkmcnt(0)
	v_mfma_scale_f32_16x16x128_f8f6f4 v[94:97], v[2:9], v[202:209], v[94:97], v1, v1 op_sel_hi:[0,0,0]
	v_mfma_scale_f32_16x16x128_f8f6f4 v[90:93], v[10:17], v[202:209], v[90:93], v1, v1 op_sel_hi:[0,0,0]
	v_mfma_scale_f32_16x16x128_f8f6f4 v[86:89], v[2:9], v[210:217], v[86:89], v1, v1 op_sel_hi:[0,0,0]
	v_mfma_scale_f32_16x16x128_f8f6f4 v[78:81], v[10:17], v[210:217], v[78:81], v1, v1 op_sel_hi:[0,0,0]
	v_mfma_scale_f32_16x16x128_f8f6f4 v[62:65], v[2:9], v[218:225], v[62:65], v1, v1 op_sel_hi:[0,0,0]
	v_mfma_scale_f32_16x16x128_f8f6f4 v[54:57], v[10:17], v[218:225], v[54:57], v1, v1 op_sel_hi:[0,0,0]
	v_mfma_scale_f32_16x16x128_f8f6f4 v[46:49], v[2:9], v[226:233], v[46:49], v1, v1 op_sel_hi:[0,0,0]
	v_mfma_scale_f32_16x16x128_f8f6f4 v[38:41], v[10:17], v[226:233], v[38:41], v1, v1 op_sel_hi:[0,0,0]
	v_mfma_scale_f32_16x16x128_f8f6f4 v[82:85], v[18:25], v[202:209], v[82:85], v1, v1 op_sel_hi:[0,0,0]
	v_mfma_scale_f32_16x16x128_f8f6f4 v[74:77], v[26:33], v[202:209], v[74:77], v1, v1 op_sel_hi:[0,0,0]
	v_mfma_scale_f32_16x16x128_f8f6f4 v[58:61], v[18:25], v[210:217], v[58:61], v1, v1 op_sel_hi:[0,0,0]
	v_mfma_scale_f32_16x16x128_f8f6f4 v[50:53], v[26:33], v[210:217], v[50:53], v1, v1 op_sel_hi:[0,0,0]
	v_mfma_scale_f32_16x16x128_f8f6f4 v[42:45], v[18:25], v[218:225], v[42:45], v1, v1 op_sel_hi:[0,0,0]
	v_mfma_scale_f32_16x16x128_f8f6f4 v[34:37], v[26:33], v[218:225], v[34:37], v1, v1 op_sel_hi:[0,0,0]
	v_mfma_scale_f32_16x16x128_f8f6f4 v[70:73], v[18:25], v[226:233], v[70:73], v1, v1 op_sel_hi:[0,0,0]
	v_mfma_scale_f32_16x16x128_f8f6f4 v[66:69], v[26:33], v[226:233], v[66:69], v1, v1 op_sel_hi:[0,0,0]
	s_barrier
	s_add_i32 s71, s71, 2
	s_cmp_gt_u32 s71, 19
	s_mov_b64 s[44:45], s[42:43]
	s_cbranch_scc0 .LBB0_2387
	s_and_b64 vcc, exec, s[20:21]
	s_cbranch_vccz .LBB0_2390
	s_barrier
